# scan pass C row loop rewritten with an 8-row load ring (was one memory round trip per row); tail-fill site A only; prep2 balance
# speedup vs baseline: 1.0224x; 1.0224x over previous
; __device__ __forceinline__ unsigned pk2(float lo, float hi) { return f2bf(lo) | (f2bf(hi) << 16); }
; __device__ __forceinline__ float gelu_tanh_(float x) { const float u = 0.7978845608028654f * (x + 0.044715f * x * x * x); const float t = 1.f - 2.f / (1.f + __expf(2.f * u)); return 0.5f * x * (1.f + t); }
; __device__ __forceinline__ void phase_attn(const Args& a, const Ctx& c0, int l, bool last) {
;     ...
;         for (int r = 0; r < 32; ++r) {
;             const u32x4 wf = *(const u32x4*)(hf + (size_t)r * 4096), wb = *(const u32x4*)(hb + (size_t)r * 4096); const u32x2 gw2 = *(const u32x2*)(zg + (size_t)r * RW); const f32x4 gr = {bflo(gw2.x), bfhi(gw2.x), bflo(gw2.y), bfhi(gw2.y)};
;             const float h0 = fmaf(bflo(wf.z), cf.x, bflo(wf.x)) + fmaf(bflo(wb.z), cb.x, bflo(wb.x)), h1 = fmaf(bfhi(wf.z), cf.y, bfhi(wf.x)) + fmaf(bfhi(wb.z), cb.y, bfhi(wb.x));
;             const float h2 = fmaf(bflo(wf.w), cf.z, bflo(wf.y)) + fmaf(bflo(wb.w), cb.z, bflo(wb.y)), h3 = fmaf(bfhi(wf.w), cf.w, bfhi(wf.y)) + fmaf(bfhi(wb.w), cb.w, bfhi(wb.y));
;             u32x2 w; w.x = pk2(h0 * gelu_tanh_(gr.x), h1 * gelu_tanh_(gr.y)); w.y = pk2(h2 * gelu_tanh_(gr.z), h3 * gelu_tanh_(gr.w));
;             *(u32x2*)(yo + (size_t)r * DM) = w; }
.LBB0_1492:
	v_add_u32_e32 v20, 0x3aa00000, v14
	v_add_u32_e32 v21, 0x4400000, v20
	v_add_u32_e32 v22, 0x5fd00000, v4
	v_add_u32_e32 v23, 0x48700000, v12
	global_load_dwordx4 v[48:51], v20, s[2:3]
	global_load_dwordx4 v[52:55], v21, s[2:3]
	global_load_dwordx2 v[56:57], v22, s[2:3]
	v_add_u32_e32 v20, 0x1000, v20
	v_add_u32_e32 v21, 0x1000, v21
	v_add_u32_e32 v22, 0x800, v22
	global_load_dwordx4 v[60:63], v20, s[2:3]
	global_load_dwordx4 v[64:67], v21, s[2:3]
	global_load_dwordx2 v[68:69], v22, s[2:3]
	v_add_u32_e32 v20, 0x1000, v20
	v_add_u32_e32 v21, 0x1000, v21
	v_add_u32_e32 v22, 0x800, v22
	global_load_dwordx4 v[72:75], v20, s[2:3]
	global_load_dwordx4 v[76:79], v21, s[2:3]
	global_load_dwordx2 v[80:81], v22, s[2:3]
	v_add_u32_e32 v20, 0x1000, v20
	v_add_u32_e32 v21, 0x1000, v21
	v_add_u32_e32 v22, 0x800, v22
	global_load_dwordx4 v[84:87], v20, s[2:3]
	global_load_dwordx4 v[88:91], v21, s[2:3]
	global_load_dwordx2 v[92:93], v22, s[2:3]
	v_add_u32_e32 v20, 0x1000, v20
	v_add_u32_e32 v21, 0x1000, v21
	v_add_u32_e32 v22, 0x800, v22
	global_load_dwordx4 v[96:99], v20, s[2:3]
	global_load_dwordx4 v[100:103], v21, s[2:3]
	global_load_dwordx2 v[104:105], v22, s[2:3]
	v_add_u32_e32 v20, 0x1000, v20
	v_add_u32_e32 v21, 0x1000, v21
	v_add_u32_e32 v22, 0x800, v22
	global_load_dwordx4 v[108:111], v20, s[2:3]
	global_load_dwordx4 v[112:115], v21, s[2:3]
	global_load_dwordx2 v[116:117], v22, s[2:3]
	v_add_u32_e32 v20, 0x1000, v20
	v_add_u32_e32 v21, 0x1000, v21
	v_add_u32_e32 v22, 0x800, v22
	global_load_dwordx4 v[120:123], v20, s[2:3]
	global_load_dwordx4 v[124:127], v21, s[2:3]
	global_load_dwordx2 v[128:129], v22, s[2:3]
	v_add_u32_e32 v20, 0x1000, v20
	v_add_u32_e32 v21, 0x1000, v21
	v_add_u32_e32 v22, 0x800, v22
	global_load_dwordx4 v[132:135], v20, s[2:3]
	global_load_dwordx4 v[136:139], v21, s[2:3]
	global_load_dwordx2 v[140:141], v22, s[2:3]
	v_add_u32_e32 v20, 0x1000, v20
	v_add_u32_e32 v21, 0x1000, v21
	v_add_u32_e32 v22, 0x800, v22
	s_waitcnt vmcnt(21)
	v_lshlrev_b32_e32 v24, 16, v48
	v_and_b32_e32 v25, 0xffff0000, v48
	v_lshlrev_b32_e32 v26, 16, v49
	v_and_b32_e32 v27, 0xffff0000, v49
	v_lshlrev_b32_e32 v28, 16, v50
	v_and_b32_e32 v29, 0xffff0000, v50
	v_lshlrev_b32_e32 v30, 16, v51
	v_and_b32_e32 v31, 0xffff0000, v51
	v_lshlrev_b32_e32 v32, 16, v52
	v_and_b32_e32 v33, 0xffff0000, v52
	v_lshlrev_b32_e32 v34, 16, v53
	v_and_b32_e32 v35, 0xffff0000, v53
	v_lshlrev_b32_e32 v36, 16, v54
	v_and_b32_e32 v37, 0xffff0000, v54
	v_lshlrev_b32_e32 v38, 16, v55
	v_and_b32_e32 v39, 0xffff0000, v55
	v_fma_f32 v24, v28, v2, v24
	v_fma_f32 v25, v29, v16, v25
	v_fma_f32 v26, v30, v3, v26
	v_fma_f32 v27, v31, v17, v27
	v_fma_f32 v32, v36, v6, v32
	v_fma_f32 v33, v37, v18, v33
	v_fma_f32 v34, v38, v7, v34
	v_fma_f32 v35, v39, v19, v35
	v_add_f32_e32 v24, v24, v32
	v_add_f32_e32 v25, v25, v33
	v_add_f32_e32 v26, v26, v34
	v_add_f32_e32 v27, v27, v35
	v_lshlrev_b32_e32 v40, 16, v56
	v_and_b32_e32 v41, 0xffff0000, v56
	v_lshlrev_b32_e32 v42, 16, v57
	v_and_b32_e32 v43, 0xffff0000, v57
	global_load_dwordx4 v[48:51], v20, s[2:3]
	global_load_dwordx4 v[52:55], v21, s[2:3]
	global_load_dwordx2 v[56:57], v22, s[2:3]
	v_add_u32_e32 v20, 0x1000, v20
	v_add_u32_e32 v21, 0x1000, v21
	v_add_u32_e32 v22, 0x800, v22
	v_mul_f32_e32 v32, 0x3d372713, v40
	v_mul_f32_e32 v33, 0x3d372713, v41
	v_mul_f32_e32 v34, 0x3d372713, v42
	v_mul_f32_e32 v35, 0x3d372713, v43
	v_mul_f32_e32 v32, v32, v40
	v_mul_f32_e32 v33, v33, v41
	v_mul_f32_e32 v34, v34, v42
	v_mul_f32_e32 v35, v35, v43
	v_mov_b32_e32 v36, v40
	v_mov_b32_e32 v37, v41
	v_mov_b32_e32 v38, v42
	v_mov_b32_e32 v39, v43
	v_fmac_f32_e32 v36, v32, v36
	v_fmac_f32_e32 v37, v33, v37
	v_fmac_f32_e32 v38, v34, v38
	v_fmac_f32_e32 v39, v35, v39
	v_mul_f32_e32 v36, 0x3f4c422a, v36
	v_mul_f32_e32 v37, 0x3f4c422a, v37
	v_mul_f32_e32 v38, 0x3f4c422a, v38
	v_mul_f32_e32 v39, 0x3f4c422a, v39
	v_add_f32_e32 v36, v36, v36
	v_add_f32_e32 v37, v37, v37
	v_add_f32_e32 v38, v38, v38
	v_add_f32_e32 v39, v39, v39
	v_mul_f32_e32 v36, 0x3fb8aa3b, v36
	v_mul_f32_e32 v37, 0x3fb8aa3b, v37
	v_mul_f32_e32 v38, 0x3fb8aa3b, v38
	v_mul_f32_e32 v39, 0x3fb8aa3b, v39
	v_exp_f32_e32 v36, v36
	v_exp_f32_e32 v37, v37
	v_exp_f32_e32 v38, v38
	v_exp_f32_e32 v39, v39
	v_add_f32_e32 v36, 1.0, v36
	v_add_f32_e32 v37, 1.0, v37
	v_add_f32_e32 v38, 1.0, v38
	v_add_f32_e32 v39, 1.0, v39
	v_div_scale_f32 v44, s[6:7], v36, v36, 2.0
	v_rcp_f32_e32 v46, v44
	v_div_scale_f32 v45, vcc, 2.0, v36, 2.0
	v_fma_f32 v32, -v44, v46, 1.0
	v_fmac_f32_e32 v46, v32, v46
	v_mul_f32_e32 v47, v45, v46
	v_fma_f32 v32, -v44, v47, v45
	v_fmac_f32_e32 v47, v32, v46
	v_fma_f32 v44, -v44, v47, v45
	v_div_fmas_f32 v44, v44, v46, v47
	v_div_fixup_f32 v36, v44, v36, 2.0
	v_div_scale_f32 v44, s[6:7], v37, v37, 2.0
	v_rcp_f32_e32 v46, v44
	v_div_scale_f32 v45, vcc, 2.0, v37, 2.0
	v_fma_f32 v33, -v44, v46, 1.0
	v_fmac_f32_e32 v46, v33, v46
	v_mul_f32_e32 v47, v45, v46
	v_fma_f32 v33, -v44, v47, v45
	v_fmac_f32_e32 v47, v33, v46
	v_fma_f32 v44, -v44, v47, v45
	v_div_fmas_f32 v44, v44, v46, v47
	v_div_fixup_f32 v37, v44, v37, 2.0
	v_div_scale_f32 v44, s[6:7], v38, v38, 2.0
	v_rcp_f32_e32 v46, v44
	v_div_scale_f32 v45, vcc, 2.0, v38, 2.0
	v_fma_f32 v34, -v44, v46, 1.0
	v_fmac_f32_e32 v46, v34, v46
	v_mul_f32_e32 v47, v45, v46
	v_fma_f32 v34, -v44, v47, v45
	v_fmac_f32_e32 v47, v34, v46
	v_fma_f32 v44, -v44, v47, v45
	v_div_fmas_f32 v44, v44, v46, v47
	v_div_fixup_f32 v38, v44, v38, 2.0
	v_div_scale_f32 v44, s[6:7], v39, v39, 2.0
	v_rcp_f32_e32 v46, v44
	v_div_scale_f32 v45, vcc, 2.0, v39, 2.0
	v_fma_f32 v35, -v44, v46, 1.0
	v_fmac_f32_e32 v46, v35, v46
	v_mul_f32_e32 v47, v45, v46
	v_fma_f32 v35, -v44, v47, v45
	v_fmac_f32_e32 v47, v35, v46
	v_fma_f32 v44, -v44, v47, v45
	v_div_fmas_f32 v44, v44, v46, v47
	v_div_fixup_f32 v39, v44, v39, 2.0
	v_sub_f32_e32 v36, 1.0, v36
	v_sub_f32_e32 v37, 1.0, v37
	v_sub_f32_e32 v38, 1.0, v38
	v_sub_f32_e32 v39, 1.0, v39
	v_add_f32_e32 v36, 1.0, v36
	v_add_f32_e32 v37, 1.0, v37
	v_add_f32_e32 v38, 1.0, v38
	v_add_f32_e32 v39, 1.0, v39
	v_mul_f32_e32 v40, 0.5, v40
	v_mul_f32_e32 v41, 0.5, v41
	v_mul_f32_e32 v42, 0.5, v42
	v_mul_f32_e32 v43, 0.5, v43
	v_mul_f32_e32 v36, v40, v36
	v_mul_f32_e32 v37, v41, v37
	v_mul_f32_e32 v38, v42, v38
	v_mul_f32_e32 v39, v43, v39
	v_mul_f32_e32 v24, v24, v36
	v_mul_f32_e32 v25, v25, v37
	v_mul_f32_e32 v26, v26, v38
	v_mul_f32_e32 v27, v27, v39
	v_cvt_pk_bf16_f32 v28, v24, v25
	v_cvt_pk_bf16_f32 v29, v26, v27
	global_store_dwordx2 v23, v[28:29], s[2:3]
	v_add_u32_e32 v23, 0x1000, v23
	s_waitcnt vmcnt(22)
; __device__ __forceinline__ unsigned pk2(float lo, float hi) { return f2bf(lo) | (f2bf(hi) << 16); }
; __device__ __forceinline__ float gelu_tanh_(float x) { const float u = 0.7978845608028654f * (x + 0.044715f * x * x * x); const float t = 1.f - 2.f / (1.f + __expf(2.f * u)); return 0.5f * x * (1.f + t); }
; __device__ __forceinline__ void phase_attn(const Args& a, const Ctx& c0, int l, bool last) {
;     ...
;         for (int r = 0; r < 32; ++r) {
;             const u32x4 wf = *(const u32x4*)(hf + (size_t)r * 4096), wb = *(const u32x4*)(hb + (size_t)r * 4096); const u32x2 gw2 = *(const u32x2*)(zg + (size_t)r * RW); const f32x4 gr = {bflo(gw2.x), bfhi(gw2.x), bflo(gw2.y), bfhi(gw2.y)};
;             const float h0 = fmaf(bflo(wf.z), cf.x, bflo(wf.x)) + fmaf(bflo(wb.z), cb.x, bflo(wb.x)), h1 = fmaf(bfhi(wf.z), cf.y, bfhi(wf.x)) + fmaf(bfhi(wb.z), cb.y, bfhi(wb.x));
;             const float h2 = fmaf(bflo(wf.w), cf.z, bflo(wf.y)) + fmaf(bflo(wb.w), cb.z, bflo(wb.y)), h3 = fmaf(bfhi(wf.w), cf.w, bfhi(wf.y)) + fmaf(bfhi(wb.w), cb.w, bfhi(wb.y));
;             u32x2 w; w.x = pk2(h0 * gelu_tanh_(gr.x), h1 * gelu_tanh_(gr.y)); w.y = pk2(h2 * gelu_tanh_(gr.z), h3 * gelu_tanh_(gr.w));
;             *(u32x2*)(yo + (size_t)r * DM) = w; }
	v_lshlrev_b32_e32 v24, 16, v60
	v_and_b32_e32 v25, 0xffff0000, v60
	v_lshlrev_b32_e32 v26, 16, v61
	v_and_b32_e32 v27, 0xffff0000, v61
	v_lshlrev_b32_e32 v28, 16, v62
	v_and_b32_e32 v29, 0xffff0000, v62
	v_lshlrev_b32_e32 v30, 16, v63
	v_and_b32_e32 v31, 0xffff0000, v63
	v_lshlrev_b32_e32 v32, 16, v64
	v_and_b32_e32 v33, 0xffff0000, v64
	v_lshlrev_b32_e32 v34, 16, v65
	v_and_b32_e32 v35, 0xffff0000, v65
	v_lshlrev_b32_e32 v36, 16, v66
	v_and_b32_e32 v37, 0xffff0000, v66
	v_lshlrev_b32_e32 v38, 16, v67
	v_and_b32_e32 v39, 0xffff0000, v67
	v_fma_f32 v24, v28, v2, v24
	v_fma_f32 v25, v29, v16, v25
	v_fma_f32 v26, v30, v3, v26
	v_fma_f32 v27, v31, v17, v27
	v_fma_f32 v32, v36, v6, v32
	v_fma_f32 v33, v37, v18, v33
	v_fma_f32 v34, v38, v7, v34
	v_fma_f32 v35, v39, v19, v35
	v_add_f32_e32 v24, v24, v32
	v_add_f32_e32 v25, v25, v33
	v_add_f32_e32 v26, v26, v34
	v_add_f32_e32 v27, v27, v35
	v_lshlrev_b32_e32 v40, 16, v68
	v_and_b32_e32 v41, 0xffff0000, v68
	v_lshlrev_b32_e32 v42, 16, v69
	v_and_b32_e32 v43, 0xffff0000, v69
	global_load_dwordx4 v[60:63], v20, s[2:3]
	global_load_dwordx4 v[64:67], v21, s[2:3]
	global_load_dwordx2 v[68:69], v22, s[2:3]
	v_add_u32_e32 v20, 0x1000, v20
	v_add_u32_e32 v21, 0x1000, v21
	v_add_u32_e32 v22, 0x800, v22
	v_mul_f32_e32 v32, 0x3d372713, v40
	v_mul_f32_e32 v33, 0x3d372713, v41
	v_mul_f32_e32 v34, 0x3d372713, v42
	v_mul_f32_e32 v35, 0x3d372713, v43
	v_mul_f32_e32 v32, v32, v40
	v_mul_f32_e32 v33, v33, v41
	v_mul_f32_e32 v34, v34, v42
	v_mul_f32_e32 v35, v35, v43
	v_mov_b32_e32 v36, v40
	v_mov_b32_e32 v37, v41
	v_mov_b32_e32 v38, v42
	v_mov_b32_e32 v39, v43
	v_fmac_f32_e32 v36, v32, v36
	v_fmac_f32_e32 v37, v33, v37
	v_fmac_f32_e32 v38, v34, v38
	v_fmac_f32_e32 v39, v35, v39
	v_mul_f32_e32 v36, 0x3f4c422a, v36
	v_mul_f32_e32 v37, 0x3f4c422a, v37
	v_mul_f32_e32 v38, 0x3f4c422a, v38
	v_mul_f32_e32 v39, 0x3f4c422a, v39
	v_add_f32_e32 v36, v36, v36
	v_add_f32_e32 v37, v37, v37
	v_add_f32_e32 v38, v38, v38
	v_add_f32_e32 v39, v39, v39
	v_mul_f32_e32 v36, 0x3fb8aa3b, v36
	v_mul_f32_e32 v37, 0x3fb8aa3b, v37
	v_mul_f32_e32 v38, 0x3fb8aa3b, v38
	v_mul_f32_e32 v39, 0x3fb8aa3b, v39
	v_exp_f32_e32 v36, v36
	v_exp_f32_e32 v37, v37
	v_exp_f32_e32 v38, v38
	v_exp_f32_e32 v39, v39
	v_add_f32_e32 v36, 1.0, v36
	v_add_f32_e32 v37, 1.0, v37
	v_add_f32_e32 v38, 1.0, v38
	v_add_f32_e32 v39, 1.0, v39
	v_div_scale_f32 v44, s[6:7], v36, v36, 2.0
	v_rcp_f32_e32 v46, v44
	v_div_scale_f32 v45, vcc, 2.0, v36, 2.0
	v_fma_f32 v32, -v44, v46, 1.0
	v_fmac_f32_e32 v46, v32, v46
	v_mul_f32_e32 v47, v45, v46
	v_fma_f32 v32, -v44, v47, v45
	v_fmac_f32_e32 v47, v32, v46
	v_fma_f32 v44, -v44, v47, v45
	v_div_fmas_f32 v44, v44, v46, v47
	v_div_fixup_f32 v36, v44, v36, 2.0
	v_div_scale_f32 v44, s[6:7], v37, v37, 2.0
	v_rcp_f32_e32 v46, v44
	v_div_scale_f32 v45, vcc, 2.0, v37, 2.0
	v_fma_f32 v33, -v44, v46, 1.0
	v_fmac_f32_e32 v46, v33, v46
	v_mul_f32_e32 v47, v45, v46
	v_fma_f32 v33, -v44, v47, v45
	v_fmac_f32_e32 v47, v33, v46
	v_fma_f32 v44, -v44, v47, v45
	v_div_fmas_f32 v44, v44, v46, v47
	v_div_fixup_f32 v37, v44, v37, 2.0
	v_div_scale_f32 v44, s[6:7], v38, v38, 2.0
	v_rcp_f32_e32 v46, v44
	v_div_scale_f32 v45, vcc, 2.0, v38, 2.0
	v_fma_f32 v34, -v44, v46, 1.0
	v_fmac_f32_e32 v46, v34, v46
	v_mul_f32_e32 v47, v45, v46
	v_fma_f32 v34, -v44, v47, v45
	v_fmac_f32_e32 v47, v34, v46
	v_fma_f32 v44, -v44, v47, v45
	v_div_fmas_f32 v44, v44, v46, v47
	v_div_fixup_f32 v38, v44, v38, 2.0
	v_div_scale_f32 v44, s[6:7], v39, v39, 2.0
	v_rcp_f32_e32 v46, v44
	v_div_scale_f32 v45, vcc, 2.0, v39, 2.0
	v_fma_f32 v35, -v44, v46, 1.0
	v_fmac_f32_e32 v46, v35, v46
	v_mul_f32_e32 v47, v45, v46
	v_fma_f32 v35, -v44, v47, v45
	v_fmac_f32_e32 v47, v35, v46
	v_fma_f32 v44, -v44, v47, v45
	v_div_fmas_f32 v44, v44, v46, v47
	v_div_fixup_f32 v39, v44, v39, 2.0
	v_sub_f32_e32 v36, 1.0, v36
	v_sub_f32_e32 v37, 1.0, v37
	v_sub_f32_e32 v38, 1.0, v38
	v_sub_f32_e32 v39, 1.0, v39
	v_add_f32_e32 v36, 1.0, v36
	v_add_f32_e32 v37, 1.0, v37
	v_add_f32_e32 v38, 1.0, v38
	v_add_f32_e32 v39, 1.0, v39
	v_mul_f32_e32 v40, 0.5, v40
	v_mul_f32_e32 v41, 0.5, v41
	v_mul_f32_e32 v42, 0.5, v42
	v_mul_f32_e32 v43, 0.5, v43
	v_mul_f32_e32 v36, v40, v36
	v_mul_f32_e32 v37, v41, v37
	v_mul_f32_e32 v38, v42, v38
	v_mul_f32_e32 v39, v43, v39
	v_mul_f32_e32 v24, v24, v36
	v_mul_f32_e32 v25, v25, v37
	v_mul_f32_e32 v26, v26, v38
	v_mul_f32_e32 v27, v27, v39
	v_cvt_pk_bf16_f32 v28, v24, v25
	v_cvt_pk_bf16_f32 v29, v26, v27
	global_store_dwordx2 v23, v[28:29], s[2:3]
	v_add_u32_e32 v23, 0x1000, v23
	s_waitcnt vmcnt(23)
; __device__ __forceinline__ unsigned pk2(float lo, float hi) { return f2bf(lo) | (f2bf(hi) << 16); }
; __device__ __forceinline__ float gelu_tanh_(float x) { const float u = 0.7978845608028654f * (x + 0.044715f * x * x * x); const float t = 1.f - 2.f / (1.f + __expf(2.f * u)); return 0.5f * x * (1.f + t); }
; __device__ __forceinline__ void phase_attn(const Args& a, const Ctx& c0, int l, bool last) {
;     ...
;         for (int r = 0; r < 32; ++r) {
;             const u32x4 wf = *(const u32x4*)(hf + (size_t)r * 4096), wb = *(const u32x4*)(hb + (size_t)r * 4096); const u32x2 gw2 = *(const u32x2*)(zg + (size_t)r * RW); const f32x4 gr = {bflo(gw2.x), bfhi(gw2.x), bflo(gw2.y), bfhi(gw2.y)};
;             const float h0 = fmaf(bflo(wf.z), cf.x, bflo(wf.x)) + fmaf(bflo(wb.z), cb.x, bflo(wb.x)), h1 = fmaf(bfhi(wf.z), cf.y, bfhi(wf.x)) + fmaf(bfhi(wb.z), cb.y, bfhi(wb.x));
;             const float h2 = fmaf(bflo(wf.w), cf.z, bflo(wf.y)) + fmaf(bflo(wb.w), cb.z, bflo(wb.y)), h3 = fmaf(bfhi(wf.w), cf.w, bfhi(wf.y)) + fmaf(bfhi(wb.w), cb.w, bfhi(wb.y));
;             u32x2 w; w.x = pk2(h0 * gelu_tanh_(gr.x), h1 * gelu_tanh_(gr.y)); w.y = pk2(h2 * gelu_tanh_(gr.z), h3 * gelu_tanh_(gr.w));
;             *(u32x2*)(yo + (size_t)r * DM) = w; }
	v_lshlrev_b32_e32 v24, 16, v72
	v_and_b32_e32 v25, 0xffff0000, v72
	v_lshlrev_b32_e32 v26, 16, v73
	v_and_b32_e32 v27, 0xffff0000, v73
	v_lshlrev_b32_e32 v28, 16, v74
	v_and_b32_e32 v29, 0xffff0000, v74
	v_lshlrev_b32_e32 v30, 16, v75
	v_and_b32_e32 v31, 0xffff0000, v75
	v_lshlrev_b32_e32 v32, 16, v76
	v_and_b32_e32 v33, 0xffff0000, v76
	v_lshlrev_b32_e32 v34, 16, v77
	v_and_b32_e32 v35, 0xffff0000, v77
	v_lshlrev_b32_e32 v36, 16, v78
	v_and_b32_e32 v37, 0xffff0000, v78
	v_lshlrev_b32_e32 v38, 16, v79
	v_and_b32_e32 v39, 0xffff0000, v79
	v_fma_f32 v24, v28, v2, v24
	v_fma_f32 v25, v29, v16, v25
	v_fma_f32 v26, v30, v3, v26
	v_fma_f32 v27, v31, v17, v27
	v_fma_f32 v32, v36, v6, v32
	v_fma_f32 v33, v37, v18, v33
	v_fma_f32 v34, v38, v7, v34
	v_fma_f32 v35, v39, v19, v35
	v_add_f32_e32 v24, v24, v32
	v_add_f32_e32 v25, v25, v33
	v_add_f32_e32 v26, v26, v34
	v_add_f32_e32 v27, v27, v35
	v_lshlrev_b32_e32 v40, 16, v80
	v_and_b32_e32 v41, 0xffff0000, v80
	v_lshlrev_b32_e32 v42, 16, v81
	v_and_b32_e32 v43, 0xffff0000, v81
	global_load_dwordx4 v[72:75], v20, s[2:3]
	global_load_dwordx4 v[76:79], v21, s[2:3]
	global_load_dwordx2 v[80:81], v22, s[2:3]
	v_add_u32_e32 v20, 0x1000, v20
	v_add_u32_e32 v21, 0x1000, v21
	v_add_u32_e32 v22, 0x800, v22
	v_mul_f32_e32 v32, 0x3d372713, v40
	v_mul_f32_e32 v33, 0x3d372713, v41
	v_mul_f32_e32 v34, 0x3d372713, v42
	v_mul_f32_e32 v35, 0x3d372713, v43
	v_mul_f32_e32 v32, v32, v40
	v_mul_f32_e32 v33, v33, v41
	v_mul_f32_e32 v34, v34, v42
	v_mul_f32_e32 v35, v35, v43
	v_mov_b32_e32 v36, v40
	v_mov_b32_e32 v37, v41
	v_mov_b32_e32 v38, v42
	v_mov_b32_e32 v39, v43
	v_fmac_f32_e32 v36, v32, v36
	v_fmac_f32_e32 v37, v33, v37
	v_fmac_f32_e32 v38, v34, v38
	v_fmac_f32_e32 v39, v35, v39
	v_mul_f32_e32 v36, 0x3f4c422a, v36
	v_mul_f32_e32 v37, 0x3f4c422a, v37
	v_mul_f32_e32 v38, 0x3f4c422a, v38
	v_mul_f32_e32 v39, 0x3f4c422a, v39
	v_add_f32_e32 v36, v36, v36
	v_add_f32_e32 v37, v37, v37
	v_add_f32_e32 v38, v38, v38
	v_add_f32_e32 v39, v39, v39
	v_mul_f32_e32 v36, 0x3fb8aa3b, v36
	v_mul_f32_e32 v37, 0x3fb8aa3b, v37
	v_mul_f32_e32 v38, 0x3fb8aa3b, v38
	v_mul_f32_e32 v39, 0x3fb8aa3b, v39
	v_exp_f32_e32 v36, v36
	v_exp_f32_e32 v37, v37
	v_exp_f32_e32 v38, v38
	v_exp_f32_e32 v39, v39
	v_add_f32_e32 v36, 1.0, v36
	v_add_f32_e32 v37, 1.0, v37
	v_add_f32_e32 v38, 1.0, v38
	v_add_f32_e32 v39, 1.0, v39
	v_div_scale_f32 v44, s[6:7], v36, v36, 2.0
	v_rcp_f32_e32 v46, v44
	v_div_scale_f32 v45, vcc, 2.0, v36, 2.0
	v_fma_f32 v32, -v44, v46, 1.0
	v_fmac_f32_e32 v46, v32, v46
	v_mul_f32_e32 v47, v45, v46
	v_fma_f32 v32, -v44, v47, v45
	v_fmac_f32_e32 v47, v32, v46
	v_fma_f32 v44, -v44, v47, v45
	v_div_fmas_f32 v44, v44, v46, v47
	v_div_fixup_f32 v36, v44, v36, 2.0
	v_div_scale_f32 v44, s[6:7], v37, v37, 2.0
	v_rcp_f32_e32 v46, v44
	v_div_scale_f32 v45, vcc, 2.0, v37, 2.0
	v_fma_f32 v33, -v44, v46, 1.0
	v_fmac_f32_e32 v46, v33, v46
	v_mul_f32_e32 v47, v45, v46
	v_fma_f32 v33, -v44, v47, v45
	v_fmac_f32_e32 v47, v33, v46
	v_fma_f32 v44, -v44, v47, v45
	v_div_fmas_f32 v44, v44, v46, v47
	v_div_fixup_f32 v37, v44, v37, 2.0
	v_div_scale_f32 v44, s[6:7], v38, v38, 2.0
	v_rcp_f32_e32 v46, v44
	v_div_scale_f32 v45, vcc, 2.0, v38, 2.0
	v_fma_f32 v34, -v44, v46, 1.0
	v_fmac_f32_e32 v46, v34, v46
	v_mul_f32_e32 v47, v45, v46
	v_fma_f32 v34, -v44, v47, v45
	v_fmac_f32_e32 v47, v34, v46
	v_fma_f32 v44, -v44, v47, v45
	v_div_fmas_f32 v44, v44, v46, v47
	v_div_fixup_f32 v38, v44, v38, 2.0
	v_div_scale_f32 v44, s[6:7], v39, v39, 2.0
	v_rcp_f32_e32 v46, v44
	v_div_scale_f32 v45, vcc, 2.0, v39, 2.0
	v_fma_f32 v35, -v44, v46, 1.0
	v_fmac_f32_e32 v46, v35, v46
	v_mul_f32_e32 v47, v45, v46
	v_fma_f32 v35, -v44, v47, v45
	v_fmac_f32_e32 v47, v35, v46
	v_fma_f32 v44, -v44, v47, v45
	v_div_fmas_f32 v44, v44, v46, v47
	v_div_fixup_f32 v39, v44, v39, 2.0
	v_sub_f32_e32 v36, 1.0, v36
	v_sub_f32_e32 v37, 1.0, v37
	v_sub_f32_e32 v38, 1.0, v38
	v_sub_f32_e32 v39, 1.0, v39
	v_add_f32_e32 v36, 1.0, v36
	v_add_f32_e32 v37, 1.0, v37
	v_add_f32_e32 v38, 1.0, v38
	v_add_f32_e32 v39, 1.0, v39
	v_mul_f32_e32 v40, 0.5, v40
	v_mul_f32_e32 v41, 0.5, v41
	v_mul_f32_e32 v42, 0.5, v42
	v_mul_f32_e32 v43, 0.5, v43
	v_mul_f32_e32 v36, v40, v36
	v_mul_f32_e32 v37, v41, v37
	v_mul_f32_e32 v38, v42, v38
	v_mul_f32_e32 v39, v43, v39
	v_mul_f32_e32 v24, v24, v36
	v_mul_f32_e32 v25, v25, v37
	v_mul_f32_e32 v26, v26, v38
	v_mul_f32_e32 v27, v27, v39
	v_cvt_pk_bf16_f32 v28, v24, v25
	v_cvt_pk_bf16_f32 v29, v26, v27
	global_store_dwordx2 v23, v[28:29], s[2:3]
	v_add_u32_e32 v23, 0x1000, v23
	s_waitcnt vmcnt(24)
; __device__ __forceinline__ unsigned pk2(float lo, float hi) { return f2bf(lo) | (f2bf(hi) << 16); }
; __device__ __forceinline__ float gelu_tanh_(float x) { const float u = 0.7978845608028654f * (x + 0.044715f * x * x * x); const float t = 1.f - 2.f / (1.f + __expf(2.f * u)); return 0.5f * x * (1.f + t); }
; __device__ __forceinline__ void phase_attn(const Args& a, const Ctx& c0, int l, bool last) {
;     ...
;         for (int r = 0; r < 32; ++r) {
;             const u32x4 wf = *(const u32x4*)(hf + (size_t)r * 4096), wb = *(const u32x4*)(hb + (size_t)r * 4096); const u32x2 gw2 = *(const u32x2*)(zg + (size_t)r * RW); const f32x4 gr = {bflo(gw2.x), bfhi(gw2.x), bflo(gw2.y), bfhi(gw2.y)};
;             const float h0 = fmaf(bflo(wf.z), cf.x, bflo(wf.x)) + fmaf(bflo(wb.z), cb.x, bflo(wb.x)), h1 = fmaf(bfhi(wf.z), cf.y, bfhi(wf.x)) + fmaf(bfhi(wb.z), cb.y, bfhi(wb.x));
;             const float h2 = fmaf(bflo(wf.w), cf.z, bflo(wf.y)) + fmaf(bflo(wb.w), cb.z, bflo(wb.y)), h3 = fmaf(bfhi(wf.w), cf.w, bfhi(wf.y)) + fmaf(bfhi(wb.w), cb.w, bfhi(wb.y));
;             u32x2 w; w.x = pk2(h0 * gelu_tanh_(gr.x), h1 * gelu_tanh_(gr.y)); w.y = pk2(h2 * gelu_tanh_(gr.z), h3 * gelu_tanh_(gr.w));
;             *(u32x2*)(yo + (size_t)r * DM) = w; }
	v_lshlrev_b32_e32 v24, 16, v84
	v_and_b32_e32 v25, 0xffff0000, v84
	v_lshlrev_b32_e32 v26, 16, v85
	v_and_b32_e32 v27, 0xffff0000, v85
	v_lshlrev_b32_e32 v28, 16, v86
	v_and_b32_e32 v29, 0xffff0000, v86
	v_lshlrev_b32_e32 v30, 16, v87
	v_and_b32_e32 v31, 0xffff0000, v87
	v_lshlrev_b32_e32 v32, 16, v88
	v_and_b32_e32 v33, 0xffff0000, v88
	v_lshlrev_b32_e32 v34, 16, v89
	v_and_b32_e32 v35, 0xffff0000, v89
	v_lshlrev_b32_e32 v36, 16, v90
	v_and_b32_e32 v37, 0xffff0000, v90
	v_lshlrev_b32_e32 v38, 16, v91
	v_and_b32_e32 v39, 0xffff0000, v91
	v_fma_f32 v24, v28, v2, v24
	v_fma_f32 v25, v29, v16, v25
	v_fma_f32 v26, v30, v3, v26
	v_fma_f32 v27, v31, v17, v27
	v_fma_f32 v32, v36, v6, v32
	v_fma_f32 v33, v37, v18, v33
	v_fma_f32 v34, v38, v7, v34
	v_fma_f32 v35, v39, v19, v35
	v_add_f32_e32 v24, v24, v32
	v_add_f32_e32 v25, v25, v33
	v_add_f32_e32 v26, v26, v34
	v_add_f32_e32 v27, v27, v35
	v_lshlrev_b32_e32 v40, 16, v92
	v_and_b32_e32 v41, 0xffff0000, v92
	v_lshlrev_b32_e32 v42, 16, v93
	v_and_b32_e32 v43, 0xffff0000, v93
	global_load_dwordx4 v[84:87], v20, s[2:3]
	global_load_dwordx4 v[88:91], v21, s[2:3]
	global_load_dwordx2 v[92:93], v22, s[2:3]
	v_add_u32_e32 v20, 0x1000, v20
	v_add_u32_e32 v21, 0x1000, v21
	v_add_u32_e32 v22, 0x800, v22
	v_mul_f32_e32 v32, 0x3d372713, v40
	v_mul_f32_e32 v33, 0x3d372713, v41
	v_mul_f32_e32 v34, 0x3d372713, v42
	v_mul_f32_e32 v35, 0x3d372713, v43
	v_mul_f32_e32 v32, v32, v40
	v_mul_f32_e32 v33, v33, v41
	v_mul_f32_e32 v34, v34, v42
	v_mul_f32_e32 v35, v35, v43
	v_mov_b32_e32 v36, v40
	v_mov_b32_e32 v37, v41
	v_mov_b32_e32 v38, v42
	v_mov_b32_e32 v39, v43
	v_fmac_f32_e32 v36, v32, v36
	v_fmac_f32_e32 v37, v33, v37
	v_fmac_f32_e32 v38, v34, v38
	v_fmac_f32_e32 v39, v35, v39
	v_mul_f32_e32 v36, 0x3f4c422a, v36
	v_mul_f32_e32 v37, 0x3f4c422a, v37
	v_mul_f32_e32 v38, 0x3f4c422a, v38
	v_mul_f32_e32 v39, 0x3f4c422a, v39
	v_add_f32_e32 v36, v36, v36
	v_add_f32_e32 v37, v37, v37
	v_add_f32_e32 v38, v38, v38
	v_add_f32_e32 v39, v39, v39
	v_mul_f32_e32 v36, 0x3fb8aa3b, v36
	v_mul_f32_e32 v37, 0x3fb8aa3b, v37
	v_mul_f32_e32 v38, 0x3fb8aa3b, v38
	v_mul_f32_e32 v39, 0x3fb8aa3b, v39
	v_exp_f32_e32 v36, v36
	v_exp_f32_e32 v37, v37
	v_exp_f32_e32 v38, v38
	v_exp_f32_e32 v39, v39
	v_add_f32_e32 v36, 1.0, v36
	v_add_f32_e32 v37, 1.0, v37
	v_add_f32_e32 v38, 1.0, v38
	v_add_f32_e32 v39, 1.0, v39
	v_div_scale_f32 v44, s[6:7], v36, v36, 2.0
	v_rcp_f32_e32 v46, v44
	v_div_scale_f32 v45, vcc, 2.0, v36, 2.0
	v_fma_f32 v32, -v44, v46, 1.0
	v_fmac_f32_e32 v46, v32, v46
	v_mul_f32_e32 v47, v45, v46
	v_fma_f32 v32, -v44, v47, v45
	v_fmac_f32_e32 v47, v32, v46
	v_fma_f32 v44, -v44, v47, v45
	v_div_fmas_f32 v44, v44, v46, v47
	v_div_fixup_f32 v36, v44, v36, 2.0
	v_div_scale_f32 v44, s[6:7], v37, v37, 2.0
	v_rcp_f32_e32 v46, v44
	v_div_scale_f32 v45, vcc, 2.0, v37, 2.0
	v_fma_f32 v33, -v44, v46, 1.0
	v_fmac_f32_e32 v46, v33, v46
	v_mul_f32_e32 v47, v45, v46
	v_fma_f32 v33, -v44, v47, v45
	v_fmac_f32_e32 v47, v33, v46
	v_fma_f32 v44, -v44, v47, v45
	v_div_fmas_f32 v44, v44, v46, v47
	v_div_fixup_f32 v37, v44, v37, 2.0
	v_div_scale_f32 v44, s[6:7], v38, v38, 2.0
	v_rcp_f32_e32 v46, v44
	v_div_scale_f32 v45, vcc, 2.0, v38, 2.0
	v_fma_f32 v34, -v44, v46, 1.0
	v_fmac_f32_e32 v46, v34, v46
	v_mul_f32_e32 v47, v45, v46
	v_fma_f32 v34, -v44, v47, v45
	v_fmac_f32_e32 v47, v34, v46
	v_fma_f32 v44, -v44, v47, v45
	v_div_fmas_f32 v44, v44, v46, v47
	v_div_fixup_f32 v38, v44, v38, 2.0
	v_div_scale_f32 v44, s[6:7], v39, v39, 2.0
	v_rcp_f32_e32 v46, v44
	v_div_scale_f32 v45, vcc, 2.0, v39, 2.0
	v_fma_f32 v35, -v44, v46, 1.0
	v_fmac_f32_e32 v46, v35, v46
	v_mul_f32_e32 v47, v45, v46
	v_fma_f32 v35, -v44, v47, v45
	v_fmac_f32_e32 v47, v35, v46
	v_fma_f32 v44, -v44, v47, v45
	v_div_fmas_f32 v44, v44, v46, v47
	v_div_fixup_f32 v39, v44, v39, 2.0
	v_sub_f32_e32 v36, 1.0, v36
	v_sub_f32_e32 v37, 1.0, v37
	v_sub_f32_e32 v38, 1.0, v38
	v_sub_f32_e32 v39, 1.0, v39
	v_add_f32_e32 v36, 1.0, v36
	v_add_f32_e32 v37, 1.0, v37
	v_add_f32_e32 v38, 1.0, v38
	v_add_f32_e32 v39, 1.0, v39
	v_mul_f32_e32 v40, 0.5, v40
	v_mul_f32_e32 v41, 0.5, v41
	v_mul_f32_e32 v42, 0.5, v42
	v_mul_f32_e32 v43, 0.5, v43
	v_mul_f32_e32 v36, v40, v36
	v_mul_f32_e32 v37, v41, v37
	v_mul_f32_e32 v38, v42, v38
	v_mul_f32_e32 v39, v43, v39
	v_mul_f32_e32 v24, v24, v36
	v_mul_f32_e32 v25, v25, v37
	v_mul_f32_e32 v26, v26, v38
	v_mul_f32_e32 v27, v27, v39
	v_cvt_pk_bf16_f32 v28, v24, v25
	v_cvt_pk_bf16_f32 v29, v26, v27
	global_store_dwordx2 v23, v[28:29], s[2:3]
	v_add_u32_e32 v23, 0x1000, v23
	s_waitcnt vmcnt(25)
; __device__ __forceinline__ unsigned pk2(float lo, float hi) { return f2bf(lo) | (f2bf(hi) << 16); }
; __device__ __forceinline__ float gelu_tanh_(float x) { const float u = 0.7978845608028654f * (x + 0.044715f * x * x * x); const float t = 1.f - 2.f / (1.f + __expf(2.f * u)); return 0.5f * x * (1.f + t); }
; __device__ __forceinline__ void phase_attn(const Args& a, const Ctx& c0, int l, bool last) {
;     ...
;         for (int r = 0; r < 32; ++r) {
;             const u32x4 wf = *(const u32x4*)(hf + (size_t)r * 4096), wb = *(const u32x4*)(hb + (size_t)r * 4096); const u32x2 gw2 = *(const u32x2*)(zg + (size_t)r * RW); const f32x4 gr = {bflo(gw2.x), bfhi(gw2.x), bflo(gw2.y), bfhi(gw2.y)};
;             const float h0 = fmaf(bflo(wf.z), cf.x, bflo(wf.x)) + fmaf(bflo(wb.z), cb.x, bflo(wb.x)), h1 = fmaf(bfhi(wf.z), cf.y, bfhi(wf.x)) + fmaf(bfhi(wb.z), cb.y, bfhi(wb.x));
;             const float h2 = fmaf(bflo(wf.w), cf.z, bflo(wf.y)) + fmaf(bflo(wb.w), cb.z, bflo(wb.y)), h3 = fmaf(bfhi(wf.w), cf.w, bfhi(wf.y)) + fmaf(bfhi(wb.w), cb.w, bfhi(wb.y));
;             u32x2 w; w.x = pk2(h0 * gelu_tanh_(gr.x), h1 * gelu_tanh_(gr.y)); w.y = pk2(h2 * gelu_tanh_(gr.z), h3 * gelu_tanh_(gr.w));
;             *(u32x2*)(yo + (size_t)r * DM) = w; }
	v_lshlrev_b32_e32 v24, 16, v96
	v_and_b32_e32 v25, 0xffff0000, v96
	v_lshlrev_b32_e32 v26, 16, v97
	v_and_b32_e32 v27, 0xffff0000, v97
	v_lshlrev_b32_e32 v28, 16, v98
	v_and_b32_e32 v29, 0xffff0000, v98
	v_lshlrev_b32_e32 v30, 16, v99
	v_and_b32_e32 v31, 0xffff0000, v99
	v_lshlrev_b32_e32 v32, 16, v100
	v_and_b32_e32 v33, 0xffff0000, v100
	v_lshlrev_b32_e32 v34, 16, v101
	v_and_b32_e32 v35, 0xffff0000, v101
	v_lshlrev_b32_e32 v36, 16, v102
	v_and_b32_e32 v37, 0xffff0000, v102
	v_lshlrev_b32_e32 v38, 16, v103
	v_and_b32_e32 v39, 0xffff0000, v103
	v_fma_f32 v24, v28, v2, v24
	v_fma_f32 v25, v29, v16, v25
	v_fma_f32 v26, v30, v3, v26
	v_fma_f32 v27, v31, v17, v27
	v_fma_f32 v32, v36, v6, v32
	v_fma_f32 v33, v37, v18, v33
	v_fma_f32 v34, v38, v7, v34
	v_fma_f32 v35, v39, v19, v35
	v_add_f32_e32 v24, v24, v32
	v_add_f32_e32 v25, v25, v33
	v_add_f32_e32 v26, v26, v34
	v_add_f32_e32 v27, v27, v35
	v_lshlrev_b32_e32 v40, 16, v104
	v_and_b32_e32 v41, 0xffff0000, v104
	v_lshlrev_b32_e32 v42, 16, v105
	v_and_b32_e32 v43, 0xffff0000, v105
	global_load_dwordx4 v[96:99], v20, s[2:3]
	global_load_dwordx4 v[100:103], v21, s[2:3]
	global_load_dwordx2 v[104:105], v22, s[2:3]
	v_add_u32_e32 v20, 0x1000, v20
	v_add_u32_e32 v21, 0x1000, v21
	v_add_u32_e32 v22, 0x800, v22
	v_mul_f32_e32 v32, 0x3d372713, v40
	v_mul_f32_e32 v33, 0x3d372713, v41
	v_mul_f32_e32 v34, 0x3d372713, v42
	v_mul_f32_e32 v35, 0x3d372713, v43
	v_mul_f32_e32 v32, v32, v40
	v_mul_f32_e32 v33, v33, v41
	v_mul_f32_e32 v34, v34, v42
	v_mul_f32_e32 v35, v35, v43
	v_mov_b32_e32 v36, v40
	v_mov_b32_e32 v37, v41
	v_mov_b32_e32 v38, v42
	v_mov_b32_e32 v39, v43
	v_fmac_f32_e32 v36, v32, v36
	v_fmac_f32_e32 v37, v33, v37
	v_fmac_f32_e32 v38, v34, v38
	v_fmac_f32_e32 v39, v35, v39
	v_mul_f32_e32 v36, 0x3f4c422a, v36
	v_mul_f32_e32 v37, 0x3f4c422a, v37
	v_mul_f32_e32 v38, 0x3f4c422a, v38
	v_mul_f32_e32 v39, 0x3f4c422a, v39
	v_add_f32_e32 v36, v36, v36
	v_add_f32_e32 v37, v37, v37
	v_add_f32_e32 v38, v38, v38
	v_add_f32_e32 v39, v39, v39
	v_mul_f32_e32 v36, 0x3fb8aa3b, v36
	v_mul_f32_e32 v37, 0x3fb8aa3b, v37
	v_mul_f32_e32 v38, 0x3fb8aa3b, v38
	v_mul_f32_e32 v39, 0x3fb8aa3b, v39
	v_exp_f32_e32 v36, v36
	v_exp_f32_e32 v37, v37
	v_exp_f32_e32 v38, v38
	v_exp_f32_e32 v39, v39
	v_add_f32_e32 v36, 1.0, v36
	v_add_f32_e32 v37, 1.0, v37
	v_add_f32_e32 v38, 1.0, v38
	v_add_f32_e32 v39, 1.0, v39
	v_div_scale_f32 v44, s[6:7], v36, v36, 2.0
	v_rcp_f32_e32 v46, v44
	v_div_scale_f32 v45, vcc, 2.0, v36, 2.0
	v_fma_f32 v32, -v44, v46, 1.0
	v_fmac_f32_e32 v46, v32, v46
	v_mul_f32_e32 v47, v45, v46
	v_fma_f32 v32, -v44, v47, v45
	v_fmac_f32_e32 v47, v32, v46
	v_fma_f32 v44, -v44, v47, v45
	v_div_fmas_f32 v44, v44, v46, v47
	v_div_fixup_f32 v36, v44, v36, 2.0
	v_div_scale_f32 v44, s[6:7], v37, v37, 2.0
	v_rcp_f32_e32 v46, v44
	v_div_scale_f32 v45, vcc, 2.0, v37, 2.0
	v_fma_f32 v33, -v44, v46, 1.0
	v_fmac_f32_e32 v46, v33, v46
	v_mul_f32_e32 v47, v45, v46
	v_fma_f32 v33, -v44, v47, v45
	v_fmac_f32_e32 v47, v33, v46
	v_fma_f32 v44, -v44, v47, v45
	v_div_fmas_f32 v44, v44, v46, v47
	v_div_fixup_f32 v37, v44, v37, 2.0
	v_div_scale_f32 v44, s[6:7], v38, v38, 2.0
	v_rcp_f32_e32 v46, v44
	v_div_scale_f32 v45, vcc, 2.0, v38, 2.0
	v_fma_f32 v34, -v44, v46, 1.0
	v_fmac_f32_e32 v46, v34, v46
	v_mul_f32_e32 v47, v45, v46
	v_fma_f32 v34, -v44, v47, v45
	v_fmac_f32_e32 v47, v34, v46
	v_fma_f32 v44, -v44, v47, v45
	v_div_fmas_f32 v44, v44, v46, v47
	v_div_fixup_f32 v38, v44, v38, 2.0
	v_div_scale_f32 v44, s[6:7], v39, v39, 2.0
	v_rcp_f32_e32 v46, v44
	v_div_scale_f32 v45, vcc, 2.0, v39, 2.0
	v_fma_f32 v35, -v44, v46, 1.0
	v_fmac_f32_e32 v46, v35, v46
	v_mul_f32_e32 v47, v45, v46
	v_fma_f32 v35, -v44, v47, v45
	v_fmac_f32_e32 v47, v35, v46
	v_fma_f32 v44, -v44, v47, v45
	v_div_fmas_f32 v44, v44, v46, v47
	v_div_fixup_f32 v39, v44, v39, 2.0
	v_sub_f32_e32 v36, 1.0, v36
	v_sub_f32_e32 v37, 1.0, v37
	v_sub_f32_e32 v38, 1.0, v38
	v_sub_f32_e32 v39, 1.0, v39
	v_add_f32_e32 v36, 1.0, v36
	v_add_f32_e32 v37, 1.0, v37
	v_add_f32_e32 v38, 1.0, v38
	v_add_f32_e32 v39, 1.0, v39
	v_mul_f32_e32 v40, 0.5, v40
	v_mul_f32_e32 v41, 0.5, v41
	v_mul_f32_e32 v42, 0.5, v42
	v_mul_f32_e32 v43, 0.5, v43
	v_mul_f32_e32 v36, v40, v36
	v_mul_f32_e32 v37, v41, v37
	v_mul_f32_e32 v38, v42, v38
	v_mul_f32_e32 v39, v43, v39
	v_mul_f32_e32 v24, v24, v36
	v_mul_f32_e32 v25, v25, v37
	v_mul_f32_e32 v26, v26, v38
	v_mul_f32_e32 v27, v27, v39
	v_cvt_pk_bf16_f32 v28, v24, v25
	v_cvt_pk_bf16_f32 v29, v26, v27
	global_store_dwordx2 v23, v[28:29], s[2:3]
	v_add_u32_e32 v23, 0x1000, v23
	s_waitcnt vmcnt(26)
; __device__ __forceinline__ unsigned pk2(float lo, float hi) { return f2bf(lo) | (f2bf(hi) << 16); }
; __device__ __forceinline__ float gelu_tanh_(float x) { const float u = 0.7978845608028654f * (x + 0.044715f * x * x * x); const float t = 1.f - 2.f / (1.f + __expf(2.f * u)); return 0.5f * x * (1.f + t); }
; __device__ __forceinline__ void phase_attn(const Args& a, const Ctx& c0, int l, bool last) {
;     ...
;         for (int r = 0; r < 32; ++r) {
;             const u32x4 wf = *(const u32x4*)(hf + (size_t)r * 4096), wb = *(const u32x4*)(hb + (size_t)r * 4096); const u32x2 gw2 = *(const u32x2*)(zg + (size_t)r * RW); const f32x4 gr = {bflo(gw2.x), bfhi(gw2.x), bflo(gw2.y), bfhi(gw2.y)};
;             const float h0 = fmaf(bflo(wf.z), cf.x, bflo(wf.x)) + fmaf(bflo(wb.z), cb.x, bflo(wb.x)), h1 = fmaf(bfhi(wf.z), cf.y, bfhi(wf.x)) + fmaf(bfhi(wb.z), cb.y, bfhi(wb.x));
;             const float h2 = fmaf(bflo(wf.w), cf.z, bflo(wf.y)) + fmaf(bflo(wb.w), cb.z, bflo(wb.y)), h3 = fmaf(bfhi(wf.w), cf.w, bfhi(wf.y)) + fmaf(bfhi(wb.w), cb.w, bfhi(wb.y));
;             u32x2 w; w.x = pk2(h0 * gelu_tanh_(gr.x), h1 * gelu_tanh_(gr.y)); w.y = pk2(h2 * gelu_tanh_(gr.z), h3 * gelu_tanh_(gr.w));
;             *(u32x2*)(yo + (size_t)r * DM) = w; }
	v_lshlrev_b32_e32 v24, 16, v108
	v_and_b32_e32 v25, 0xffff0000, v108
	v_lshlrev_b32_e32 v26, 16, v109
	v_and_b32_e32 v27, 0xffff0000, v109
	v_lshlrev_b32_e32 v28, 16, v110
	v_and_b32_e32 v29, 0xffff0000, v110
	v_lshlrev_b32_e32 v30, 16, v111
	v_and_b32_e32 v31, 0xffff0000, v111
	v_lshlrev_b32_e32 v32, 16, v112
	v_and_b32_e32 v33, 0xffff0000, v112
	v_lshlrev_b32_e32 v34, 16, v113
	v_and_b32_e32 v35, 0xffff0000, v113
	v_lshlrev_b32_e32 v36, 16, v114
	v_and_b32_e32 v37, 0xffff0000, v114
	v_lshlrev_b32_e32 v38, 16, v115
	v_and_b32_e32 v39, 0xffff0000, v115
	v_fma_f32 v24, v28, v2, v24
	v_fma_f32 v25, v29, v16, v25
	v_fma_f32 v26, v30, v3, v26
	v_fma_f32 v27, v31, v17, v27
	v_fma_f32 v32, v36, v6, v32
	v_fma_f32 v33, v37, v18, v33
	v_fma_f32 v34, v38, v7, v34
	v_fma_f32 v35, v39, v19, v35
	v_add_f32_e32 v24, v24, v32
	v_add_f32_e32 v25, v25, v33
	v_add_f32_e32 v26, v26, v34
	v_add_f32_e32 v27, v27, v35
	v_lshlrev_b32_e32 v40, 16, v116
	v_and_b32_e32 v41, 0xffff0000, v116
	v_lshlrev_b32_e32 v42, 16, v117
	v_and_b32_e32 v43, 0xffff0000, v117
	global_load_dwordx4 v[108:111], v20, s[2:3]
	global_load_dwordx4 v[112:115], v21, s[2:3]
	global_load_dwordx2 v[116:117], v22, s[2:3]
	v_add_u32_e32 v20, 0x1000, v20
	v_add_u32_e32 v21, 0x1000, v21
	v_add_u32_e32 v22, 0x800, v22
	v_mul_f32_e32 v32, 0x3d372713, v40
	v_mul_f32_e32 v33, 0x3d372713, v41
	v_mul_f32_e32 v34, 0x3d372713, v42
	v_mul_f32_e32 v35, 0x3d372713, v43
	v_mul_f32_e32 v32, v32, v40
	v_mul_f32_e32 v33, v33, v41
	v_mul_f32_e32 v34, v34, v42
	v_mul_f32_e32 v35, v35, v43
	v_mov_b32_e32 v36, v40
	v_mov_b32_e32 v37, v41
	v_mov_b32_e32 v38, v42
	v_mov_b32_e32 v39, v43
	v_fmac_f32_e32 v36, v32, v36
	v_fmac_f32_e32 v37, v33, v37
	v_fmac_f32_e32 v38, v34, v38
	v_fmac_f32_e32 v39, v35, v39
	v_mul_f32_e32 v36, 0x3f4c422a, v36
	v_mul_f32_e32 v37, 0x3f4c422a, v37
	v_mul_f32_e32 v38, 0x3f4c422a, v38
	v_mul_f32_e32 v39, 0x3f4c422a, v39
	v_add_f32_e32 v36, v36, v36
	v_add_f32_e32 v37, v37, v37
	v_add_f32_e32 v38, v38, v38
	v_add_f32_e32 v39, v39, v39
	v_mul_f32_e32 v36, 0x3fb8aa3b, v36
	v_mul_f32_e32 v37, 0x3fb8aa3b, v37
	v_mul_f32_e32 v38, 0x3fb8aa3b, v38
	v_mul_f32_e32 v39, 0x3fb8aa3b, v39
	v_exp_f32_e32 v36, v36
	v_exp_f32_e32 v37, v37
	v_exp_f32_e32 v38, v38
	v_exp_f32_e32 v39, v39
	v_add_f32_e32 v36, 1.0, v36
	v_add_f32_e32 v37, 1.0, v37
	v_add_f32_e32 v38, 1.0, v38
	v_add_f32_e32 v39, 1.0, v39
	v_div_scale_f32 v44, s[6:7], v36, v36, 2.0
	v_rcp_f32_e32 v46, v44
	v_div_scale_f32 v45, vcc, 2.0, v36, 2.0
	v_fma_f32 v32, -v44, v46, 1.0
	v_fmac_f32_e32 v46, v32, v46
	v_mul_f32_e32 v47, v45, v46
	v_fma_f32 v32, -v44, v47, v45
	v_fmac_f32_e32 v47, v32, v46
	v_fma_f32 v44, -v44, v47, v45
	v_div_fmas_f32 v44, v44, v46, v47
	v_div_fixup_f32 v36, v44, v36, 2.0
	v_div_scale_f32 v44, s[6:7], v37, v37, 2.0
	v_rcp_f32_e32 v46, v44
	v_div_scale_f32 v45, vcc, 2.0, v37, 2.0
	v_fma_f32 v33, -v44, v46, 1.0
	v_fmac_f32_e32 v46, v33, v46
	v_mul_f32_e32 v47, v45, v46
	v_fma_f32 v33, -v44, v47, v45
	v_fmac_f32_e32 v47, v33, v46
	v_fma_f32 v44, -v44, v47, v45
	v_div_fmas_f32 v44, v44, v46, v47
	v_div_fixup_f32 v37, v44, v37, 2.0
	v_div_scale_f32 v44, s[6:7], v38, v38, 2.0
	v_rcp_f32_e32 v46, v44
	v_div_scale_f32 v45, vcc, 2.0, v38, 2.0
	v_fma_f32 v34, -v44, v46, 1.0
	v_fmac_f32_e32 v46, v34, v46
	v_mul_f32_e32 v47, v45, v46
	v_fma_f32 v34, -v44, v47, v45
	v_fmac_f32_e32 v47, v34, v46
	v_fma_f32 v44, -v44, v47, v45
	v_div_fmas_f32 v44, v44, v46, v47
	v_div_fixup_f32 v38, v44, v38, 2.0
	v_div_scale_f32 v44, s[6:7], v39, v39, 2.0
	v_rcp_f32_e32 v46, v44
	v_div_scale_f32 v45, vcc, 2.0, v39, 2.0
	v_fma_f32 v35, -v44, v46, 1.0
	v_fmac_f32_e32 v46, v35, v46
	v_mul_f32_e32 v47, v45, v46
	v_fma_f32 v35, -v44, v47, v45
	v_fmac_f32_e32 v47, v35, v46
	v_fma_f32 v44, -v44, v47, v45
	v_div_fmas_f32 v44, v44, v46, v47
	v_div_fixup_f32 v39, v44, v39, 2.0
	v_sub_f32_e32 v36, 1.0, v36
	v_sub_f32_e32 v37, 1.0, v37
	v_sub_f32_e32 v38, 1.0, v38
	v_sub_f32_e32 v39, 1.0, v39
	v_add_f32_e32 v36, 1.0, v36
	v_add_f32_e32 v37, 1.0, v37
	v_add_f32_e32 v38, 1.0, v38
	v_add_f32_e32 v39, 1.0, v39
	v_mul_f32_e32 v40, 0.5, v40
	v_mul_f32_e32 v41, 0.5, v41
	v_mul_f32_e32 v42, 0.5, v42
	v_mul_f32_e32 v43, 0.5, v43
	v_mul_f32_e32 v36, v40, v36
	v_mul_f32_e32 v37, v41, v37
	v_mul_f32_e32 v38, v42, v38
	v_mul_f32_e32 v39, v43, v39
	v_mul_f32_e32 v24, v24, v36
	v_mul_f32_e32 v25, v25, v37
	v_mul_f32_e32 v26, v26, v38
	v_mul_f32_e32 v27, v27, v39
	v_cvt_pk_bf16_f32 v28, v24, v25
	v_cvt_pk_bf16_f32 v29, v26, v27
	global_store_dwordx2 v23, v[28:29], s[2:3]
	v_add_u32_e32 v23, 0x1000, v23
	s_waitcnt vmcnt(27)
; __device__ __forceinline__ unsigned pk2(float lo, float hi) { return f2bf(lo) | (f2bf(hi) << 16); }
; __device__ __forceinline__ float gelu_tanh_(float x) { const float u = 0.7978845608028654f * (x + 0.044715f * x * x * x); const float t = 1.f - 2.f / (1.f + __expf(2.f * u)); return 0.5f * x * (1.f + t); }
; __device__ __forceinline__ void phase_attn(const Args& a, const Ctx& c0, int l, bool last) {
;     ...
;         for (int r = 0; r < 32; ++r) {
;             const u32x4 wf = *(const u32x4*)(hf + (size_t)r * 4096), wb = *(const u32x4*)(hb + (size_t)r * 4096); const u32x2 gw2 = *(const u32x2*)(zg + (size_t)r * RW); const f32x4 gr = {bflo(gw2.x), bfhi(gw2.x), bflo(gw2.y), bfhi(gw2.y)};
;             const float h0 = fmaf(bflo(wf.z), cf.x, bflo(wf.x)) + fmaf(bflo(wb.z), cb.x, bflo(wb.x)), h1 = fmaf(bfhi(wf.z), cf.y, bfhi(wf.x)) + fmaf(bfhi(wb.z), cb.y, bfhi(wb.x));
;             const float h2 = fmaf(bflo(wf.w), cf.z, bflo(wf.y)) + fmaf(bflo(wb.w), cb.z, bflo(wb.y)), h3 = fmaf(bfhi(wf.w), cf.w, bfhi(wf.y)) + fmaf(bfhi(wb.w), cb.w, bfhi(wb.y));
;             u32x2 w; w.x = pk2(h0 * gelu_tanh_(gr.x), h1 * gelu_tanh_(gr.y)); w.y = pk2(h2 * gelu_tanh_(gr.z), h3 * gelu_tanh_(gr.w));
;             *(u32x2*)(yo + (size_t)r * DM) = w; }
	v_lshlrev_b32_e32 v24, 16, v120
	v_and_b32_e32 v25, 0xffff0000, v120
	v_lshlrev_b32_e32 v26, 16, v121
	v_and_b32_e32 v27, 0xffff0000, v121
	v_lshlrev_b32_e32 v28, 16, v122
	v_and_b32_e32 v29, 0xffff0000, v122
	v_lshlrev_b32_e32 v30, 16, v123
	v_and_b32_e32 v31, 0xffff0000, v123
	v_lshlrev_b32_e32 v32, 16, v124
	v_and_b32_e32 v33, 0xffff0000, v124
	v_lshlrev_b32_e32 v34, 16, v125
	v_and_b32_e32 v35, 0xffff0000, v125
	v_lshlrev_b32_e32 v36, 16, v126
	v_and_b32_e32 v37, 0xffff0000, v126
	v_lshlrev_b32_e32 v38, 16, v127
	v_and_b32_e32 v39, 0xffff0000, v127
	v_fma_f32 v24, v28, v2, v24
	v_fma_f32 v25, v29, v16, v25
	v_fma_f32 v26, v30, v3, v26
	v_fma_f32 v27, v31, v17, v27
	v_fma_f32 v32, v36, v6, v32
	v_fma_f32 v33, v37, v18, v33
	v_fma_f32 v34, v38, v7, v34
	v_fma_f32 v35, v39, v19, v35
	v_add_f32_e32 v24, v24, v32
	v_add_f32_e32 v25, v25, v33
	v_add_f32_e32 v26, v26, v34
	v_add_f32_e32 v27, v27, v35
	v_lshlrev_b32_e32 v40, 16, v128
	v_and_b32_e32 v41, 0xffff0000, v128
	v_lshlrev_b32_e32 v42, 16, v129
	v_and_b32_e32 v43, 0xffff0000, v129
	global_load_dwordx4 v[120:123], v20, s[2:3]
	global_load_dwordx4 v[124:127], v21, s[2:3]
	global_load_dwordx2 v[128:129], v22, s[2:3]
	v_add_u32_e32 v20, 0x1000, v20
	v_add_u32_e32 v21, 0x1000, v21
	v_add_u32_e32 v22, 0x800, v22
	v_mul_f32_e32 v32, 0x3d372713, v40
	v_mul_f32_e32 v33, 0x3d372713, v41
	v_mul_f32_e32 v34, 0x3d372713, v42
	v_mul_f32_e32 v35, 0x3d372713, v43
	v_mul_f32_e32 v32, v32, v40
	v_mul_f32_e32 v33, v33, v41
	v_mul_f32_e32 v34, v34, v42
	v_mul_f32_e32 v35, v35, v43
	v_mov_b32_e32 v36, v40
	v_mov_b32_e32 v37, v41
	v_mov_b32_e32 v38, v42
	v_mov_b32_e32 v39, v43
	v_fmac_f32_e32 v36, v32, v36
	v_fmac_f32_e32 v37, v33, v37
	v_fmac_f32_e32 v38, v34, v38
	v_fmac_f32_e32 v39, v35, v39
	v_mul_f32_e32 v36, 0x3f4c422a, v36
	v_mul_f32_e32 v37, 0x3f4c422a, v37
	v_mul_f32_e32 v38, 0x3f4c422a, v38
	v_mul_f32_e32 v39, 0x3f4c422a, v39
	v_add_f32_e32 v36, v36, v36
	v_add_f32_e32 v37, v37, v37
	v_add_f32_e32 v38, v38, v38
	v_add_f32_e32 v39, v39, v39
	v_mul_f32_e32 v36, 0x3fb8aa3b, v36
	v_mul_f32_e32 v37, 0x3fb8aa3b, v37
	v_mul_f32_e32 v38, 0x3fb8aa3b, v38
	v_mul_f32_e32 v39, 0x3fb8aa3b, v39
	v_exp_f32_e32 v36, v36
	v_exp_f32_e32 v37, v37
	v_exp_f32_e32 v38, v38
	v_exp_f32_e32 v39, v39
	v_add_f32_e32 v36, 1.0, v36
	v_add_f32_e32 v37, 1.0, v37
	v_add_f32_e32 v38, 1.0, v38
	v_add_f32_e32 v39, 1.0, v39
	v_div_scale_f32 v44, s[6:7], v36, v36, 2.0
	v_rcp_f32_e32 v46, v44
	v_div_scale_f32 v45, vcc, 2.0, v36, 2.0
	v_fma_f32 v32, -v44, v46, 1.0
	v_fmac_f32_e32 v46, v32, v46
	v_mul_f32_e32 v47, v45, v46
	v_fma_f32 v32, -v44, v47, v45
	v_fmac_f32_e32 v47, v32, v46
	v_fma_f32 v44, -v44, v47, v45
	v_div_fmas_f32 v44, v44, v46, v47
	v_div_fixup_f32 v36, v44, v36, 2.0
	v_div_scale_f32 v44, s[6:7], v37, v37, 2.0
	v_rcp_f32_e32 v46, v44
	v_div_scale_f32 v45, vcc, 2.0, v37, 2.0
	v_fma_f32 v33, -v44, v46, 1.0
	v_fmac_f32_e32 v46, v33, v46
	v_mul_f32_e32 v47, v45, v46
	v_fma_f32 v33, -v44, v47, v45
	v_fmac_f32_e32 v47, v33, v46
	v_fma_f32 v44, -v44, v47, v45
	v_div_fmas_f32 v44, v44, v46, v47
	v_div_fixup_f32 v37, v44, v37, 2.0
	v_div_scale_f32 v44, s[6:7], v38, v38, 2.0
	v_rcp_f32_e32 v46, v44
	v_div_scale_f32 v45, vcc, 2.0, v38, 2.0
	v_fma_f32 v34, -v44, v46, 1.0
	v_fmac_f32_e32 v46, v34, v46
	v_mul_f32_e32 v47, v45, v46
	v_fma_f32 v34, -v44, v47, v45
	v_fmac_f32_e32 v47, v34, v46
	v_fma_f32 v44, -v44, v47, v45
	v_div_fmas_f32 v44, v44, v46, v47
	v_div_fixup_f32 v38, v44, v38, 2.0
	v_div_scale_f32 v44, s[6:7], v39, v39, 2.0
	v_rcp_f32_e32 v46, v44
	v_div_scale_f32 v45, vcc, 2.0, v39, 2.0
	v_fma_f32 v35, -v44, v46, 1.0
	v_fmac_f32_e32 v46, v35, v46
	v_mul_f32_e32 v47, v45, v46
	v_fma_f32 v35, -v44, v47, v45
	v_fmac_f32_e32 v47, v35, v46
	v_fma_f32 v44, -v44, v47, v45
	v_div_fmas_f32 v44, v44, v46, v47
	v_div_fixup_f32 v39, v44, v39, 2.0
	v_sub_f32_e32 v36, 1.0, v36
	v_sub_f32_e32 v37, 1.0, v37
	v_sub_f32_e32 v38, 1.0, v38
	v_sub_f32_e32 v39, 1.0, v39
	v_add_f32_e32 v36, 1.0, v36
	v_add_f32_e32 v37, 1.0, v37
	v_add_f32_e32 v38, 1.0, v38
	v_add_f32_e32 v39, 1.0, v39
	v_mul_f32_e32 v40, 0.5, v40
	v_mul_f32_e32 v41, 0.5, v41
	v_mul_f32_e32 v42, 0.5, v42
	v_mul_f32_e32 v43, 0.5, v43
	v_mul_f32_e32 v36, v40, v36
	v_mul_f32_e32 v37, v41, v37
	v_mul_f32_e32 v38, v42, v38
	v_mul_f32_e32 v39, v43, v39
	v_mul_f32_e32 v24, v24, v36
	v_mul_f32_e32 v25, v25, v37
	v_mul_f32_e32 v26, v26, v38
	v_mul_f32_e32 v27, v27, v39
	v_cvt_pk_bf16_f32 v28, v24, v25
	v_cvt_pk_bf16_f32 v29, v26, v27
	global_store_dwordx2 v23, v[28:29], s[2:3]
	v_add_u32_e32 v23, 0x1000, v23
	s_waitcnt vmcnt(28)
; __device__ __forceinline__ unsigned pk2(float lo, float hi) { return f2bf(lo) | (f2bf(hi) << 16); }
; __device__ __forceinline__ float gelu_tanh_(float x) { const float u = 0.7978845608028654f * (x + 0.044715f * x * x * x); const float t = 1.f - 2.f / (1.f + __expf(2.f * u)); return 0.5f * x * (1.f + t); }
; __device__ __forceinline__ void phase_attn(const Args& a, const Ctx& c0, int l, bool last) {
;     ...
;         for (int r = 0; r < 32; ++r) {
;             const u32x4 wf = *(const u32x4*)(hf + (size_t)r * 4096), wb = *(const u32x4*)(hb + (size_t)r * 4096); const u32x2 gw2 = *(const u32x2*)(zg + (size_t)r * RW); const f32x4 gr = {bflo(gw2.x), bfhi(gw2.x), bflo(gw2.y), bfhi(gw2.y)};
;             const float h0 = fmaf(bflo(wf.z), cf.x, bflo(wf.x)) + fmaf(bflo(wb.z), cb.x, bflo(wb.x)), h1 = fmaf(bfhi(wf.z), cf.y, bfhi(wf.x)) + fmaf(bfhi(wb.z), cb.y, bfhi(wb.x));
;             const float h2 = fmaf(bflo(wf.w), cf.z, bflo(wf.y)) + fmaf(bflo(wb.w), cb.z, bflo(wb.y)), h3 = fmaf(bfhi(wf.w), cf.w, bfhi(wf.y)) + fmaf(bfhi(wb.w), cb.w, bfhi(wb.y));
;             u32x2 w; w.x = pk2(h0 * gelu_tanh_(gr.x), h1 * gelu_tanh_(gr.y)); w.y = pk2(h2 * gelu_tanh_(gr.z), h3 * gelu_tanh_(gr.w));
;             *(u32x2*)(yo + (size_t)r * DM) = w; }
	v_lshlrev_b32_e32 v24, 16, v132
	v_and_b32_e32 v25, 0xffff0000, v132
	v_lshlrev_b32_e32 v26, 16, v133
	v_and_b32_e32 v27, 0xffff0000, v133
	v_lshlrev_b32_e32 v28, 16, v134
	v_and_b32_e32 v29, 0xffff0000, v134
	v_lshlrev_b32_e32 v30, 16, v135
	v_and_b32_e32 v31, 0xffff0000, v135
	v_lshlrev_b32_e32 v32, 16, v136
	v_and_b32_e32 v33, 0xffff0000, v136
	v_lshlrev_b32_e32 v34, 16, v137
	v_and_b32_e32 v35, 0xffff0000, v137
	v_lshlrev_b32_e32 v36, 16, v138
	v_and_b32_e32 v37, 0xffff0000, v138
	v_lshlrev_b32_e32 v38, 16, v139
	v_and_b32_e32 v39, 0xffff0000, v139
	v_fma_f32 v24, v28, v2, v24
	v_fma_f32 v25, v29, v16, v25
	v_fma_f32 v26, v30, v3, v26
	v_fma_f32 v27, v31, v17, v27
	v_fma_f32 v32, v36, v6, v32
	v_fma_f32 v33, v37, v18, v33
	v_fma_f32 v34, v38, v7, v34
	v_fma_f32 v35, v39, v19, v35
	v_add_f32_e32 v24, v24, v32
	v_add_f32_e32 v25, v25, v33
	v_add_f32_e32 v26, v26, v34
	v_add_f32_e32 v27, v27, v35
	v_lshlrev_b32_e32 v40, 16, v140
	v_and_b32_e32 v41, 0xffff0000, v140
	v_lshlrev_b32_e32 v42, 16, v141
	v_and_b32_e32 v43, 0xffff0000, v141
	global_load_dwordx4 v[132:135], v20, s[2:3]
	global_load_dwordx4 v[136:139], v21, s[2:3]
	global_load_dwordx2 v[140:141], v22, s[2:3]
	v_add_u32_e32 v20, 0x1000, v20
	v_add_u32_e32 v21, 0x1000, v21
	v_add_u32_e32 v22, 0x800, v22
	v_mul_f32_e32 v32, 0x3d372713, v40
	v_mul_f32_e32 v33, 0x3d372713, v41
	v_mul_f32_e32 v34, 0x3d372713, v42
	v_mul_f32_e32 v35, 0x3d372713, v43
	v_mul_f32_e32 v32, v32, v40
	v_mul_f32_e32 v33, v33, v41
	v_mul_f32_e32 v34, v34, v42
	v_mul_f32_e32 v35, v35, v43
	v_mov_b32_e32 v36, v40
	v_mov_b32_e32 v37, v41
	v_mov_b32_e32 v38, v42
	v_mov_b32_e32 v39, v43
	v_fmac_f32_e32 v36, v32, v36
	v_fmac_f32_e32 v37, v33, v37
	v_fmac_f32_e32 v38, v34, v38
	v_fmac_f32_e32 v39, v35, v39
	v_mul_f32_e32 v36, 0x3f4c422a, v36
	v_mul_f32_e32 v37, 0x3f4c422a, v37
	v_mul_f32_e32 v38, 0x3f4c422a, v38
	v_mul_f32_e32 v39, 0x3f4c422a, v39
	v_add_f32_e32 v36, v36, v36
	v_add_f32_e32 v37, v37, v37
	v_add_f32_e32 v38, v38, v38
	v_add_f32_e32 v39, v39, v39
	v_mul_f32_e32 v36, 0x3fb8aa3b, v36
	v_mul_f32_e32 v37, 0x3fb8aa3b, v37
	v_mul_f32_e32 v38, 0x3fb8aa3b, v38
	v_mul_f32_e32 v39, 0x3fb8aa3b, v39
	v_exp_f32_e32 v36, v36
	v_exp_f32_e32 v37, v37
	v_exp_f32_e32 v38, v38
	v_exp_f32_e32 v39, v39
	v_add_f32_e32 v36, 1.0, v36
	v_add_f32_e32 v37, 1.0, v37
	v_add_f32_e32 v38, 1.0, v38
	v_add_f32_e32 v39, 1.0, v39
	v_div_scale_f32 v44, s[6:7], v36, v36, 2.0
	v_rcp_f32_e32 v46, v44
	v_div_scale_f32 v45, vcc, 2.0, v36, 2.0
	v_fma_f32 v32, -v44, v46, 1.0
	v_fmac_f32_e32 v46, v32, v46
	v_mul_f32_e32 v47, v45, v46
	v_fma_f32 v32, -v44, v47, v45
	v_fmac_f32_e32 v47, v32, v46
	v_fma_f32 v44, -v44, v47, v45
	v_div_fmas_f32 v44, v44, v46, v47
	v_div_fixup_f32 v36, v44, v36, 2.0
	v_div_scale_f32 v44, s[6:7], v37, v37, 2.0
	v_rcp_f32_e32 v46, v44
	v_div_scale_f32 v45, vcc, 2.0, v37, 2.0
	v_fma_f32 v33, -v44, v46, 1.0
	v_fmac_f32_e32 v46, v33, v46
	v_mul_f32_e32 v47, v45, v46
	v_fma_f32 v33, -v44, v47, v45
	v_fmac_f32_e32 v47, v33, v46
	v_fma_f32 v44, -v44, v47, v45
	v_div_fmas_f32 v44, v44, v46, v47
	v_div_fixup_f32 v37, v44, v37, 2.0
	v_div_scale_f32 v44, s[6:7], v38, v38, 2.0
	v_rcp_f32_e32 v46, v44
	v_div_scale_f32 v45, vcc, 2.0, v38, 2.0
	v_fma_f32 v34, -v44, v46, 1.0
	v_fmac_f32_e32 v46, v34, v46
	v_mul_f32_e32 v47, v45, v46
	v_fma_f32 v34, -v44, v47, v45
	v_fmac_f32_e32 v47, v34, v46
	v_fma_f32 v44, -v44, v47, v45
	v_div_fmas_f32 v44, v44, v46, v47
	v_div_fixup_f32 v38, v44, v38, 2.0
	v_div_scale_f32 v44, s[6:7], v39, v39, 2.0
	v_rcp_f32_e32 v46, v44
	v_div_scale_f32 v45, vcc, 2.0, v39, 2.0
	v_fma_f32 v35, -v44, v46, 1.0
	v_fmac_f32_e32 v46, v35, v46
	v_mul_f32_e32 v47, v45, v46
	v_fma_f32 v35, -v44, v47, v45
	v_fmac_f32_e32 v47, v35, v46
	v_fma_f32 v44, -v44, v47, v45
	v_div_fmas_f32 v44, v44, v46, v47
	v_div_fixup_f32 v39, v44, v39, 2.0
	v_sub_f32_e32 v36, 1.0, v36
	v_sub_f32_e32 v37, 1.0, v37
	v_sub_f32_e32 v38, 1.0, v38
	v_sub_f32_e32 v39, 1.0, v39
	v_add_f32_e32 v36, 1.0, v36
	v_add_f32_e32 v37, 1.0, v37
	v_add_f32_e32 v38, 1.0, v38
	v_add_f32_e32 v39, 1.0, v39
	v_mul_f32_e32 v40, 0.5, v40
	v_mul_f32_e32 v41, 0.5, v41
	v_mul_f32_e32 v42, 0.5, v42
	v_mul_f32_e32 v43, 0.5, v43
	v_mul_f32_e32 v36, v40, v36
	v_mul_f32_e32 v37, v41, v37
	v_mul_f32_e32 v38, v42, v38
	v_mul_f32_e32 v39, v43, v39
	v_mul_f32_e32 v24, v24, v36
	v_mul_f32_e32 v25, v25, v37
	v_mul_f32_e32 v26, v26, v38
	v_mul_f32_e32 v27, v27, v39
	v_cvt_pk_bf16_f32 v28, v24, v25
	v_cvt_pk_bf16_f32 v29, v26, v27
	global_store_dwordx2 v23, v[28:29], s[2:3]
	v_add_u32_e32 v23, 0x1000, v23
	s_waitcnt vmcnt(29)
; __device__ __forceinline__ unsigned pk2(float lo, float hi) { return f2bf(lo) | (f2bf(hi) << 16); }
; __device__ __forceinline__ float gelu_tanh_(float x) { const float u = 0.7978845608028654f * (x + 0.044715f * x * x * x); const float t = 1.f - 2.f / (1.f + __expf(2.f * u)); return 0.5f * x * (1.f + t); }
; __device__ __forceinline__ void phase_attn(const Args& a, const Ctx& c0, int l, bool last) {
;     ...
;         for (int r = 0; r < 32; ++r) {
;             const u32x4 wf = *(const u32x4*)(hf + (size_t)r * 4096), wb = *(const u32x4*)(hb + (size_t)r * 4096); const u32x2 gw2 = *(const u32x2*)(zg + (size_t)r * RW); const f32x4 gr = {bflo(gw2.x), bfhi(gw2.x), bflo(gw2.y), bfhi(gw2.y)};
;             const float h0 = fmaf(bflo(wf.z), cf.x, bflo(wf.x)) + fmaf(bflo(wb.z), cb.x, bflo(wb.x)), h1 = fmaf(bfhi(wf.z), cf.y, bfhi(wf.x)) + fmaf(bfhi(wb.z), cb.y, bfhi(wb.x));
;             const float h2 = fmaf(bflo(wf.w), cf.z, bflo(wf.y)) + fmaf(bflo(wb.w), cb.z, bflo(wb.y)), h3 = fmaf(bfhi(wf.w), cf.w, bfhi(wf.y)) + fmaf(bfhi(wb.w), cb.w, bfhi(wb.y));
;             u32x2 w; w.x = pk2(h0 * gelu_tanh_(gr.x), h1 * gelu_tanh_(gr.y)); w.y = pk2(h2 * gelu_tanh_(gr.z), h3 * gelu_tanh_(gr.w));
;             *(u32x2*)(yo + (size_t)r * DM) = w; }
	v_lshlrev_b32_e32 v24, 16, v48
	v_and_b32_e32 v25, 0xffff0000, v48
	v_lshlrev_b32_e32 v26, 16, v49
	v_and_b32_e32 v27, 0xffff0000, v49
	v_lshlrev_b32_e32 v28, 16, v50
	v_and_b32_e32 v29, 0xffff0000, v50
	v_lshlrev_b32_e32 v30, 16, v51
	v_and_b32_e32 v31, 0xffff0000, v51
	v_lshlrev_b32_e32 v32, 16, v52
	v_and_b32_e32 v33, 0xffff0000, v52
	v_lshlrev_b32_e32 v34, 16, v53
	v_and_b32_e32 v35, 0xffff0000, v53
	v_lshlrev_b32_e32 v36, 16, v54
	v_and_b32_e32 v37, 0xffff0000, v54
	v_lshlrev_b32_e32 v38, 16, v55
	v_and_b32_e32 v39, 0xffff0000, v55
	v_fma_f32 v24, v28, v2, v24
	v_fma_f32 v25, v29, v16, v25
	v_fma_f32 v26, v30, v3, v26
	v_fma_f32 v27, v31, v17, v27
	v_fma_f32 v32, v36, v6, v32
	v_fma_f32 v33, v37, v18, v33
	v_fma_f32 v34, v38, v7, v34
	v_fma_f32 v35, v39, v19, v35
	v_add_f32_e32 v24, v24, v32
	v_add_f32_e32 v25, v25, v33
	v_add_f32_e32 v26, v26, v34
	v_add_f32_e32 v27, v27, v35
	v_lshlrev_b32_e32 v40, 16, v56
	v_and_b32_e32 v41, 0xffff0000, v56
	v_lshlrev_b32_e32 v42, 16, v57
	v_and_b32_e32 v43, 0xffff0000, v57
	global_load_dwordx4 v[48:51], v20, s[2:3]
	global_load_dwordx4 v[52:55], v21, s[2:3]
	global_load_dwordx2 v[56:57], v22, s[2:3]
	v_add_u32_e32 v20, 0x1000, v20
	v_add_u32_e32 v21, 0x1000, v21
	v_add_u32_e32 v22, 0x800, v22
	v_mul_f32_e32 v32, 0x3d372713, v40
	v_mul_f32_e32 v33, 0x3d372713, v41
	v_mul_f32_e32 v34, 0x3d372713, v42
	v_mul_f32_e32 v35, 0x3d372713, v43
	v_mul_f32_e32 v32, v32, v40
	v_mul_f32_e32 v33, v33, v41
	v_mul_f32_e32 v34, v34, v42
	v_mul_f32_e32 v35, v35, v43
	v_mov_b32_e32 v36, v40
	v_mov_b32_e32 v37, v41
	v_mov_b32_e32 v38, v42
	v_mov_b32_e32 v39, v43
	v_fmac_f32_e32 v36, v32, v36
	v_fmac_f32_e32 v37, v33, v37
	v_fmac_f32_e32 v38, v34, v38
	v_fmac_f32_e32 v39, v35, v39
	v_mul_f32_e32 v36, 0x3f4c422a, v36
	v_mul_f32_e32 v37, 0x3f4c422a, v37
	v_mul_f32_e32 v38, 0x3f4c422a, v38
	v_mul_f32_e32 v39, 0x3f4c422a, v39
	v_add_f32_e32 v36, v36, v36
	v_add_f32_e32 v37, v37, v37
	v_add_f32_e32 v38, v38, v38
	v_add_f32_e32 v39, v39, v39
	v_mul_f32_e32 v36, 0x3fb8aa3b, v36
	v_mul_f32_e32 v37, 0x3fb8aa3b, v37
	v_mul_f32_e32 v38, 0x3fb8aa3b, v38
	v_mul_f32_e32 v39, 0x3fb8aa3b, v39
	v_exp_f32_e32 v36, v36
	v_exp_f32_e32 v37, v37
	v_exp_f32_e32 v38, v38
	v_exp_f32_e32 v39, v39
	v_add_f32_e32 v36, 1.0, v36
	v_add_f32_e32 v37, 1.0, v37
	v_add_f32_e32 v38, 1.0, v38
	v_add_f32_e32 v39, 1.0, v39
	v_div_scale_f32 v44, s[6:7], v36, v36, 2.0
	v_rcp_f32_e32 v46, v44
	v_div_scale_f32 v45, vcc, 2.0, v36, 2.0
	v_fma_f32 v32, -v44, v46, 1.0
	v_fmac_f32_e32 v46, v32, v46
	v_mul_f32_e32 v47, v45, v46
	v_fma_f32 v32, -v44, v47, v45
	v_fmac_f32_e32 v47, v32, v46
	v_fma_f32 v44, -v44, v47, v45
	v_div_fmas_f32 v44, v44, v46, v47
	v_div_fixup_f32 v36, v44, v36, 2.0
	v_div_scale_f32 v44, s[6:7], v37, v37, 2.0
	v_rcp_f32_e32 v46, v44
	v_div_scale_f32 v45, vcc, 2.0, v37, 2.0
	v_fma_f32 v33, -v44, v46, 1.0
	v_fmac_f32_e32 v46, v33, v46
	v_mul_f32_e32 v47, v45, v46
	v_fma_f32 v33, -v44, v47, v45
	v_fmac_f32_e32 v47, v33, v46
	v_fma_f32 v44, -v44, v47, v45
	v_div_fmas_f32 v44, v44, v46, v47
	v_div_fixup_f32 v37, v44, v37, 2.0
	v_div_scale_f32 v44, s[6:7], v38, v38, 2.0
	v_rcp_f32_e32 v46, v44
	v_div_scale_f32 v45, vcc, 2.0, v38, 2.0
	v_fma_f32 v34, -v44, v46, 1.0
	v_fmac_f32_e32 v46, v34, v46
	v_mul_f32_e32 v47, v45, v46
	v_fma_f32 v34, -v44, v47, v45
	v_fmac_f32_e32 v47, v34, v46
	v_fma_f32 v44, -v44, v47, v45
	v_div_fmas_f32 v44, v44, v46, v47
	v_div_fixup_f32 v38, v44, v38, 2.0
	v_div_scale_f32 v44, s[6:7], v39, v39, 2.0
	v_rcp_f32_e32 v46, v44
	v_div_scale_f32 v45, vcc, 2.0, v39, 2.0
	v_fma_f32 v35, -v44, v46, 1.0
	v_fmac_f32_e32 v46, v35, v46
	v_mul_f32_e32 v47, v45, v46
	v_fma_f32 v35, -v44, v47, v45
	v_fmac_f32_e32 v47, v35, v46
	v_fma_f32 v44, -v44, v47, v45
	v_div_fmas_f32 v44, v44, v46, v47
	v_div_fixup_f32 v39, v44, v39, 2.0
	v_sub_f32_e32 v36, 1.0, v36
	v_sub_f32_e32 v37, 1.0, v37
	v_sub_f32_e32 v38, 1.0, v38
	v_sub_f32_e32 v39, 1.0, v39
	v_add_f32_e32 v36, 1.0, v36
	v_add_f32_e32 v37, 1.0, v37
	v_add_f32_e32 v38, 1.0, v38
	v_add_f32_e32 v39, 1.0, v39
	v_mul_f32_e32 v40, 0.5, v40
	v_mul_f32_e32 v41, 0.5, v41
	v_mul_f32_e32 v42, 0.5, v42
	v_mul_f32_e32 v43, 0.5, v43
	v_mul_f32_e32 v36, v40, v36
	v_mul_f32_e32 v37, v41, v37
	v_mul_f32_e32 v38, v42, v38
	v_mul_f32_e32 v39, v43, v39
	v_mul_f32_e32 v24, v24, v36
	v_mul_f32_e32 v25, v25, v37
	v_mul_f32_e32 v26, v26, v38
	v_mul_f32_e32 v27, v27, v39
	v_cvt_pk_bf16_f32 v28, v24, v25
	v_cvt_pk_bf16_f32 v29, v26, v27
	global_store_dwordx2 v23, v[28:29], s[2:3]
	v_add_u32_e32 v23, 0x1000, v23
	s_waitcnt vmcnt(29)
; __device__ __forceinline__ unsigned pk2(float lo, float hi) { return f2bf(lo) | (f2bf(hi) << 16); }
; __device__ __forceinline__ float gelu_tanh_(float x) { const float u = 0.7978845608028654f * (x + 0.044715f * x * x * x); const float t = 1.f - 2.f / (1.f + __expf(2.f * u)); return 0.5f * x * (1.f + t); }
; __device__ __forceinline__ void phase_attn(const Args& a, const Ctx& c0, int l, bool last) {
;     ...
;         for (int r = 0; r < 32; ++r) {
;             const u32x4 wf = *(const u32x4*)(hf + (size_t)r * 4096), wb = *(const u32x4*)(hb + (size_t)r * 4096); const u32x2 gw2 = *(const u32x2*)(zg + (size_t)r * RW); const f32x4 gr = {bflo(gw2.x), bfhi(gw2.x), bflo(gw2.y), bfhi(gw2.y)};
;             const float h0 = fmaf(bflo(wf.z), cf.x, bflo(wf.x)) + fmaf(bflo(wb.z), cb.x, bflo(wb.x)), h1 = fmaf(bfhi(wf.z), cf.y, bfhi(wf.x)) + fmaf(bfhi(wb.z), cb.y, bfhi(wb.x));
;             const float h2 = fmaf(bflo(wf.w), cf.z, bflo(wf.y)) + fmaf(bflo(wb.w), cb.z, bflo(wb.y)), h3 = fmaf(bfhi(wf.w), cf.w, bfhi(wf.y)) + fmaf(bfhi(wb.w), cb.w, bfhi(wb.y));
;             u32x2 w; w.x = pk2(h0 * gelu_tanh_(gr.x), h1 * gelu_tanh_(gr.y)); w.y = pk2(h2 * gelu_tanh_(gr.z), h3 * gelu_tanh_(gr.w));
;             *(u32x2*)(yo + (size_t)r * DM) = w; }
	v_lshlrev_b32_e32 v24, 16, v60
	v_and_b32_e32 v25, 0xffff0000, v60
	v_lshlrev_b32_e32 v26, 16, v61
	v_and_b32_e32 v27, 0xffff0000, v61
	v_lshlrev_b32_e32 v28, 16, v62
	v_and_b32_e32 v29, 0xffff0000, v62
	v_lshlrev_b32_e32 v30, 16, v63
	v_and_b32_e32 v31, 0xffff0000, v63
	v_lshlrev_b32_e32 v32, 16, v64
	v_and_b32_e32 v33, 0xffff0000, v64
	v_lshlrev_b32_e32 v34, 16, v65
	v_and_b32_e32 v35, 0xffff0000, v65
	v_lshlrev_b32_e32 v36, 16, v66
	v_and_b32_e32 v37, 0xffff0000, v66
	v_lshlrev_b32_e32 v38, 16, v67
	v_and_b32_e32 v39, 0xffff0000, v67
	v_fma_f32 v24, v28, v2, v24
	v_fma_f32 v25, v29, v16, v25
	v_fma_f32 v26, v30, v3, v26
	v_fma_f32 v27, v31, v17, v27
	v_fma_f32 v32, v36, v6, v32
	v_fma_f32 v33, v37, v18, v33
	v_fma_f32 v34, v38, v7, v34
	v_fma_f32 v35, v39, v19, v35
	v_add_f32_e32 v24, v24, v32
	v_add_f32_e32 v25, v25, v33
	v_add_f32_e32 v26, v26, v34
	v_add_f32_e32 v27, v27, v35
	v_lshlrev_b32_e32 v40, 16, v68
	v_and_b32_e32 v41, 0xffff0000, v68
	v_lshlrev_b32_e32 v42, 16, v69
	v_and_b32_e32 v43, 0xffff0000, v69
	global_load_dwordx4 v[60:63], v20, s[2:3]
	global_load_dwordx4 v[64:67], v21, s[2:3]
	global_load_dwordx2 v[68:69], v22, s[2:3]
	v_add_u32_e32 v20, 0x1000, v20
	v_add_u32_e32 v21, 0x1000, v21
	v_add_u32_e32 v22, 0x800, v22
	v_mul_f32_e32 v32, 0x3d372713, v40
	v_mul_f32_e32 v33, 0x3d372713, v41
	v_mul_f32_e32 v34, 0x3d372713, v42
	v_mul_f32_e32 v35, 0x3d372713, v43
	v_mul_f32_e32 v32, v32, v40
	v_mul_f32_e32 v33, v33, v41
	v_mul_f32_e32 v34, v34, v42
	v_mul_f32_e32 v35, v35, v43
	v_mov_b32_e32 v36, v40
	v_mov_b32_e32 v37, v41
	v_mov_b32_e32 v38, v42
	v_mov_b32_e32 v39, v43
	v_fmac_f32_e32 v36, v32, v36
	v_fmac_f32_e32 v37, v33, v37
	v_fmac_f32_e32 v38, v34, v38
	v_fmac_f32_e32 v39, v35, v39
	v_mul_f32_e32 v36, 0x3f4c422a, v36
	v_mul_f32_e32 v37, 0x3f4c422a, v37
	v_mul_f32_e32 v38, 0x3f4c422a, v38
	v_mul_f32_e32 v39, 0x3f4c422a, v39
	v_add_f32_e32 v36, v36, v36
	v_add_f32_e32 v37, v37, v37
	v_add_f32_e32 v38, v38, v38
	v_add_f32_e32 v39, v39, v39
	v_mul_f32_e32 v36, 0x3fb8aa3b, v36
	v_mul_f32_e32 v37, 0x3fb8aa3b, v37
	v_mul_f32_e32 v38, 0x3fb8aa3b, v38
	v_mul_f32_e32 v39, 0x3fb8aa3b, v39
	v_exp_f32_e32 v36, v36
	v_exp_f32_e32 v37, v37
	v_exp_f32_e32 v38, v38
	v_exp_f32_e32 v39, v39
	v_add_f32_e32 v36, 1.0, v36
	v_add_f32_e32 v37, 1.0, v37
	v_add_f32_e32 v38, 1.0, v38
	v_add_f32_e32 v39, 1.0, v39
	v_div_scale_f32 v44, s[6:7], v36, v36, 2.0
	v_rcp_f32_e32 v46, v44
	v_div_scale_f32 v45, vcc, 2.0, v36, 2.0
	v_fma_f32 v32, -v44, v46, 1.0
	v_fmac_f32_e32 v46, v32, v46
	v_mul_f32_e32 v47, v45, v46
	v_fma_f32 v32, -v44, v47, v45
	v_fmac_f32_e32 v47, v32, v46
	v_fma_f32 v44, -v44, v47, v45
	v_div_fmas_f32 v44, v44, v46, v47
	v_div_fixup_f32 v36, v44, v36, 2.0
	v_div_scale_f32 v44, s[6:7], v37, v37, 2.0
	v_rcp_f32_e32 v46, v44
	v_div_scale_f32 v45, vcc, 2.0, v37, 2.0
	v_fma_f32 v33, -v44, v46, 1.0
	v_fmac_f32_e32 v46, v33, v46
	v_mul_f32_e32 v47, v45, v46
	v_fma_f32 v33, -v44, v47, v45
	v_fmac_f32_e32 v47, v33, v46
	v_fma_f32 v44, -v44, v47, v45
	v_div_fmas_f32 v44, v44, v46, v47
	v_div_fixup_f32 v37, v44, v37, 2.0
	v_div_scale_f32 v44, s[6:7], v38, v38, 2.0
	v_rcp_f32_e32 v46, v44
	v_div_scale_f32 v45, vcc, 2.0, v38, 2.0
	v_fma_f32 v34, -v44, v46, 1.0
	v_fmac_f32_e32 v46, v34, v46
	v_mul_f32_e32 v47, v45, v46
	v_fma_f32 v34, -v44, v47, v45
	v_fmac_f32_e32 v47, v34, v46
	v_fma_f32 v44, -v44, v47, v45
	v_div_fmas_f32 v44, v44, v46, v47
	v_div_fixup_f32 v38, v44, v38, 2.0
	v_div_scale_f32 v44, s[6:7], v39, v39, 2.0
	v_rcp_f32_e32 v46, v44
	v_div_scale_f32 v45, vcc, 2.0, v39, 2.0
	v_fma_f32 v35, -v44, v46, 1.0
	v_fmac_f32_e32 v46, v35, v46
	v_mul_f32_e32 v47, v45, v46
	v_fma_f32 v35, -v44, v47, v45
	v_fmac_f32_e32 v47, v35, v46
	v_fma_f32 v44, -v44, v47, v45
	v_div_fmas_f32 v44, v44, v46, v47
	v_div_fixup_f32 v39, v44, v39, 2.0
	v_sub_f32_e32 v36, 1.0, v36
	v_sub_f32_e32 v37, 1.0, v37
	v_sub_f32_e32 v38, 1.0, v38
	v_sub_f32_e32 v39, 1.0, v39
	v_add_f32_e32 v36, 1.0, v36
	v_add_f32_e32 v37, 1.0, v37
	v_add_f32_e32 v38, 1.0, v38
	v_add_f32_e32 v39, 1.0, v39
	v_mul_f32_e32 v40, 0.5, v40
	v_mul_f32_e32 v41, 0.5, v41
	v_mul_f32_e32 v42, 0.5, v42
	v_mul_f32_e32 v43, 0.5, v43
	v_mul_f32_e32 v36, v40, v36
	v_mul_f32_e32 v37, v41, v37
	v_mul_f32_e32 v38, v42, v38
	v_mul_f32_e32 v39, v43, v39
	v_mul_f32_e32 v24, v24, v36
	v_mul_f32_e32 v25, v25, v37
	v_mul_f32_e32 v26, v26, v38
	v_mul_f32_e32 v27, v27, v39
	v_cvt_pk_bf16_f32 v28, v24, v25
	v_cvt_pk_bf16_f32 v29, v26, v27
	global_store_dwordx2 v23, v[28:29], s[2:3]
	v_add_u32_e32 v23, 0x1000, v23
	s_waitcnt vmcnt(29)
; __device__ __forceinline__ unsigned pk2(float lo, float hi) { return f2bf(lo) | (f2bf(hi) << 16); }
; __device__ __forceinline__ float gelu_tanh_(float x) { const float u = 0.7978845608028654f * (x + 0.044715f * x * x * x); const float t = 1.f - 2.f / (1.f + __expf(2.f * u)); return 0.5f * x * (1.f + t); }
; __device__ __forceinline__ void phase_attn(const Args& a, const Ctx& c0, int l, bool last) {
;     ...
;         for (int r = 0; r < 32; ++r) {
;             const u32x4 wf = *(const u32x4*)(hf + (size_t)r * 4096), wb = *(const u32x4*)(hb + (size_t)r * 4096); const u32x2 gw2 = *(const u32x2*)(zg + (size_t)r * RW); const f32x4 gr = {bflo(gw2.x), bfhi(gw2.x), bflo(gw2.y), bfhi(gw2.y)};
;             const float h0 = fmaf(bflo(wf.z), cf.x, bflo(wf.x)) + fmaf(bflo(wb.z), cb.x, bflo(wb.x)), h1 = fmaf(bfhi(wf.z), cf.y, bfhi(wf.x)) + fmaf(bfhi(wb.z), cb.y, bfhi(wb.x));
;             const float h2 = fmaf(bflo(wf.w), cf.z, bflo(wf.y)) + fmaf(bflo(wb.w), cb.z, bflo(wb.y)), h3 = fmaf(bfhi(wf.w), cf.w, bfhi(wf.y)) + fmaf(bfhi(wb.w), cb.w, bfhi(wb.y));
;             u32x2 w; w.x = pk2(h0 * gelu_tanh_(gr.x), h1 * gelu_tanh_(gr.y)); w.y = pk2(h2 * gelu_tanh_(gr.z), h3 * gelu_tanh_(gr.w));
;             *(u32x2*)(yo + (size_t)r * DM) = w; }
	v_lshlrev_b32_e32 v24, 16, v72
	v_and_b32_e32 v25, 0xffff0000, v72
	v_lshlrev_b32_e32 v26, 16, v73
	v_and_b32_e32 v27, 0xffff0000, v73
	v_lshlrev_b32_e32 v28, 16, v74
	v_and_b32_e32 v29, 0xffff0000, v74
	v_lshlrev_b32_e32 v30, 16, v75
	v_and_b32_e32 v31, 0xffff0000, v75
	v_lshlrev_b32_e32 v32, 16, v76
	v_and_b32_e32 v33, 0xffff0000, v76
	v_lshlrev_b32_e32 v34, 16, v77
	v_and_b32_e32 v35, 0xffff0000, v77
	v_lshlrev_b32_e32 v36, 16, v78
	v_and_b32_e32 v37, 0xffff0000, v78
	v_lshlrev_b32_e32 v38, 16, v79
	v_and_b32_e32 v39, 0xffff0000, v79
	v_fma_f32 v24, v28, v2, v24
	v_fma_f32 v25, v29, v16, v25
	v_fma_f32 v26, v30, v3, v26
	v_fma_f32 v27, v31, v17, v27
	v_fma_f32 v32, v36, v6, v32
	v_fma_f32 v33, v37, v18, v33
	v_fma_f32 v34, v38, v7, v34
	v_fma_f32 v35, v39, v19, v35
	v_add_f32_e32 v24, v24, v32
	v_add_f32_e32 v25, v25, v33
	v_add_f32_e32 v26, v26, v34
	v_add_f32_e32 v27, v27, v35
	v_lshlrev_b32_e32 v40, 16, v80
	v_and_b32_e32 v41, 0xffff0000, v80
	v_lshlrev_b32_e32 v42, 16, v81
	v_and_b32_e32 v43, 0xffff0000, v81
	global_load_dwordx4 v[72:75], v20, s[2:3]
	global_load_dwordx4 v[76:79], v21, s[2:3]
	global_load_dwordx2 v[80:81], v22, s[2:3]
	v_add_u32_e32 v20, 0x1000, v20
	v_add_u32_e32 v21, 0x1000, v21
	v_add_u32_e32 v22, 0x800, v22
	v_mul_f32_e32 v32, 0x3d372713, v40
	v_mul_f32_e32 v33, 0x3d372713, v41
	v_mul_f32_e32 v34, 0x3d372713, v42
	v_mul_f32_e32 v35, 0x3d372713, v43
	v_mul_f32_e32 v32, v32, v40
	v_mul_f32_e32 v33, v33, v41
	v_mul_f32_e32 v34, v34, v42
	v_mul_f32_e32 v35, v35, v43
	v_mov_b32_e32 v36, v40
	v_mov_b32_e32 v37, v41
	v_mov_b32_e32 v38, v42
	v_mov_b32_e32 v39, v43
	v_fmac_f32_e32 v36, v32, v36
	v_fmac_f32_e32 v37, v33, v37
	v_fmac_f32_e32 v38, v34, v38
	v_fmac_f32_e32 v39, v35, v39
	v_mul_f32_e32 v36, 0x3f4c422a, v36
	v_mul_f32_e32 v37, 0x3f4c422a, v37
	v_mul_f32_e32 v38, 0x3f4c422a, v38
	v_mul_f32_e32 v39, 0x3f4c422a, v39
	v_add_f32_e32 v36, v36, v36
	v_add_f32_e32 v37, v37, v37
	v_add_f32_e32 v38, v38, v38
	v_add_f32_e32 v39, v39, v39
	v_mul_f32_e32 v36, 0x3fb8aa3b, v36
	v_mul_f32_e32 v37, 0x3fb8aa3b, v37
	v_mul_f32_e32 v38, 0x3fb8aa3b, v38
	v_mul_f32_e32 v39, 0x3fb8aa3b, v39
	v_exp_f32_e32 v36, v36
	v_exp_f32_e32 v37, v37
	v_exp_f32_e32 v38, v38
	v_exp_f32_e32 v39, v39
	v_add_f32_e32 v36, 1.0, v36
	v_add_f32_e32 v37, 1.0, v37
	v_add_f32_e32 v38, 1.0, v38
	v_add_f32_e32 v39, 1.0, v39
	v_div_scale_f32 v44, s[6:7], v36, v36, 2.0
	v_rcp_f32_e32 v46, v44
	v_div_scale_f32 v45, vcc, 2.0, v36, 2.0
	v_fma_f32 v32, -v44, v46, 1.0
	v_fmac_f32_e32 v46, v32, v46
	v_mul_f32_e32 v47, v45, v46
	v_fma_f32 v32, -v44, v47, v45
	v_fmac_f32_e32 v47, v32, v46
	v_fma_f32 v44, -v44, v47, v45
	v_div_fmas_f32 v44, v44, v46, v47
	v_div_fixup_f32 v36, v44, v36, 2.0
	v_div_scale_f32 v44, s[6:7], v37, v37, 2.0
	v_rcp_f32_e32 v46, v44
	v_div_scale_f32 v45, vcc, 2.0, v37, 2.0
	v_fma_f32 v33, -v44, v46, 1.0
	v_fmac_f32_e32 v46, v33, v46
	v_mul_f32_e32 v47, v45, v46
	v_fma_f32 v33, -v44, v47, v45
	v_fmac_f32_e32 v47, v33, v46
	v_fma_f32 v44, -v44, v47, v45
	v_div_fmas_f32 v44, v44, v46, v47
	v_div_fixup_f32 v37, v44, v37, 2.0
	v_div_scale_f32 v44, s[6:7], v38, v38, 2.0
	v_rcp_f32_e32 v46, v44
	v_div_scale_f32 v45, vcc, 2.0, v38, 2.0
	v_fma_f32 v34, -v44, v46, 1.0
	v_fmac_f32_e32 v46, v34, v46
	v_mul_f32_e32 v47, v45, v46
	v_fma_f32 v34, -v44, v47, v45
	v_fmac_f32_e32 v47, v34, v46
	v_fma_f32 v44, -v44, v47, v45
	v_div_fmas_f32 v44, v44, v46, v47
	v_div_fixup_f32 v38, v44, v38, 2.0
	v_div_scale_f32 v44, s[6:7], v39, v39, 2.0
	v_rcp_f32_e32 v46, v44
	v_div_scale_f32 v45, vcc, 2.0, v39, 2.0
	v_fma_f32 v35, -v44, v46, 1.0
	v_fmac_f32_e32 v46, v35, v46
	v_mul_f32_e32 v47, v45, v46
	v_fma_f32 v35, -v44, v47, v45
	v_fmac_f32_e32 v47, v35, v46
	v_fma_f32 v44, -v44, v47, v45
	v_div_fmas_f32 v44, v44, v46, v47
	v_div_fixup_f32 v39, v44, v39, 2.0
	v_sub_f32_e32 v36, 1.0, v36
	v_sub_f32_e32 v37, 1.0, v37
	v_sub_f32_e32 v38, 1.0, v38
	v_sub_f32_e32 v39, 1.0, v39
	v_add_f32_e32 v36, 1.0, v36
	v_add_f32_e32 v37, 1.0, v37
	v_add_f32_e32 v38, 1.0, v38
	v_add_f32_e32 v39, 1.0, v39
	v_mul_f32_e32 v40, 0.5, v40
	v_mul_f32_e32 v41, 0.5, v41
	v_mul_f32_e32 v42, 0.5, v42
	v_mul_f32_e32 v43, 0.5, v43
	v_mul_f32_e32 v36, v40, v36
	v_mul_f32_e32 v37, v41, v37
	v_mul_f32_e32 v38, v42, v38
	v_mul_f32_e32 v39, v43, v39
	v_mul_f32_e32 v24, v24, v36
	v_mul_f32_e32 v25, v25, v37
	v_mul_f32_e32 v26, v26, v38
	v_mul_f32_e32 v27, v27, v39
	v_cvt_pk_bf16_f32 v28, v24, v25
	v_cvt_pk_bf16_f32 v29, v26, v27
	global_store_dwordx2 v23, v[28:29], s[2:3]
	v_add_u32_e32 v23, 0x1000, v23
	s_waitcnt vmcnt(29)
; __device__ __forceinline__ unsigned pk2(float lo, float hi) { return f2bf(lo) | (f2bf(hi) << 16); }
; __device__ __forceinline__ float gelu_tanh_(float x) { const float u = 0.7978845608028654f * (x + 0.044715f * x * x * x); const float t = 1.f - 2.f / (1.f + __expf(2.f * u)); return 0.5f * x * (1.f + t); }
; __device__ __forceinline__ void phase_attn(const Args& a, const Ctx& c0, int l, bool last) {
;     ...
;         for (int r = 0; r < 32; ++r) {
;             const u32x4 wf = *(const u32x4*)(hf + (size_t)r * 4096), wb = *(const u32x4*)(hb + (size_t)r * 4096); const u32x2 gw2 = *(const u32x2*)(zg + (size_t)r * RW); const f32x4 gr = {bflo(gw2.x), bfhi(gw2.x), bflo(gw2.y), bfhi(gw2.y)};
;             const float h0 = fmaf(bflo(wf.z), cf.x, bflo(wf.x)) + fmaf(bflo(wb.z), cb.x, bflo(wb.x)), h1 = fmaf(bfhi(wf.z), cf.y, bfhi(wf.x)) + fmaf(bfhi(wb.z), cb.y, bfhi(wb.x));
;             const float h2 = fmaf(bflo(wf.w), cf.z, bflo(wf.y)) + fmaf(bflo(wb.w), cb.z, bflo(wb.y)), h3 = fmaf(bfhi(wf.w), cf.w, bfhi(wf.y)) + fmaf(bfhi(wb.w), cb.w, bfhi(wb.y));
;             u32x2 w; w.x = pk2(h0 * gelu_tanh_(gr.x), h1 * gelu_tanh_(gr.y)); w.y = pk2(h2 * gelu_tanh_(gr.z), h3 * gelu_tanh_(gr.w));
;             *(u32x2*)(yo + (size_t)r * DM) = w; }
	v_lshlrev_b32_e32 v24, 16, v84
	v_and_b32_e32 v25, 0xffff0000, v84
	v_lshlrev_b32_e32 v26, 16, v85
	v_and_b32_e32 v27, 0xffff0000, v85
	v_lshlrev_b32_e32 v28, 16, v86
	v_and_b32_e32 v29, 0xffff0000, v86
	v_lshlrev_b32_e32 v30, 16, v87
	v_and_b32_e32 v31, 0xffff0000, v87
	v_lshlrev_b32_e32 v32, 16, v88
	v_and_b32_e32 v33, 0xffff0000, v88
	v_lshlrev_b32_e32 v34, 16, v89
	v_and_b32_e32 v35, 0xffff0000, v89
	v_lshlrev_b32_e32 v36, 16, v90
	v_and_b32_e32 v37, 0xffff0000, v90
	v_lshlrev_b32_e32 v38, 16, v91
	v_and_b32_e32 v39, 0xffff0000, v91
	v_fma_f32 v24, v28, v2, v24
	v_fma_f32 v25, v29, v16, v25
	v_fma_f32 v26, v30, v3, v26
	v_fma_f32 v27, v31, v17, v27
	v_fma_f32 v32, v36, v6, v32
	v_fma_f32 v33, v37, v18, v33
	v_fma_f32 v34, v38, v7, v34
	v_fma_f32 v35, v39, v19, v35
	v_add_f32_e32 v24, v24, v32
	v_add_f32_e32 v25, v25, v33
	v_add_f32_e32 v26, v26, v34
	v_add_f32_e32 v27, v27, v35
	v_lshlrev_b32_e32 v40, 16, v92
	v_and_b32_e32 v41, 0xffff0000, v92
	v_lshlrev_b32_e32 v42, 16, v93
	v_and_b32_e32 v43, 0xffff0000, v93
	global_load_dwordx4 v[84:87], v20, s[2:3]
	global_load_dwordx4 v[88:91], v21, s[2:3]
	global_load_dwordx2 v[92:93], v22, s[2:3]
	v_add_u32_e32 v20, 0x1000, v20
	v_add_u32_e32 v21, 0x1000, v21
	v_add_u32_e32 v22, 0x800, v22
	v_mul_f32_e32 v32, 0x3d372713, v40
	v_mul_f32_e32 v33, 0x3d372713, v41
	v_mul_f32_e32 v34, 0x3d372713, v42
	v_mul_f32_e32 v35, 0x3d372713, v43
	v_mul_f32_e32 v32, v32, v40
	v_mul_f32_e32 v33, v33, v41
	v_mul_f32_e32 v34, v34, v42
	v_mul_f32_e32 v35, v35, v43
	v_mov_b32_e32 v36, v40
	v_mov_b32_e32 v37, v41
	v_mov_b32_e32 v38, v42
	v_mov_b32_e32 v39, v43
	v_fmac_f32_e32 v36, v32, v36
	v_fmac_f32_e32 v37, v33, v37
	v_fmac_f32_e32 v38, v34, v38
	v_fmac_f32_e32 v39, v35, v39
	v_mul_f32_e32 v36, 0x3f4c422a, v36
	v_mul_f32_e32 v37, 0x3f4c422a, v37
	v_mul_f32_e32 v38, 0x3f4c422a, v38
	v_mul_f32_e32 v39, 0x3f4c422a, v39
	v_add_f32_e32 v36, v36, v36
	v_add_f32_e32 v37, v37, v37
	v_add_f32_e32 v38, v38, v38
	v_add_f32_e32 v39, v39, v39
	v_mul_f32_e32 v36, 0x3fb8aa3b, v36
	v_mul_f32_e32 v37, 0x3fb8aa3b, v37
	v_mul_f32_e32 v38, 0x3fb8aa3b, v38
	v_mul_f32_e32 v39, 0x3fb8aa3b, v39
	v_exp_f32_e32 v36, v36
	v_exp_f32_e32 v37, v37
	v_exp_f32_e32 v38, v38
	v_exp_f32_e32 v39, v39
	v_add_f32_e32 v36, 1.0, v36
	v_add_f32_e32 v37, 1.0, v37
	v_add_f32_e32 v38, 1.0, v38
	v_add_f32_e32 v39, 1.0, v39
	v_div_scale_f32 v44, s[6:7], v36, v36, 2.0
	v_rcp_f32_e32 v46, v44
	v_div_scale_f32 v45, vcc, 2.0, v36, 2.0
	v_fma_f32 v32, -v44, v46, 1.0
	v_fmac_f32_e32 v46, v32, v46
	v_mul_f32_e32 v47, v45, v46
	v_fma_f32 v32, -v44, v47, v45
	v_fmac_f32_e32 v47, v32, v46
	v_fma_f32 v44, -v44, v47, v45
	v_div_fmas_f32 v44, v44, v46, v47
	v_div_fixup_f32 v36, v44, v36, 2.0
	v_div_scale_f32 v44, s[6:7], v37, v37, 2.0
	v_rcp_f32_e32 v46, v44
	v_div_scale_f32 v45, vcc, 2.0, v37, 2.0
	v_fma_f32 v33, -v44, v46, 1.0
	v_fmac_f32_e32 v46, v33, v46
	v_mul_f32_e32 v47, v45, v46
	v_fma_f32 v33, -v44, v47, v45
	v_fmac_f32_e32 v47, v33, v46
	v_fma_f32 v44, -v44, v47, v45
	v_div_fmas_f32 v44, v44, v46, v47
	v_div_fixup_f32 v37, v44, v37, 2.0
	v_div_scale_f32 v44, s[6:7], v38, v38, 2.0
	v_rcp_f32_e32 v46, v44
	v_div_scale_f32 v45, vcc, 2.0, v38, 2.0
	v_fma_f32 v34, -v44, v46, 1.0
	v_fmac_f32_e32 v46, v34, v46
	v_mul_f32_e32 v47, v45, v46
	v_fma_f32 v34, -v44, v47, v45
	v_fmac_f32_e32 v47, v34, v46
	v_fma_f32 v44, -v44, v47, v45
	v_div_fmas_f32 v44, v44, v46, v47
	v_div_fixup_f32 v38, v44, v38, 2.0
	v_div_scale_f32 v44, s[6:7], v39, v39, 2.0
	v_rcp_f32_e32 v46, v44
	v_div_scale_f32 v45, vcc, 2.0, v39, 2.0
	v_fma_f32 v35, -v44, v46, 1.0
	v_fmac_f32_e32 v46, v35, v46
	v_mul_f32_e32 v47, v45, v46
	v_fma_f32 v35, -v44, v47, v45
	v_fmac_f32_e32 v47, v35, v46
	v_fma_f32 v44, -v44, v47, v45
	v_div_fmas_f32 v44, v44, v46, v47
	v_div_fixup_f32 v39, v44, v39, 2.0
	v_sub_f32_e32 v36, 1.0, v36
	v_sub_f32_e32 v37, 1.0, v37
	v_sub_f32_e32 v38, 1.0, v38
	v_sub_f32_e32 v39, 1.0, v39
	v_add_f32_e32 v36, 1.0, v36
	v_add_f32_e32 v37, 1.0, v37
	v_add_f32_e32 v38, 1.0, v38
	v_add_f32_e32 v39, 1.0, v39
	v_mul_f32_e32 v40, 0.5, v40
	v_mul_f32_e32 v41, 0.5, v41
	v_mul_f32_e32 v42, 0.5, v42
	v_mul_f32_e32 v43, 0.5, v43
	v_mul_f32_e32 v36, v40, v36
	v_mul_f32_e32 v37, v41, v37
	v_mul_f32_e32 v38, v42, v38
	v_mul_f32_e32 v39, v43, v39
	v_mul_f32_e32 v24, v24, v36
	v_mul_f32_e32 v25, v25, v37
	v_mul_f32_e32 v26, v26, v38
	v_mul_f32_e32 v27, v27, v39
	v_cvt_pk_bf16_f32 v28, v24, v25
	v_cvt_pk_bf16_f32 v29, v26, v27
	global_store_dwordx2 v23, v[28:29], s[2:3]
	v_add_u32_e32 v23, 0x1000, v23
	s_waitcnt vmcnt(29)
; __device__ __forceinline__ unsigned pk2(float lo, float hi) { return f2bf(lo) | (f2bf(hi) << 16); }
; __device__ __forceinline__ float gelu_tanh_(float x) { const float u = 0.7978845608028654f * (x + 0.044715f * x * x * x); const float t = 1.f - 2.f / (1.f + __expf(2.f * u)); return 0.5f * x * (1.f + t); }
; __device__ __forceinline__ void phase_attn(const Args& a, const Ctx& c0, int l, bool last) {
;     ...
;         for (int r = 0; r < 32; ++r) {
;             const u32x4 wf = *(const u32x4*)(hf + (size_t)r * 4096), wb = *(const u32x4*)(hb + (size_t)r * 4096); const u32x2 gw2 = *(const u32x2*)(zg + (size_t)r * RW); const f32x4 gr = {bflo(gw2.x), bfhi(gw2.x), bflo(gw2.y), bfhi(gw2.y)};
;             const float h0 = fmaf(bflo(wf.z), cf.x, bflo(wf.x)) + fmaf(bflo(wb.z), cb.x, bflo(wb.x)), h1 = fmaf(bfhi(wf.z), cf.y, bfhi(wf.x)) + fmaf(bfhi(wb.z), cb.y, bfhi(wb.x));
;             const float h2 = fmaf(bflo(wf.w), cf.z, bflo(wf.y)) + fmaf(bflo(wb.w), cb.z, bflo(wb.y)), h3 = fmaf(bfhi(wf.w), cf.w, bfhi(wf.y)) + fmaf(bfhi(wb.w), cb.w, bfhi(wb.y));
;             u32x2 w; w.x = pk2(h0 * gelu_tanh_(gr.x), h1 * gelu_tanh_(gr.y)); w.y = pk2(h2 * gelu_tanh_(gr.z), h3 * gelu_tanh_(gr.w));
;             *(u32x2*)(yo + (size_t)r * DM) = w; }
	v_lshlrev_b32_e32 v24, 16, v96
	v_and_b32_e32 v25, 0xffff0000, v96
	v_lshlrev_b32_e32 v26, 16, v97
	v_and_b32_e32 v27, 0xffff0000, v97
	v_lshlrev_b32_e32 v28, 16, v98
	v_and_b32_e32 v29, 0xffff0000, v98
	v_lshlrev_b32_e32 v30, 16, v99
	v_and_b32_e32 v31, 0xffff0000, v99
	v_lshlrev_b32_e32 v32, 16, v100
	v_and_b32_e32 v33, 0xffff0000, v100
	v_lshlrev_b32_e32 v34, 16, v101
	v_and_b32_e32 v35, 0xffff0000, v101
	v_lshlrev_b32_e32 v36, 16, v102
	v_and_b32_e32 v37, 0xffff0000, v102
	v_lshlrev_b32_e32 v38, 16, v103
	v_and_b32_e32 v39, 0xffff0000, v103
	v_fma_f32 v24, v28, v2, v24
	v_fma_f32 v25, v29, v16, v25
	v_fma_f32 v26, v30, v3, v26
	v_fma_f32 v27, v31, v17, v27
	v_fma_f32 v32, v36, v6, v32
	v_fma_f32 v33, v37, v18, v33
	v_fma_f32 v34, v38, v7, v34
	v_fma_f32 v35, v39, v19, v35
	v_add_f32_e32 v24, v24, v32
	v_add_f32_e32 v25, v25, v33
	v_add_f32_e32 v26, v26, v34
	v_add_f32_e32 v27, v27, v35
	v_lshlrev_b32_e32 v40, 16, v104
	v_and_b32_e32 v41, 0xffff0000, v104
	v_lshlrev_b32_e32 v42, 16, v105
	v_and_b32_e32 v43, 0xffff0000, v105
	global_load_dwordx4 v[96:99], v20, s[2:3]
	global_load_dwordx4 v[100:103], v21, s[2:3]
	global_load_dwordx2 v[104:105], v22, s[2:3]
	v_add_u32_e32 v20, 0x1000, v20
	v_add_u32_e32 v21, 0x1000, v21
	v_add_u32_e32 v22, 0x800, v22
	v_mul_f32_e32 v32, 0x3d372713, v40
	v_mul_f32_e32 v33, 0x3d372713, v41
	v_mul_f32_e32 v34, 0x3d372713, v42
	v_mul_f32_e32 v35, 0x3d372713, v43
	v_mul_f32_e32 v32, v32, v40
	v_mul_f32_e32 v33, v33, v41
	v_mul_f32_e32 v34, v34, v42
	v_mul_f32_e32 v35, v35, v43
	v_mov_b32_e32 v36, v40
	v_mov_b32_e32 v37, v41
	v_mov_b32_e32 v38, v42
	v_mov_b32_e32 v39, v43
	v_fmac_f32_e32 v36, v32, v36
	v_fmac_f32_e32 v37, v33, v37
	v_fmac_f32_e32 v38, v34, v38
	v_fmac_f32_e32 v39, v35, v39
	v_mul_f32_e32 v36, 0x3f4c422a, v36
	v_mul_f32_e32 v37, 0x3f4c422a, v37
	v_mul_f32_e32 v38, 0x3f4c422a, v38
	v_mul_f32_e32 v39, 0x3f4c422a, v39
	v_add_f32_e32 v36, v36, v36
	v_add_f32_e32 v37, v37, v37
	v_add_f32_e32 v38, v38, v38
	v_add_f32_e32 v39, v39, v39
	v_mul_f32_e32 v36, 0x3fb8aa3b, v36
	v_mul_f32_e32 v37, 0x3fb8aa3b, v37
	v_mul_f32_e32 v38, 0x3fb8aa3b, v38
	v_mul_f32_e32 v39, 0x3fb8aa3b, v39
	v_exp_f32_e32 v36, v36
	v_exp_f32_e32 v37, v37
	v_exp_f32_e32 v38, v38
	v_exp_f32_e32 v39, v39
	v_add_f32_e32 v36, 1.0, v36
	v_add_f32_e32 v37, 1.0, v37
	v_add_f32_e32 v38, 1.0, v38
	v_add_f32_e32 v39, 1.0, v39
	v_div_scale_f32 v44, s[6:7], v36, v36, 2.0
	v_rcp_f32_e32 v46, v44
	v_div_scale_f32 v45, vcc, 2.0, v36, 2.0
	v_fma_f32 v32, -v44, v46, 1.0
	v_fmac_f32_e32 v46, v32, v46
	v_mul_f32_e32 v47, v45, v46
	v_fma_f32 v32, -v44, v47, v45
	v_fmac_f32_e32 v47, v32, v46
	v_fma_f32 v44, -v44, v47, v45
	v_div_fmas_f32 v44, v44, v46, v47
	v_div_fixup_f32 v36, v44, v36, 2.0
	v_div_scale_f32 v44, s[6:7], v37, v37, 2.0
	v_rcp_f32_e32 v46, v44
	v_div_scale_f32 v45, vcc, 2.0, v37, 2.0
	v_fma_f32 v33, -v44, v46, 1.0
	v_fmac_f32_e32 v46, v33, v46
	v_mul_f32_e32 v47, v45, v46
	v_fma_f32 v33, -v44, v47, v45
	v_fmac_f32_e32 v47, v33, v46
	v_fma_f32 v44, -v44, v47, v45
	v_div_fmas_f32 v44, v44, v46, v47
	v_div_fixup_f32 v37, v44, v37, 2.0
	v_div_scale_f32 v44, s[6:7], v38, v38, 2.0
	v_rcp_f32_e32 v46, v44
	v_div_scale_f32 v45, vcc, 2.0, v38, 2.0
	v_fma_f32 v34, -v44, v46, 1.0
	v_fmac_f32_e32 v46, v34, v46
	v_mul_f32_e32 v47, v45, v46
	v_fma_f32 v34, -v44, v47, v45
	v_fmac_f32_e32 v47, v34, v46
	v_fma_f32 v44, -v44, v47, v45
	v_div_fmas_f32 v44, v44, v46, v47
	v_div_fixup_f32 v38, v44, v38, 2.0
	v_div_scale_f32 v44, s[6:7], v39, v39, 2.0
	v_rcp_f32_e32 v46, v44
	v_div_scale_f32 v45, vcc, 2.0, v39, 2.0
	v_fma_f32 v35, -v44, v46, 1.0
	v_fmac_f32_e32 v46, v35, v46
	v_mul_f32_e32 v47, v45, v46
	v_fma_f32 v35, -v44, v47, v45
	v_fmac_f32_e32 v47, v35, v46
	v_fma_f32 v44, -v44, v47, v45
	v_div_fmas_f32 v44, v44, v46, v47
	v_div_fixup_f32 v39, v44, v39, 2.0
	v_sub_f32_e32 v36, 1.0, v36
	v_sub_f32_e32 v37, 1.0, v37
	v_sub_f32_e32 v38, 1.0, v38
	v_sub_f32_e32 v39, 1.0, v39
	v_add_f32_e32 v36, 1.0, v36
	v_add_f32_e32 v37, 1.0, v37
	v_add_f32_e32 v38, 1.0, v38
	v_add_f32_e32 v39, 1.0, v39
	v_mul_f32_e32 v40, 0.5, v40
	v_mul_f32_e32 v41, 0.5, v41
	v_mul_f32_e32 v42, 0.5, v42
	v_mul_f32_e32 v43, 0.5, v43
	v_mul_f32_e32 v36, v40, v36
	v_mul_f32_e32 v37, v41, v37
	v_mul_f32_e32 v38, v42, v38
	v_mul_f32_e32 v39, v43, v39
	v_mul_f32_e32 v24, v24, v36
	v_mul_f32_e32 v25, v25, v37
	v_mul_f32_e32 v26, v26, v38
	v_mul_f32_e32 v27, v27, v39
	v_cvt_pk_bf16_f32 v28, v24, v25
	v_cvt_pk_bf16_f32 v29, v26, v27
	global_store_dwordx2 v23, v[28:29], s[2:3]
	v_add_u32_e32 v23, 0x1000, v23
	s_waitcnt vmcnt(29)
; __device__ __forceinline__ unsigned pk2(float lo, float hi) { return f2bf(lo) | (f2bf(hi) << 16); }
; __device__ __forceinline__ float gelu_tanh_(float x) { const float u = 0.7978845608028654f * (x + 0.044715f * x * x * x); const float t = 1.f - 2.f / (1.f + __expf(2.f * u)); return 0.5f * x * (1.f + t); }
; __device__ __forceinline__ void phase_attn(const Args& a, const Ctx& c0, int l, bool last) {
;     ...
;         for (int r = 0; r < 32; ++r) {
;             const u32x4 wf = *(const u32x4*)(hf + (size_t)r * 4096), wb = *(const u32x4*)(hb + (size_t)r * 4096); const u32x2 gw2 = *(const u32x2*)(zg + (size_t)r * RW); const f32x4 gr = {bflo(gw2.x), bfhi(gw2.x), bflo(gw2.y), bfhi(gw2.y)};
;             const float h0 = fmaf(bflo(wf.z), cf.x, bflo(wf.x)) + fmaf(bflo(wb.z), cb.x, bflo(wb.x)), h1 = fmaf(bfhi(wf.z), cf.y, bfhi(wf.x)) + fmaf(bfhi(wb.z), cb.y, bfhi(wb.x));
;             const float h2 = fmaf(bflo(wf.w), cf.z, bflo(wf.y)) + fmaf(bflo(wb.w), cb.z, bflo(wb.y)), h3 = fmaf(bfhi(wf.w), cf.w, bfhi(wf.y)) + fmaf(bfhi(wb.w), cb.w, bfhi(wb.y));
;             u32x2 w; w.x = pk2(h0 * gelu_tanh_(gr.x), h1 * gelu_tanh_(gr.y)); w.y = pk2(h2 * gelu_tanh_(gr.z), h3 * gelu_tanh_(gr.w));
;             *(u32x2*)(yo + (size_t)r * DM) = w; }
	v_lshlrev_b32_e32 v24, 16, v108
	v_and_b32_e32 v25, 0xffff0000, v108
	v_lshlrev_b32_e32 v26, 16, v109
	v_and_b32_e32 v27, 0xffff0000, v109
	v_lshlrev_b32_e32 v28, 16, v110
	v_and_b32_e32 v29, 0xffff0000, v110
	v_lshlrev_b32_e32 v30, 16, v111
	v_and_b32_e32 v31, 0xffff0000, v111
	v_lshlrev_b32_e32 v32, 16, v112
	v_and_b32_e32 v33, 0xffff0000, v112
	v_lshlrev_b32_e32 v34, 16, v113
	v_and_b32_e32 v35, 0xffff0000, v113
	v_lshlrev_b32_e32 v36, 16, v114
	v_and_b32_e32 v37, 0xffff0000, v114
	v_lshlrev_b32_e32 v38, 16, v115
	v_and_b32_e32 v39, 0xffff0000, v115
	v_fma_f32 v24, v28, v2, v24
	v_fma_f32 v25, v29, v16, v25
	v_fma_f32 v26, v30, v3, v26
	v_fma_f32 v27, v31, v17, v27
	v_fma_f32 v32, v36, v6, v32
	v_fma_f32 v33, v37, v18, v33
	v_fma_f32 v34, v38, v7, v34
	v_fma_f32 v35, v39, v19, v35
	v_add_f32_e32 v24, v24, v32
	v_add_f32_e32 v25, v25, v33
	v_add_f32_e32 v26, v26, v34
	v_add_f32_e32 v27, v27, v35
	v_lshlrev_b32_e32 v40, 16, v116
	v_and_b32_e32 v41, 0xffff0000, v116
	v_lshlrev_b32_e32 v42, 16, v117
	v_and_b32_e32 v43, 0xffff0000, v117
	global_load_dwordx4 v[108:111], v20, s[2:3]
	global_load_dwordx4 v[112:115], v21, s[2:3]
	global_load_dwordx2 v[116:117], v22, s[2:3]
	v_add_u32_e32 v20, 0x1000, v20
	v_add_u32_e32 v21, 0x1000, v21
	v_add_u32_e32 v22, 0x800, v22
	v_mul_f32_e32 v32, 0x3d372713, v40
	v_mul_f32_e32 v33, 0x3d372713, v41
	v_mul_f32_e32 v34, 0x3d372713, v42
	v_mul_f32_e32 v35, 0x3d372713, v43
	v_mul_f32_e32 v32, v32, v40
	v_mul_f32_e32 v33, v33, v41
	v_mul_f32_e32 v34, v34, v42
	v_mul_f32_e32 v35, v35, v43
	v_mov_b32_e32 v36, v40
	v_mov_b32_e32 v37, v41
	v_mov_b32_e32 v38, v42
	v_mov_b32_e32 v39, v43
	v_fmac_f32_e32 v36, v32, v36
	v_fmac_f32_e32 v37, v33, v37
	v_fmac_f32_e32 v38, v34, v38
	v_fmac_f32_e32 v39, v35, v39
	v_mul_f32_e32 v36, 0x3f4c422a, v36
	v_mul_f32_e32 v37, 0x3f4c422a, v37
	v_mul_f32_e32 v38, 0x3f4c422a, v38
	v_mul_f32_e32 v39, 0x3f4c422a, v39
	v_add_f32_e32 v36, v36, v36
	v_add_f32_e32 v37, v37, v37
	v_add_f32_e32 v38, v38, v38
	v_add_f32_e32 v39, v39, v39
	v_mul_f32_e32 v36, 0x3fb8aa3b, v36
	v_mul_f32_e32 v37, 0x3fb8aa3b, v37
	v_mul_f32_e32 v38, 0x3fb8aa3b, v38
	v_mul_f32_e32 v39, 0x3fb8aa3b, v39
	v_exp_f32_e32 v36, v36
	v_exp_f32_e32 v37, v37
	v_exp_f32_e32 v38, v38
	v_exp_f32_e32 v39, v39
	v_add_f32_e32 v36, 1.0, v36
	v_add_f32_e32 v37, 1.0, v37
	v_add_f32_e32 v38, 1.0, v38
	v_add_f32_e32 v39, 1.0, v39
	v_div_scale_f32 v44, s[6:7], v36, v36, 2.0
	v_rcp_f32_e32 v46, v44
	v_div_scale_f32 v45, vcc, 2.0, v36, 2.0
	v_fma_f32 v32, -v44, v46, 1.0
	v_fmac_f32_e32 v46, v32, v46
	v_mul_f32_e32 v47, v45, v46
	v_fma_f32 v32, -v44, v47, v45
	v_fmac_f32_e32 v47, v32, v46
	v_fma_f32 v44, -v44, v47, v45
	v_div_fmas_f32 v44, v44, v46, v47
	v_div_fixup_f32 v36, v44, v36, 2.0
	v_div_scale_f32 v44, s[6:7], v37, v37, 2.0
	v_rcp_f32_e32 v46, v44
	v_div_scale_f32 v45, vcc, 2.0, v37, 2.0
	v_fma_f32 v33, -v44, v46, 1.0
	v_fmac_f32_e32 v46, v33, v46
	v_mul_f32_e32 v47, v45, v46
	v_fma_f32 v33, -v44, v47, v45
	v_fmac_f32_e32 v47, v33, v46
	v_fma_f32 v44, -v44, v47, v45
	v_div_fmas_f32 v44, v44, v46, v47
	v_div_fixup_f32 v37, v44, v37, 2.0
	v_div_scale_f32 v44, s[6:7], v38, v38, 2.0
	v_rcp_f32_e32 v46, v44
	v_div_scale_f32 v45, vcc, 2.0, v38, 2.0
	v_fma_f32 v34, -v44, v46, 1.0
	v_fmac_f32_e32 v46, v34, v46
	v_mul_f32_e32 v47, v45, v46
	v_fma_f32 v34, -v44, v47, v45
	v_fmac_f32_e32 v47, v34, v46
	v_fma_f32 v44, -v44, v47, v45
	v_div_fmas_f32 v44, v44, v46, v47
	v_div_fixup_f32 v38, v44, v38, 2.0
	v_div_scale_f32 v44, s[6:7], v39, v39, 2.0
	v_rcp_f32_e32 v46, v44
	v_div_scale_f32 v45, vcc, 2.0, v39, 2.0
	v_fma_f32 v35, -v44, v46, 1.0
	v_fmac_f32_e32 v46, v35, v46
	v_mul_f32_e32 v47, v45, v46
	v_fma_f32 v35, -v44, v47, v45
	v_fmac_f32_e32 v47, v35, v46
	v_fma_f32 v44, -v44, v47, v45
	v_div_fmas_f32 v44, v44, v46, v47
	v_div_fixup_f32 v39, v44, v39, 2.0
	v_sub_f32_e32 v36, 1.0, v36
	v_sub_f32_e32 v37, 1.0, v37
	v_sub_f32_e32 v38, 1.0, v38
	v_sub_f32_e32 v39, 1.0, v39
	v_add_f32_e32 v36, 1.0, v36
	v_add_f32_e32 v37, 1.0, v37
	v_add_f32_e32 v38, 1.0, v38
	v_add_f32_e32 v39, 1.0, v39
	v_mul_f32_e32 v40, 0.5, v40
	v_mul_f32_e32 v41, 0.5, v41
	v_mul_f32_e32 v42, 0.5, v42
	v_mul_f32_e32 v43, 0.5, v43
	v_mul_f32_e32 v36, v40, v36
	v_mul_f32_e32 v37, v41, v37
	v_mul_f32_e32 v38, v42, v38
	v_mul_f32_e32 v39, v43, v39
	v_mul_f32_e32 v24, v24, v36
	v_mul_f32_e32 v25, v25, v37
	v_mul_f32_e32 v26, v26, v38
	v_mul_f32_e32 v27, v27, v39
	v_cvt_pk_bf16_f32 v28, v24, v25
	v_cvt_pk_bf16_f32 v29, v26, v27
	global_store_dwordx2 v23, v[28:29], s[2:3]
	v_add_u32_e32 v23, 0x1000, v23
	s_waitcnt vmcnt(29)
; __device__ __forceinline__ unsigned pk2(float lo, float hi) { return f2bf(lo) | (f2bf(hi) << 16); }
; __device__ __forceinline__ float gelu_tanh_(float x) { const float u = 0.7978845608028654f * (x + 0.044715f * x * x * x); const float t = 1.f - 2.f / (1.f + __expf(2.f * u)); return 0.5f * x * (1.f + t); }
; __device__ __forceinline__ void phase_attn(const Args& a, const Ctx& c0, int l, bool last) {
;     ...
;         for (int r = 0; r < 32; ++r) {
;             const u32x4 wf = *(const u32x4*)(hf + (size_t)r * 4096), wb = *(const u32x4*)(hb + (size_t)r * 4096); const u32x2 gw2 = *(const u32x2*)(zg + (size_t)r * RW); const f32x4 gr = {bflo(gw2.x), bfhi(gw2.x), bflo(gw2.y), bfhi(gw2.y)};
;             const float h0 = fmaf(bflo(wf.z), cf.x, bflo(wf.x)) + fmaf(bflo(wb.z), cb.x, bflo(wb.x)), h1 = fmaf(bfhi(wf.z), cf.y, bfhi(wf.x)) + fmaf(bfhi(wb.z), cb.y, bfhi(wb.x));
;             const float h2 = fmaf(bflo(wf.w), cf.z, bflo(wf.y)) + fmaf(bflo(wb.w), cb.z, bflo(wb.y)), h3 = fmaf(bfhi(wf.w), cf.w, bfhi(wf.y)) + fmaf(bfhi(wb.w), cb.w, bfhi(wb.y));
;             u32x2 w; w.x = pk2(h0 * gelu_tanh_(gr.x), h1 * gelu_tanh_(gr.y)); w.y = pk2(h2 * gelu_tanh_(gr.z), h3 * gelu_tanh_(gr.w));
;             *(u32x2*)(yo + (size_t)r * DM) = w; }
	v_lshlrev_b32_e32 v24, 16, v120
	v_and_b32_e32 v25, 0xffff0000, v120
	v_lshlrev_b32_e32 v26, 16, v121
	v_and_b32_e32 v27, 0xffff0000, v121
	v_lshlrev_b32_e32 v28, 16, v122
	v_and_b32_e32 v29, 0xffff0000, v122
	v_lshlrev_b32_e32 v30, 16, v123
	v_and_b32_e32 v31, 0xffff0000, v123
	v_lshlrev_b32_e32 v32, 16, v124
	v_and_b32_e32 v33, 0xffff0000, v124
	v_lshlrev_b32_e32 v34, 16, v125
	v_and_b32_e32 v35, 0xffff0000, v125
	v_lshlrev_b32_e32 v36, 16, v126
	v_and_b32_e32 v37, 0xffff0000, v126
	v_lshlrev_b32_e32 v38, 16, v127
	v_and_b32_e32 v39, 0xffff0000, v127
	v_fma_f32 v24, v28, v2, v24
	v_fma_f32 v25, v29, v16, v25
	v_fma_f32 v26, v30, v3, v26
	v_fma_f32 v27, v31, v17, v27
	v_fma_f32 v32, v36, v6, v32
	v_fma_f32 v33, v37, v18, v33
	v_fma_f32 v34, v38, v7, v34
	v_fma_f32 v35, v39, v19, v35
	v_add_f32_e32 v24, v24, v32
	v_add_f32_e32 v25, v25, v33
	v_add_f32_e32 v26, v26, v34
	v_add_f32_e32 v27, v27, v35
	v_lshlrev_b32_e32 v40, 16, v128
	v_and_b32_e32 v41, 0xffff0000, v128
	v_lshlrev_b32_e32 v42, 16, v129
	v_and_b32_e32 v43, 0xffff0000, v129
	global_load_dwordx4 v[120:123], v20, s[2:3]
	global_load_dwordx4 v[124:127], v21, s[2:3]
	global_load_dwordx2 v[128:129], v22, s[2:3]
	v_add_u32_e32 v20, 0x1000, v20
	v_add_u32_e32 v21, 0x1000, v21
	v_add_u32_e32 v22, 0x800, v22
	v_mul_f32_e32 v32, 0x3d372713, v40
	v_mul_f32_e32 v33, 0x3d372713, v41
	v_mul_f32_e32 v34, 0x3d372713, v42
	v_mul_f32_e32 v35, 0x3d372713, v43
	v_mul_f32_e32 v32, v32, v40
	v_mul_f32_e32 v33, v33, v41
	v_mul_f32_e32 v34, v34, v42
	v_mul_f32_e32 v35, v35, v43
	v_mov_b32_e32 v36, v40
	v_mov_b32_e32 v37, v41
	v_mov_b32_e32 v38, v42
	v_mov_b32_e32 v39, v43
	v_fmac_f32_e32 v36, v32, v36
	v_fmac_f32_e32 v37, v33, v37
	v_fmac_f32_e32 v38, v34, v38
	v_fmac_f32_e32 v39, v35, v39
	v_mul_f32_e32 v36, 0x3f4c422a, v36
	v_mul_f32_e32 v37, 0x3f4c422a, v37
	v_mul_f32_e32 v38, 0x3f4c422a, v38
	v_mul_f32_e32 v39, 0x3f4c422a, v39
	v_add_f32_e32 v36, v36, v36
	v_add_f32_e32 v37, v37, v37
	v_add_f32_e32 v38, v38, v38
	v_add_f32_e32 v39, v39, v39
	v_mul_f32_e32 v36, 0x3fb8aa3b, v36
	v_mul_f32_e32 v37, 0x3fb8aa3b, v37
	v_mul_f32_e32 v38, 0x3fb8aa3b, v38
	v_mul_f32_e32 v39, 0x3fb8aa3b, v39
	v_exp_f32_e32 v36, v36
	v_exp_f32_e32 v37, v37
	v_exp_f32_e32 v38, v38
	v_exp_f32_e32 v39, v39
	v_add_f32_e32 v36, 1.0, v36
	v_add_f32_e32 v37, 1.0, v37
	v_add_f32_e32 v38, 1.0, v38
	v_add_f32_e32 v39, 1.0, v39
	v_div_scale_f32 v44, s[6:7], v36, v36, 2.0
	v_rcp_f32_e32 v46, v44
	v_div_scale_f32 v45, vcc, 2.0, v36, 2.0
	v_fma_f32 v32, -v44, v46, 1.0
	v_fmac_f32_e32 v46, v32, v46
	v_mul_f32_e32 v47, v45, v46
	v_fma_f32 v32, -v44, v47, v45
	v_fmac_f32_e32 v47, v32, v46
	v_fma_f32 v44, -v44, v47, v45
	v_div_fmas_f32 v44, v44, v46, v47
	v_div_fixup_f32 v36, v44, v36, 2.0
	v_div_scale_f32 v44, s[6:7], v37, v37, 2.0
	v_rcp_f32_e32 v46, v44
	v_div_scale_f32 v45, vcc, 2.0, v37, 2.0
	v_fma_f32 v33, -v44, v46, 1.0
	v_fmac_f32_e32 v46, v33, v46
	v_mul_f32_e32 v47, v45, v46
	v_fma_f32 v33, -v44, v47, v45
	v_fmac_f32_e32 v47, v33, v46
	v_fma_f32 v44, -v44, v47, v45
	v_div_fmas_f32 v44, v44, v46, v47
	v_div_fixup_f32 v37, v44, v37, 2.0
	v_div_scale_f32 v44, s[6:7], v38, v38, 2.0
	v_rcp_f32_e32 v46, v44
	v_div_scale_f32 v45, vcc, 2.0, v38, 2.0
	v_fma_f32 v34, -v44, v46, 1.0
	v_fmac_f32_e32 v46, v34, v46
	v_mul_f32_e32 v47, v45, v46
	v_fma_f32 v34, -v44, v47, v45
	v_fmac_f32_e32 v47, v34, v46
	v_fma_f32 v44, -v44, v47, v45
	v_div_fmas_f32 v44, v44, v46, v47
	v_div_fixup_f32 v38, v44, v38, 2.0
	v_div_scale_f32 v44, s[6:7], v39, v39, 2.0
	v_rcp_f32_e32 v46, v44
	v_div_scale_f32 v45, vcc, 2.0, v39, 2.0
	v_fma_f32 v35, -v44, v46, 1.0
	v_fmac_f32_e32 v46, v35, v46
	v_mul_f32_e32 v47, v45, v46
	v_fma_f32 v35, -v44, v47, v45
	v_fmac_f32_e32 v47, v35, v46
	v_fma_f32 v44, -v44, v47, v45
	v_div_fmas_f32 v44, v44, v46, v47
	v_div_fixup_f32 v39, v44, v39, 2.0
	v_sub_f32_e32 v36, 1.0, v36
	v_sub_f32_e32 v37, 1.0, v37
	v_sub_f32_e32 v38, 1.0, v38
	v_sub_f32_e32 v39, 1.0, v39
	v_add_f32_e32 v36, 1.0, v36
	v_add_f32_e32 v37, 1.0, v37
	v_add_f32_e32 v38, 1.0, v38
	v_add_f32_e32 v39, 1.0, v39
	v_mul_f32_e32 v40, 0.5, v40
	v_mul_f32_e32 v41, 0.5, v41
	v_mul_f32_e32 v42, 0.5, v42
	v_mul_f32_e32 v43, 0.5, v43
	v_mul_f32_e32 v36, v40, v36
	v_mul_f32_e32 v37, v41, v37
	v_mul_f32_e32 v38, v42, v38
	v_mul_f32_e32 v39, v43, v39
	v_mul_f32_e32 v24, v24, v36
	v_mul_f32_e32 v25, v25, v37
	v_mul_f32_e32 v26, v26, v38
	v_mul_f32_e32 v27, v27, v39
	v_cvt_pk_bf16_f32 v28, v24, v25
	v_cvt_pk_bf16_f32 v29, v26, v27
	global_store_dwordx2 v23, v[28:29], s[2:3]
	v_add_u32_e32 v23, 0x1000, v23
	s_waitcnt vmcnt(29)
; __device__ __forceinline__ unsigned pk2(float lo, float hi) { return f2bf(lo) | (f2bf(hi) << 16); }
; __device__ __forceinline__ float gelu_tanh_(float x) { const float u = 0.7978845608028654f * (x + 0.044715f * x * x * x); const float t = 1.f - 2.f / (1.f + __expf(2.f * u)); return 0.5f * x * (1.f + t); }
; __device__ __forceinline__ void phase_attn(const Args& a, const Ctx& c0, int l, bool last) {
;     ...
;         for (int r = 0; r < 32; ++r) {
;             const u32x4 wf = *(const u32x4*)(hf + (size_t)r * 4096), wb = *(const u32x4*)(hb + (size_t)r * 4096); const u32x2 gw2 = *(const u32x2*)(zg + (size_t)r * RW); const f32x4 gr = {bflo(gw2.x), bfhi(gw2.x), bflo(gw2.y), bfhi(gw2.y)};
;             const float h0 = fmaf(bflo(wf.z), cf.x, bflo(wf.x)) + fmaf(bflo(wb.z), cb.x, bflo(wb.x)), h1 = fmaf(bfhi(wf.z), cf.y, bfhi(wf.x)) + fmaf(bfhi(wb.z), cb.y, bfhi(wb.x));
;             const float h2 = fmaf(bflo(wf.w), cf.z, bflo(wf.y)) + fmaf(bflo(wb.w), cb.z, bflo(wb.y)), h3 = fmaf(bfhi(wf.w), cf.w, bfhi(wf.y)) + fmaf(bfhi(wb.w), cb.w, bfhi(wb.y));
;             u32x2 w; w.x = pk2(h0 * gelu_tanh_(gr.x), h1 * gelu_tanh_(gr.y)); w.y = pk2(h2 * gelu_tanh_(gr.z), h3 * gelu_tanh_(gr.w));
;             *(u32x2*)(yo + (size_t)r * DM) = w; }
	v_lshlrev_b32_e32 v24, 16, v132
	v_and_b32_e32 v25, 0xffff0000, v132
	v_lshlrev_b32_e32 v26, 16, v133
	v_and_b32_e32 v27, 0xffff0000, v133
	v_lshlrev_b32_e32 v28, 16, v134
	v_and_b32_e32 v29, 0xffff0000, v134
	v_lshlrev_b32_e32 v30, 16, v135
	v_and_b32_e32 v31, 0xffff0000, v135
	v_lshlrev_b32_e32 v32, 16, v136
	v_and_b32_e32 v33, 0xffff0000, v136
	v_lshlrev_b32_e32 v34, 16, v137
	v_and_b32_e32 v35, 0xffff0000, v137
	v_lshlrev_b32_e32 v36, 16, v138
	v_and_b32_e32 v37, 0xffff0000, v138
	v_lshlrev_b32_e32 v38, 16, v139
	v_and_b32_e32 v39, 0xffff0000, v139
	v_fma_f32 v24, v28, v2, v24
	v_fma_f32 v25, v29, v16, v25
	v_fma_f32 v26, v30, v3, v26
	v_fma_f32 v27, v31, v17, v27
	v_fma_f32 v32, v36, v6, v32
	v_fma_f32 v33, v37, v18, v33
	v_fma_f32 v34, v38, v7, v34
	v_fma_f32 v35, v39, v19, v35
	v_add_f32_e32 v24, v24, v32
	v_add_f32_e32 v25, v25, v33
	v_add_f32_e32 v26, v26, v34
	v_add_f32_e32 v27, v27, v35
	v_lshlrev_b32_e32 v40, 16, v140
	v_and_b32_e32 v41, 0xffff0000, v140
	v_lshlrev_b32_e32 v42, 16, v141
	v_and_b32_e32 v43, 0xffff0000, v141
	global_load_dwordx4 v[132:135], v20, s[2:3]
	global_load_dwordx4 v[136:139], v21, s[2:3]
	global_load_dwordx2 v[140:141], v22, s[2:3]
	v_add_u32_e32 v20, 0x1000, v20
	v_add_u32_e32 v21, 0x1000, v21
	v_add_u32_e32 v22, 0x800, v22
	v_mul_f32_e32 v32, 0x3d372713, v40
	v_mul_f32_e32 v33, 0x3d372713, v41
	v_mul_f32_e32 v34, 0x3d372713, v42
	v_mul_f32_e32 v35, 0x3d372713, v43
	v_mul_f32_e32 v32, v32, v40
	v_mul_f32_e32 v33, v33, v41
	v_mul_f32_e32 v34, v34, v42
	v_mul_f32_e32 v35, v35, v43
	v_mov_b32_e32 v36, v40
	v_mov_b32_e32 v37, v41
	v_mov_b32_e32 v38, v42
	v_mov_b32_e32 v39, v43
	v_fmac_f32_e32 v36, v32, v36
	v_fmac_f32_e32 v37, v33, v37
	v_fmac_f32_e32 v38, v34, v38
	v_fmac_f32_e32 v39, v35, v39
	v_mul_f32_e32 v36, 0x3f4c422a, v36
	v_mul_f32_e32 v37, 0x3f4c422a, v37
	v_mul_f32_e32 v38, 0x3f4c422a, v38
	v_mul_f32_e32 v39, 0x3f4c422a, v39
	v_add_f32_e32 v36, v36, v36
	v_add_f32_e32 v37, v37, v37
	v_add_f32_e32 v38, v38, v38
	v_add_f32_e32 v39, v39, v39
	v_mul_f32_e32 v36, 0x3fb8aa3b, v36
	v_mul_f32_e32 v37, 0x3fb8aa3b, v37
	v_mul_f32_e32 v38, 0x3fb8aa3b, v38
	v_mul_f32_e32 v39, 0x3fb8aa3b, v39
	v_exp_f32_e32 v36, v36
	v_exp_f32_e32 v37, v37
	v_exp_f32_e32 v38, v38
	v_exp_f32_e32 v39, v39
	v_add_f32_e32 v36, 1.0, v36
	v_add_f32_e32 v37, 1.0, v37
	v_add_f32_e32 v38, 1.0, v38
	v_add_f32_e32 v39, 1.0, v39
	v_div_scale_f32 v44, s[6:7], v36, v36, 2.0
	v_rcp_f32_e32 v46, v44
	v_div_scale_f32 v45, vcc, 2.0, v36, 2.0
	v_fma_f32 v32, -v44, v46, 1.0
	v_fmac_f32_e32 v46, v32, v46
	v_mul_f32_e32 v47, v45, v46
	v_fma_f32 v32, -v44, v47, v45
	v_fmac_f32_e32 v47, v32, v46
	v_fma_f32 v44, -v44, v47, v45
	v_div_fmas_f32 v44, v44, v46, v47
	v_div_fixup_f32 v36, v44, v36, 2.0
	v_div_scale_f32 v44, s[6:7], v37, v37, 2.0
	v_rcp_f32_e32 v46, v44
	v_div_scale_f32 v45, vcc, 2.0, v37, 2.0
	v_fma_f32 v33, -v44, v46, 1.0
	v_fmac_f32_e32 v46, v33, v46
	v_mul_f32_e32 v47, v45, v46
	v_fma_f32 v33, -v44, v47, v45
	v_fmac_f32_e32 v47, v33, v46
	v_fma_f32 v44, -v44, v47, v45
	v_div_fmas_f32 v44, v44, v46, v47
	v_div_fixup_f32 v37, v44, v37, 2.0
	v_div_scale_f32 v44, s[6:7], v38, v38, 2.0
	v_rcp_f32_e32 v46, v44
	v_div_scale_f32 v45, vcc, 2.0, v38, 2.0
	v_fma_f32 v34, -v44, v46, 1.0
	v_fmac_f32_e32 v46, v34, v46
	v_mul_f32_e32 v47, v45, v46
	v_fma_f32 v34, -v44, v47, v45
	v_fmac_f32_e32 v47, v34, v46
	v_fma_f32 v44, -v44, v47, v45
	v_div_fmas_f32 v44, v44, v46, v47
	v_div_fixup_f32 v38, v44, v38, 2.0
	v_div_scale_f32 v44, s[6:7], v39, v39, 2.0
	v_rcp_f32_e32 v46, v44
	v_div_scale_f32 v45, vcc, 2.0, v39, 2.0
	v_fma_f32 v35, -v44, v46, 1.0
	v_fmac_f32_e32 v46, v35, v46
	v_mul_f32_e32 v47, v45, v46
	v_fma_f32 v35, -v44, v47, v45
	v_fmac_f32_e32 v47, v35, v46
	v_fma_f32 v44, -v44, v47, v45
	v_div_fmas_f32 v44, v44, v46, v47
	v_div_fixup_f32 v39, v44, v39, 2.0
	v_sub_f32_e32 v36, 1.0, v36
	v_sub_f32_e32 v37, 1.0, v37
	v_sub_f32_e32 v38, 1.0, v38
	v_sub_f32_e32 v39, 1.0, v39
	v_add_f32_e32 v36, 1.0, v36
	v_add_f32_e32 v37, 1.0, v37
	v_add_f32_e32 v38, 1.0, v38
	v_add_f32_e32 v39, 1.0, v39
	v_mul_f32_e32 v40, 0.5, v40
	v_mul_f32_e32 v41, 0.5, v41
	v_mul_f32_e32 v42, 0.5, v42
	v_mul_f32_e32 v43, 0.5, v43
	v_mul_f32_e32 v36, v40, v36
	v_mul_f32_e32 v37, v41, v37
	v_mul_f32_e32 v38, v42, v38
	v_mul_f32_e32 v39, v43, v39
	v_mul_f32_e32 v24, v24, v36
	v_mul_f32_e32 v25, v25, v37
	v_mul_f32_e32 v26, v26, v38
	v_mul_f32_e32 v27, v27, v39
	v_cvt_pk_bf16_f32 v28, v24, v25
	v_cvt_pk_bf16_f32 v29, v26, v27
	global_store_dwordx2 v23, v[28:29], s[2:3]
	v_add_u32_e32 v23, 0x1000, v23
	s_waitcnt vmcnt(29)
; __device__ __forceinline__ unsigned pk2(float lo, float hi) { return f2bf(lo) | (f2bf(hi) << 16); }
; __device__ __forceinline__ float gelu_tanh_(float x) { const float u = 0.7978845608028654f * (x + 0.044715f * x * x * x); const float t = 1.f - 2.f / (1.f + __expf(2.f * u)); return 0.5f * x * (1.f + t); }
; __device__ __forceinline__ void phase_attn(const Args& a, const Ctx& c0, int l, bool last) {
;     ...
;         for (int r = 0; r < 32; ++r) {
;             const u32x4 wf = *(const u32x4*)(hf + (size_t)r * 4096), wb = *(const u32x4*)(hb + (size_t)r * 4096); const u32x2 gw2 = *(const u32x2*)(zg + (size_t)r * RW); const f32x4 gr = {bflo(gw2.x), bfhi(gw2.x), bflo(gw2.y), bfhi(gw2.y)};
;             const float h0 = fmaf(bflo(wf.z), cf.x, bflo(wf.x)) + fmaf(bflo(wb.z), cb.x, bflo(wb.x)), h1 = fmaf(bfhi(wf.z), cf.y, bfhi(wf.x)) + fmaf(bfhi(wb.z), cb.y, bfhi(wb.x));
;             const float h2 = fmaf(bflo(wf.w), cf.z, bflo(wf.y)) + fmaf(bflo(wb.w), cb.z, bflo(wb.y)), h3 = fmaf(bfhi(wf.w), cf.w, bfhi(wf.y)) + fmaf(bfhi(wb.w), cb.w, bfhi(wb.y));
;             u32x2 w; w.x = pk2(h0 * gelu_tanh_(gr.x), h1 * gelu_tanh_(gr.y)); w.y = pk2(h2 * gelu_tanh_(gr.z), h3 * gelu_tanh_(gr.w));
;             *(u32x2*)(yo + (size_t)r * DM) = w; }
	v_lshlrev_b32_e32 v24, 16, v48
	v_and_b32_e32 v25, 0xffff0000, v48
	v_lshlrev_b32_e32 v26, 16, v49
	v_and_b32_e32 v27, 0xffff0000, v49
	v_lshlrev_b32_e32 v28, 16, v50
	v_and_b32_e32 v29, 0xffff0000, v50
	v_lshlrev_b32_e32 v30, 16, v51
	v_and_b32_e32 v31, 0xffff0000, v51
	v_lshlrev_b32_e32 v32, 16, v52
	v_and_b32_e32 v33, 0xffff0000, v52
	v_lshlrev_b32_e32 v34, 16, v53
	v_and_b32_e32 v35, 0xffff0000, v53
	v_lshlrev_b32_e32 v36, 16, v54
	v_and_b32_e32 v37, 0xffff0000, v54
	v_lshlrev_b32_e32 v38, 16, v55
	v_and_b32_e32 v39, 0xffff0000, v55
	v_fma_f32 v24, v28, v2, v24
	v_fma_f32 v25, v29, v16, v25
	v_fma_f32 v26, v30, v3, v26
	v_fma_f32 v27, v31, v17, v27
	v_fma_f32 v32, v36, v6, v32
	v_fma_f32 v33, v37, v18, v33
	v_fma_f32 v34, v38, v7, v34
	v_fma_f32 v35, v39, v19, v35
	v_add_f32_e32 v24, v24, v32
	v_add_f32_e32 v25, v25, v33
	v_add_f32_e32 v26, v26, v34
	v_add_f32_e32 v27, v27, v35
	v_lshlrev_b32_e32 v40, 16, v56
	v_and_b32_e32 v41, 0xffff0000, v56
	v_lshlrev_b32_e32 v42, 16, v57
	v_and_b32_e32 v43, 0xffff0000, v57
	global_load_dwordx4 v[48:51], v20, s[2:3]
	global_load_dwordx4 v[52:55], v21, s[2:3]
	global_load_dwordx2 v[56:57], v22, s[2:3]
	v_add_u32_e32 v20, 0x1000, v20
	v_add_u32_e32 v21, 0x1000, v21
	v_add_u32_e32 v22, 0x800, v22
	v_mul_f32_e32 v32, 0x3d372713, v40
	v_mul_f32_e32 v33, 0x3d372713, v41
	v_mul_f32_e32 v34, 0x3d372713, v42
	v_mul_f32_e32 v35, 0x3d372713, v43
	v_mul_f32_e32 v32, v32, v40
	v_mul_f32_e32 v33, v33, v41
	v_mul_f32_e32 v34, v34, v42
	v_mul_f32_e32 v35, v35, v43
	v_mov_b32_e32 v36, v40
	v_mov_b32_e32 v37, v41
	v_mov_b32_e32 v38, v42
	v_mov_b32_e32 v39, v43
	v_fmac_f32_e32 v36, v32, v36
	v_fmac_f32_e32 v37, v33, v37
	v_fmac_f32_e32 v38, v34, v38
	v_fmac_f32_e32 v39, v35, v39
	v_mul_f32_e32 v36, 0x3f4c422a, v36
	v_mul_f32_e32 v37, 0x3f4c422a, v37
	v_mul_f32_e32 v38, 0x3f4c422a, v38
	v_mul_f32_e32 v39, 0x3f4c422a, v39
	v_add_f32_e32 v36, v36, v36
	v_add_f32_e32 v37, v37, v37
	v_add_f32_e32 v38, v38, v38
	v_add_f32_e32 v39, v39, v39
	v_mul_f32_e32 v36, 0x3fb8aa3b, v36
	v_mul_f32_e32 v37, 0x3fb8aa3b, v37
	v_mul_f32_e32 v38, 0x3fb8aa3b, v38
	v_mul_f32_e32 v39, 0x3fb8aa3b, v39
	v_exp_f32_e32 v36, v36
	v_exp_f32_e32 v37, v37
	v_exp_f32_e32 v38, v38
	v_exp_f32_e32 v39, v39
	v_add_f32_e32 v36, 1.0, v36
	v_add_f32_e32 v37, 1.0, v37
	v_add_f32_e32 v38, 1.0, v38
	v_add_f32_e32 v39, 1.0, v39
	v_div_scale_f32 v44, s[6:7], v36, v36, 2.0
	v_rcp_f32_e32 v46, v44
	v_div_scale_f32 v45, vcc, 2.0, v36, 2.0
	v_fma_f32 v32, -v44, v46, 1.0
	v_fmac_f32_e32 v46, v32, v46
	v_mul_f32_e32 v47, v45, v46
	v_fma_f32 v32, -v44, v47, v45
	v_fmac_f32_e32 v47, v32, v46
	v_fma_f32 v44, -v44, v47, v45
	v_div_fmas_f32 v44, v44, v46, v47
	v_div_fixup_f32 v36, v44, v36, 2.0
	v_div_scale_f32 v44, s[6:7], v37, v37, 2.0
	v_rcp_f32_e32 v46, v44
	v_div_scale_f32 v45, vcc, 2.0, v37, 2.0
	v_fma_f32 v33, -v44, v46, 1.0
	v_fmac_f32_e32 v46, v33, v46
	v_mul_f32_e32 v47, v45, v46
	v_fma_f32 v33, -v44, v47, v45
	v_fmac_f32_e32 v47, v33, v46
	v_fma_f32 v44, -v44, v47, v45
	v_div_fmas_f32 v44, v44, v46, v47
	v_div_fixup_f32 v37, v44, v37, 2.0
	v_div_scale_f32 v44, s[6:7], v38, v38, 2.0
	v_rcp_f32_e32 v46, v44
	v_div_scale_f32 v45, vcc, 2.0, v38, 2.0
	v_fma_f32 v34, -v44, v46, 1.0
	v_fmac_f32_e32 v46, v34, v46
	v_mul_f32_e32 v47, v45, v46
	v_fma_f32 v34, -v44, v47, v45
	v_fmac_f32_e32 v47, v34, v46
	v_fma_f32 v44, -v44, v47, v45
	v_div_fmas_f32 v44, v44, v46, v47
	v_div_fixup_f32 v38, v44, v38, 2.0
	v_div_scale_f32 v44, s[6:7], v39, v39, 2.0
	v_rcp_f32_e32 v46, v44
	v_div_scale_f32 v45, vcc, 2.0, v39, 2.0
	v_fma_f32 v35, -v44, v46, 1.0
	v_fmac_f32_e32 v46, v35, v46
	v_mul_f32_e32 v47, v45, v46
	v_fma_f32 v35, -v44, v47, v45
	v_fmac_f32_e32 v47, v35, v46
	v_fma_f32 v44, -v44, v47, v45
	v_div_fmas_f32 v44, v44, v46, v47
	v_div_fixup_f32 v39, v44, v39, 2.0
	v_sub_f32_e32 v36, 1.0, v36
	v_sub_f32_e32 v37, 1.0, v37
	v_sub_f32_e32 v38, 1.0, v38
	v_sub_f32_e32 v39, 1.0, v39
	v_add_f32_e32 v36, 1.0, v36
	v_add_f32_e32 v37, 1.0, v37
	v_add_f32_e32 v38, 1.0, v38
	v_add_f32_e32 v39, 1.0, v39
	v_mul_f32_e32 v40, 0.5, v40
	v_mul_f32_e32 v41, 0.5, v41
	v_mul_f32_e32 v42, 0.5, v42
	v_mul_f32_e32 v43, 0.5, v43
	v_mul_f32_e32 v36, v40, v36
	v_mul_f32_e32 v37, v41, v37
	v_mul_f32_e32 v38, v42, v38
	v_mul_f32_e32 v39, v43, v39
	v_mul_f32_e32 v24, v24, v36
	v_mul_f32_e32 v25, v25, v37
	v_mul_f32_e32 v26, v26, v38
	v_mul_f32_e32 v27, v27, v39
	v_cvt_pk_bf16_f32 v28, v24, v25
	v_cvt_pk_bf16_f32 v29, v26, v27
	global_store_dwordx2 v23, v[28:29], s[2:3]
	v_add_u32_e32 v23, 0x1000, v23
	s_waitcnt vmcnt(29)
; __device__ __forceinline__ unsigned pk2(float lo, float hi) { return f2bf(lo) | (f2bf(hi) << 16); }
; __device__ __forceinline__ float gelu_tanh_(float x) { const float u = 0.7978845608028654f * (x + 0.044715f * x * x * x); const float t = 1.f - 2.f / (1.f + __expf(2.f * u)); return 0.5f * x * (1.f + t); }
; __device__ __forceinline__ void phase_attn(const Args& a, const Ctx& c0, int l, bool last) {
;     ...
;         for (int r = 0; r < 32; ++r) {
;             const u32x4 wf = *(const u32x4*)(hf + (size_t)r * 4096), wb = *(const u32x4*)(hb + (size_t)r * 4096); const u32x2 gw2 = *(const u32x2*)(zg + (size_t)r * RW); const f32x4 gr = {bflo(gw2.x), bfhi(gw2.x), bflo(gw2.y), bfhi(gw2.y)};
;             const float h0 = fmaf(bflo(wf.z), cf.x, bflo(wf.x)) + fmaf(bflo(wb.z), cb.x, bflo(wb.x)), h1 = fmaf(bfhi(wf.z), cf.y, bfhi(wf.x)) + fmaf(bfhi(wb.z), cb.y, bfhi(wb.x));
;             const float h2 = fmaf(bflo(wf.w), cf.z, bflo(wf.y)) + fmaf(bflo(wb.w), cb.z, bflo(wb.y)), h3 = fmaf(bfhi(wf.w), cf.w, bfhi(wf.y)) + fmaf(bfhi(wb.w), cb.w, bfhi(wb.y));
;             u32x2 w; w.x = pk2(h0 * gelu_tanh_(gr.x), h1 * gelu_tanh_(gr.y)); w.y = pk2(h2 * gelu_tanh_(gr.z), h3 * gelu_tanh_(gr.w));
;             *(u32x2*)(yo + (size_t)r * DM) = w; }
	v_lshlrev_b32_e32 v24, 16, v60
	v_and_b32_e32 v25, 0xffff0000, v60
	v_lshlrev_b32_e32 v26, 16, v61
	v_and_b32_e32 v27, 0xffff0000, v61
	v_lshlrev_b32_e32 v28, 16, v62
	v_and_b32_e32 v29, 0xffff0000, v62
	v_lshlrev_b32_e32 v30, 16, v63
	v_and_b32_e32 v31, 0xffff0000, v63
	v_lshlrev_b32_e32 v32, 16, v64
	v_and_b32_e32 v33, 0xffff0000, v64
	v_lshlrev_b32_e32 v34, 16, v65
	v_and_b32_e32 v35, 0xffff0000, v65
	v_lshlrev_b32_e32 v36, 16, v66
	v_and_b32_e32 v37, 0xffff0000, v66
	v_lshlrev_b32_e32 v38, 16, v67
	v_and_b32_e32 v39, 0xffff0000, v67
	v_fma_f32 v24, v28, v2, v24
	v_fma_f32 v25, v29, v16, v25
	v_fma_f32 v26, v30, v3, v26
	v_fma_f32 v27, v31, v17, v27
	v_fma_f32 v32, v36, v6, v32
	v_fma_f32 v33, v37, v18, v33
	v_fma_f32 v34, v38, v7, v34
	v_fma_f32 v35, v39, v19, v35
	v_add_f32_e32 v24, v24, v32
	v_add_f32_e32 v25, v25, v33
	v_add_f32_e32 v26, v26, v34
	v_add_f32_e32 v27, v27, v35
	v_lshlrev_b32_e32 v40, 16, v68
	v_and_b32_e32 v41, 0xffff0000, v68
	v_lshlrev_b32_e32 v42, 16, v69
	v_and_b32_e32 v43, 0xffff0000, v69
	global_load_dwordx4 v[60:63], v20, s[2:3]
	global_load_dwordx4 v[64:67], v21, s[2:3]
	global_load_dwordx2 v[68:69], v22, s[2:3]
	v_add_u32_e32 v20, 0x1000, v20
	v_add_u32_e32 v21, 0x1000, v21
	v_add_u32_e32 v22, 0x800, v22
	v_mul_f32_e32 v32, 0x3d372713, v40
	v_mul_f32_e32 v33, 0x3d372713, v41
	v_mul_f32_e32 v34, 0x3d372713, v42
	v_mul_f32_e32 v35, 0x3d372713, v43
	v_mul_f32_e32 v32, v32, v40
	v_mul_f32_e32 v33, v33, v41
	v_mul_f32_e32 v34, v34, v42
	v_mul_f32_e32 v35, v35, v43
	v_mov_b32_e32 v36, v40
	v_mov_b32_e32 v37, v41
	v_mov_b32_e32 v38, v42
	v_mov_b32_e32 v39, v43
	v_fmac_f32_e32 v36, v32, v36
	v_fmac_f32_e32 v37, v33, v37
	v_fmac_f32_e32 v38, v34, v38
	v_fmac_f32_e32 v39, v35, v39
	v_mul_f32_e32 v36, 0x3f4c422a, v36
	v_mul_f32_e32 v37, 0x3f4c422a, v37
	v_mul_f32_e32 v38, 0x3f4c422a, v38
	v_mul_f32_e32 v39, 0x3f4c422a, v39
	v_add_f32_e32 v36, v36, v36
	v_add_f32_e32 v37, v37, v37
	v_add_f32_e32 v38, v38, v38
	v_add_f32_e32 v39, v39, v39
	v_mul_f32_e32 v36, 0x3fb8aa3b, v36
	v_mul_f32_e32 v37, 0x3fb8aa3b, v37
	v_mul_f32_e32 v38, 0x3fb8aa3b, v38
	v_mul_f32_e32 v39, 0x3fb8aa3b, v39
	v_exp_f32_e32 v36, v36
	v_exp_f32_e32 v37, v37
	v_exp_f32_e32 v38, v38
	v_exp_f32_e32 v39, v39
	v_add_f32_e32 v36, 1.0, v36
	v_add_f32_e32 v37, 1.0, v37
	v_add_f32_e32 v38, 1.0, v38
	v_add_f32_e32 v39, 1.0, v39
	v_div_scale_f32 v44, s[6:7], v36, v36, 2.0
	v_rcp_f32_e32 v46, v44
	v_div_scale_f32 v45, vcc, 2.0, v36, 2.0
	v_fma_f32 v32, -v44, v46, 1.0
	v_fmac_f32_e32 v46, v32, v46
	v_mul_f32_e32 v47, v45, v46
	v_fma_f32 v32, -v44, v47, v45
	v_fmac_f32_e32 v47, v32, v46
	v_fma_f32 v44, -v44, v47, v45
	v_div_fmas_f32 v44, v44, v46, v47
	v_div_fixup_f32 v36, v44, v36, 2.0
	v_div_scale_f32 v44, s[6:7], v37, v37, 2.0
	v_rcp_f32_e32 v46, v44
	v_div_scale_f32 v45, vcc, 2.0, v37, 2.0
	v_fma_f32 v33, -v44, v46, 1.0
	v_fmac_f32_e32 v46, v33, v46
	v_mul_f32_e32 v47, v45, v46
	v_fma_f32 v33, -v44, v47, v45
	v_fmac_f32_e32 v47, v33, v46
	v_fma_f32 v44, -v44, v47, v45
	v_div_fmas_f32 v44, v44, v46, v47
	v_div_fixup_f32 v37, v44, v37, 2.0
	v_div_scale_f32 v44, s[6:7], v38, v38, 2.0
	v_rcp_f32_e32 v46, v44
	v_div_scale_f32 v45, vcc, 2.0, v38, 2.0
	v_fma_f32 v34, -v44, v46, 1.0
	v_fmac_f32_e32 v46, v34, v46
	v_mul_f32_e32 v47, v45, v46
	v_fma_f32 v34, -v44, v47, v45
	v_fmac_f32_e32 v47, v34, v46
	v_fma_f32 v44, -v44, v47, v45
	v_div_fmas_f32 v44, v44, v46, v47
	v_div_fixup_f32 v38, v44, v38, 2.0
	v_div_scale_f32 v44, s[6:7], v39, v39, 2.0
	v_rcp_f32_e32 v46, v44
	v_div_scale_f32 v45, vcc, 2.0, v39, 2.0
	v_fma_f32 v35, -v44, v46, 1.0
	v_fmac_f32_e32 v46, v35, v46
	v_mul_f32_e32 v47, v45, v46
	v_fma_f32 v35, -v44, v47, v45
	v_fmac_f32_e32 v47, v35, v46
	v_fma_f32 v44, -v44, v47, v45
	v_div_fmas_f32 v44, v44, v46, v47
	v_div_fixup_f32 v39, v44, v39, 2.0
	v_sub_f32_e32 v36, 1.0, v36
	v_sub_f32_e32 v37, 1.0, v37
	v_sub_f32_e32 v38, 1.0, v38
	v_sub_f32_e32 v39, 1.0, v39
	v_add_f32_e32 v36, 1.0, v36
	v_add_f32_e32 v37, 1.0, v37
	v_add_f32_e32 v38, 1.0, v38
	v_add_f32_e32 v39, 1.0, v39
	v_mul_f32_e32 v40, 0.5, v40
	v_mul_f32_e32 v41, 0.5, v41
	v_mul_f32_e32 v42, 0.5, v42
	v_mul_f32_e32 v43, 0.5, v43
	v_mul_f32_e32 v36, v40, v36
	v_mul_f32_e32 v37, v41, v37
	v_mul_f32_e32 v38, v42, v38
	v_mul_f32_e32 v39, v43, v39
	v_mul_f32_e32 v24, v24, v36
	v_mul_f32_e32 v25, v25, v37
	v_mul_f32_e32 v26, v26, v38
	v_mul_f32_e32 v27, v27, v39
	v_cvt_pk_bf16_f32 v28, v24, v25
	v_cvt_pk_bf16_f32 v29, v26, v27
	global_store_dwordx2 v23, v[28:29], s[2:3]
	v_add_u32_e32 v23, 0x1000, v23
	s_waitcnt vmcnt(29)
; __device__ __forceinline__ unsigned pk2(float lo, float hi) { return f2bf(lo) | (f2bf(hi) << 16); }
; __device__ __forceinline__ float gelu_tanh_(float x) { const float u = 0.7978845608028654f * (x + 0.044715f * x * x * x); const float t = 1.f - 2.f / (1.f + __expf(2.f * u)); return 0.5f * x * (1.f + t); }
; __device__ __forceinline__ void phase_attn(const Args& a, const Ctx& c0, int l, bool last) {
;     ...
;         for (int r = 0; r < 32; ++r) {
;             const u32x4 wf = *(const u32x4*)(hf + (size_t)r * 4096), wb = *(const u32x4*)(hb + (size_t)r * 4096); const u32x2 gw2 = *(const u32x2*)(zg + (size_t)r * RW); const f32x4 gr = {bflo(gw2.x), bfhi(gw2.x), bflo(gw2.y), bfhi(gw2.y)};
;             const float h0 = fmaf(bflo(wf.z), cf.x, bflo(wf.x)) + fmaf(bflo(wb.z), cb.x, bflo(wb.x)), h1 = fmaf(bfhi(wf.z), cf.y, bfhi(wf.x)) + fmaf(bfhi(wb.z), cb.y, bfhi(wb.x));
;             const float h2 = fmaf(bflo(wf.w), cf.z, bflo(wf.y)) + fmaf(bflo(wb.w), cb.z, bflo(wb.y)), h3 = fmaf(bfhi(wf.w), cf.w, bfhi(wf.y)) + fmaf(bfhi(wb.w), cb.w, bfhi(wb.y));
;             u32x2 w; w.x = pk2(h0 * gelu_tanh_(gr.x), h1 * gelu_tanh_(gr.y)); w.y = pk2(h2 * gelu_tanh_(gr.z), h3 * gelu_tanh_(gr.w));
;             *(u32x2*)(yo + (size_t)r * DM) = w; }
	v_lshlrev_b32_e32 v24, 16, v72
	v_and_b32_e32 v25, 0xffff0000, v72
	v_lshlrev_b32_e32 v26, 16, v73
	v_and_b32_e32 v27, 0xffff0000, v73
	v_lshlrev_b32_e32 v28, 16, v74
	v_and_b32_e32 v29, 0xffff0000, v74
	v_lshlrev_b32_e32 v30, 16, v75
	v_and_b32_e32 v31, 0xffff0000, v75
	v_lshlrev_b32_e32 v32, 16, v76
	v_and_b32_e32 v33, 0xffff0000, v76
	v_lshlrev_b32_e32 v34, 16, v77
	v_and_b32_e32 v35, 0xffff0000, v77
	v_lshlrev_b32_e32 v36, 16, v78
	v_and_b32_e32 v37, 0xffff0000, v78
	v_lshlrev_b32_e32 v38, 16, v79
	v_and_b32_e32 v39, 0xffff0000, v79
	v_fma_f32 v24, v28, v2, v24
	v_fma_f32 v25, v29, v16, v25
	v_fma_f32 v26, v30, v3, v26
	v_fma_f32 v27, v31, v17, v27
	v_fma_f32 v32, v36, v6, v32
	v_fma_f32 v33, v37, v18, v33
	v_fma_f32 v34, v38, v7, v34
	v_fma_f32 v35, v39, v19, v35
	v_add_f32_e32 v24, v24, v32
	v_add_f32_e32 v25, v25, v33
	v_add_f32_e32 v26, v26, v34
	v_add_f32_e32 v27, v27, v35
	v_lshlrev_b32_e32 v40, 16, v80
	v_and_b32_e32 v41, 0xffff0000, v80
	v_lshlrev_b32_e32 v42, 16, v81
	v_and_b32_e32 v43, 0xffff0000, v81
	global_load_dwordx4 v[72:75], v20, s[2:3]
	global_load_dwordx4 v[76:79], v21, s[2:3]
	global_load_dwordx2 v[80:81], v22, s[2:3]
	v_add_u32_e32 v20, 0x1000, v20
	v_add_u32_e32 v21, 0x1000, v21
	v_add_u32_e32 v22, 0x800, v22
	v_mul_f32_e32 v32, 0x3d372713, v40
	v_mul_f32_e32 v33, 0x3d372713, v41
	v_mul_f32_e32 v34, 0x3d372713, v42
	v_mul_f32_e32 v35, 0x3d372713, v43
	v_mul_f32_e32 v32, v32, v40
	v_mul_f32_e32 v33, v33, v41
	v_mul_f32_e32 v34, v34, v42
	v_mul_f32_e32 v35, v35, v43
	v_mov_b32_e32 v36, v40
	v_mov_b32_e32 v37, v41
	v_mov_b32_e32 v38, v42
	v_mov_b32_e32 v39, v43
	v_fmac_f32_e32 v36, v32, v36
	v_fmac_f32_e32 v37, v33, v37
	v_fmac_f32_e32 v38, v34, v38
	v_fmac_f32_e32 v39, v35, v39
	v_mul_f32_e32 v36, 0x3f4c422a, v36
	v_mul_f32_e32 v37, 0x3f4c422a, v37
	v_mul_f32_e32 v38, 0x3f4c422a, v38
	v_mul_f32_e32 v39, 0x3f4c422a, v39
	v_add_f32_e32 v36, v36, v36
	v_add_f32_e32 v37, v37, v37
	v_add_f32_e32 v38, v38, v38
	v_add_f32_e32 v39, v39, v39
	v_mul_f32_e32 v36, 0x3fb8aa3b, v36
	v_mul_f32_e32 v37, 0x3fb8aa3b, v37
	v_mul_f32_e32 v38, 0x3fb8aa3b, v38
	v_mul_f32_e32 v39, 0x3fb8aa3b, v39
	v_exp_f32_e32 v36, v36
	v_exp_f32_e32 v37, v37
	v_exp_f32_e32 v38, v38
	v_exp_f32_e32 v39, v39
	v_add_f32_e32 v36, 1.0, v36
	v_add_f32_e32 v37, 1.0, v37
	v_add_f32_e32 v38, 1.0, v38
	v_add_f32_e32 v39, 1.0, v39
	v_div_scale_f32 v44, s[6:7], v36, v36, 2.0
	v_rcp_f32_e32 v46, v44
	v_div_scale_f32 v45, vcc, 2.0, v36, 2.0
	v_fma_f32 v32, -v44, v46, 1.0
	v_fmac_f32_e32 v46, v32, v46
	v_mul_f32_e32 v47, v45, v46
	v_fma_f32 v32, -v44, v47, v45
	v_fmac_f32_e32 v47, v32, v46
	v_fma_f32 v44, -v44, v47, v45
	v_div_fmas_f32 v44, v44, v46, v47
	v_div_fixup_f32 v36, v44, v36, 2.0
	v_div_scale_f32 v44, s[6:7], v37, v37, 2.0
	v_rcp_f32_e32 v46, v44
	v_div_scale_f32 v45, vcc, 2.0, v37, 2.0
	v_fma_f32 v33, -v44, v46, 1.0
	v_fmac_f32_e32 v46, v33, v46
	v_mul_f32_e32 v47, v45, v46
	v_fma_f32 v33, -v44, v47, v45
	v_fmac_f32_e32 v47, v33, v46
	v_fma_f32 v44, -v44, v47, v45
	v_div_fmas_f32 v44, v44, v46, v47
	v_div_fixup_f32 v37, v44, v37, 2.0
	v_div_scale_f32 v44, s[6:7], v38, v38, 2.0
	v_rcp_f32_e32 v46, v44
	v_div_scale_f32 v45, vcc, 2.0, v38, 2.0
	v_fma_f32 v34, -v44, v46, 1.0
	v_fmac_f32_e32 v46, v34, v46
	v_mul_f32_e32 v47, v45, v46
	v_fma_f32 v34, -v44, v47, v45
	v_fmac_f32_e32 v47, v34, v46
	v_fma_f32 v44, -v44, v47, v45
	v_div_fmas_f32 v44, v44, v46, v47
	v_div_fixup_f32 v38, v44, v38, 2.0
	v_div_scale_f32 v44, s[6:7], v39, v39, 2.0
	v_rcp_f32_e32 v46, v44
	v_div_scale_f32 v45, vcc, 2.0, v39, 2.0
	v_fma_f32 v35, -v44, v46, 1.0
	v_fmac_f32_e32 v46, v35, v46
	v_mul_f32_e32 v47, v45, v46
	v_fma_f32 v35, -v44, v47, v45
	v_fmac_f32_e32 v47, v35, v46
	v_fma_f32 v44, -v44, v47, v45
	v_div_fmas_f32 v44, v44, v46, v47
	v_div_fixup_f32 v39, v44, v39, 2.0
	v_sub_f32_e32 v36, 1.0, v36
	v_sub_f32_e32 v37, 1.0, v37
	v_sub_f32_e32 v38, 1.0, v38
	v_sub_f32_e32 v39, 1.0, v39
	v_add_f32_e32 v36, 1.0, v36
	v_add_f32_e32 v37, 1.0, v37
	v_add_f32_e32 v38, 1.0, v38
	v_add_f32_e32 v39, 1.0, v39
	v_mul_f32_e32 v40, 0.5, v40
	v_mul_f32_e32 v41, 0.5, v41
	v_mul_f32_e32 v42, 0.5, v42
	v_mul_f32_e32 v43, 0.5, v43
	v_mul_f32_e32 v36, v40, v36
	v_mul_f32_e32 v37, v41, v37
	v_mul_f32_e32 v38, v42, v38
	v_mul_f32_e32 v39, v43, v39
	v_mul_f32_e32 v24, v24, v36
	v_mul_f32_e32 v25, v25, v37
	v_mul_f32_e32 v26, v26, v38
	v_mul_f32_e32 v27, v27, v39
	v_cvt_pk_bf16_f32 v28, v24, v25
	v_cvt_pk_bf16_f32 v29, v26, v27
	global_store_dwordx2 v23, v[28:29], s[2:3]
	v_add_u32_e32 v23, 0x1000, v23
	s_waitcnt vmcnt(29)
; __device__ __forceinline__ unsigned pk2(float lo, float hi) { return f2bf(lo) | (f2bf(hi) << 16); }
; __device__ __forceinline__ float gelu_tanh_(float x) { const float u = 0.7978845608028654f * (x + 0.044715f * x * x * x); const float t = 1.f - 2.f / (1.f + __expf(2.f * u)); return 0.5f * x * (1.f + t); }
; __device__ __forceinline__ void phase_attn(const Args& a, const Ctx& c0, int l, bool last) {
;     ...
;         for (int r = 0; r < 32; ++r) {
;             const u32x4 wf = *(const u32x4*)(hf + (size_t)r * 4096), wb = *(const u32x4*)(hb + (size_t)r * 4096); const u32x2 gw2 = *(const u32x2*)(zg + (size_t)r * RW); const f32x4 gr = {bflo(gw2.x), bfhi(gw2.x), bflo(gw2.y), bfhi(gw2.y)};
;             const float h0 = fmaf(bflo(wf.z), cf.x, bflo(wf.x)) + fmaf(bflo(wb.z), cb.x, bflo(wb.x)), h1 = fmaf(bfhi(wf.z), cf.y, bfhi(wf.x)) + fmaf(bfhi(wb.z), cb.y, bfhi(wb.x));
;             const float h2 = fmaf(bflo(wf.w), cf.z, bflo(wf.y)) + fmaf(bflo(wb.w), cb.z, bflo(wb.y)), h3 = fmaf(bfhi(wf.w), cf.w, bfhi(wf.y)) + fmaf(bfhi(wb.w), cb.w, bfhi(wb.y));
;             u32x2 w; w.x = pk2(h0 * gelu_tanh_(gr.x), h1 * gelu_tanh_(gr.y)); w.y = pk2(h2 * gelu_tanh_(gr.z), h3 * gelu_tanh_(gr.w));
;             *(u32x2*)(yo + (size_t)r * DM) = w; }
	v_lshlrev_b32_e32 v24, 16, v84
	v_and_b32_e32 v25, 0xffff0000, v84
	v_lshlrev_b32_e32 v26, 16, v85
	v_and_b32_e32 v27, 0xffff0000, v85
	v_lshlrev_b32_e32 v28, 16, v86
	v_and_b32_e32 v29, 0xffff0000, v86
	v_lshlrev_b32_e32 v30, 16, v87
	v_and_b32_e32 v31, 0xffff0000, v87
	v_lshlrev_b32_e32 v32, 16, v88
	v_and_b32_e32 v33, 0xffff0000, v88
	v_lshlrev_b32_e32 v34, 16, v89
	v_and_b32_e32 v35, 0xffff0000, v89
	v_lshlrev_b32_e32 v36, 16, v90
	v_and_b32_e32 v37, 0xffff0000, v90
	v_lshlrev_b32_e32 v38, 16, v91
	v_and_b32_e32 v39, 0xffff0000, v91
	v_fma_f32 v24, v28, v2, v24
	v_fma_f32 v25, v29, v16, v25
	v_fma_f32 v26, v30, v3, v26
	v_fma_f32 v27, v31, v17, v27
	v_fma_f32 v32, v36, v6, v32
	v_fma_f32 v33, v37, v18, v33
	v_fma_f32 v34, v38, v7, v34
	v_fma_f32 v35, v39, v19, v35
	v_add_f32_e32 v24, v24, v32
	v_add_f32_e32 v25, v25, v33
	v_add_f32_e32 v26, v26, v34
	v_add_f32_e32 v27, v27, v35
	v_lshlrev_b32_e32 v40, 16, v92
	v_and_b32_e32 v41, 0xffff0000, v92
	v_lshlrev_b32_e32 v42, 16, v93
	v_and_b32_e32 v43, 0xffff0000, v93
	global_load_dwordx4 v[84:87], v20, s[2:3]
	global_load_dwordx4 v[88:91], v21, s[2:3]
	global_load_dwordx2 v[92:93], v22, s[2:3]
	v_add_u32_e32 v20, 0x1000, v20
	v_add_u32_e32 v21, 0x1000, v21
	v_add_u32_e32 v22, 0x800, v22
	v_mul_f32_e32 v32, 0x3d372713, v40
	v_mul_f32_e32 v33, 0x3d372713, v41
	v_mul_f32_e32 v34, 0x3d372713, v42
	v_mul_f32_e32 v35, 0x3d372713, v43
	v_mul_f32_e32 v32, v32, v40
	v_mul_f32_e32 v33, v33, v41
	v_mul_f32_e32 v34, v34, v42
	v_mul_f32_e32 v35, v35, v43
	v_mov_b32_e32 v36, v40
	v_mov_b32_e32 v37, v41
	v_mov_b32_e32 v38, v42
	v_mov_b32_e32 v39, v43
	v_fmac_f32_e32 v36, v32, v36
	v_fmac_f32_e32 v37, v33, v37
	v_fmac_f32_e32 v38, v34, v38
	v_fmac_f32_e32 v39, v35, v39
	v_mul_f32_e32 v36, 0x3f4c422a, v36
	v_mul_f32_e32 v37, 0x3f4c422a, v37
	v_mul_f32_e32 v38, 0x3f4c422a, v38
	v_mul_f32_e32 v39, 0x3f4c422a, v39
	v_add_f32_e32 v36, v36, v36
	v_add_f32_e32 v37, v37, v37
	v_add_f32_e32 v38, v38, v38
	v_add_f32_e32 v39, v39, v39
	v_mul_f32_e32 v36, 0x3fb8aa3b, v36
	v_mul_f32_e32 v37, 0x3fb8aa3b, v37
	v_mul_f32_e32 v38, 0x3fb8aa3b, v38
	v_mul_f32_e32 v39, 0x3fb8aa3b, v39
	v_exp_f32_e32 v36, v36
	v_exp_f32_e32 v37, v37
	v_exp_f32_e32 v38, v38
	v_exp_f32_e32 v39, v39
	v_add_f32_e32 v36, 1.0, v36
	v_add_f32_e32 v37, 1.0, v37
	v_add_f32_e32 v38, 1.0, v38
	v_add_f32_e32 v39, 1.0, v39
	v_div_scale_f32 v44, s[6:7], v36, v36, 2.0
	v_rcp_f32_e32 v46, v44
	v_div_scale_f32 v45, vcc, 2.0, v36, 2.0
	v_fma_f32 v32, -v44, v46, 1.0
	v_fmac_f32_e32 v46, v32, v46
	v_mul_f32_e32 v47, v45, v46
	v_fma_f32 v32, -v44, v47, v45
	v_fmac_f32_e32 v47, v32, v46
	v_fma_f32 v44, -v44, v47, v45
	v_div_fmas_f32 v44, v44, v46, v47
	v_div_fixup_f32 v36, v44, v36, 2.0
	v_div_scale_f32 v44, s[6:7], v37, v37, 2.0
	v_rcp_f32_e32 v46, v44
	v_div_scale_f32 v45, vcc, 2.0, v37, 2.0
	v_fma_f32 v33, -v44, v46, 1.0
	v_fmac_f32_e32 v46, v33, v46
	v_mul_f32_e32 v47, v45, v46
	v_fma_f32 v33, -v44, v47, v45
	v_fmac_f32_e32 v47, v33, v46
	v_fma_f32 v44, -v44, v47, v45
	v_div_fmas_f32 v44, v44, v46, v47
	v_div_fixup_f32 v37, v44, v37, 2.0
	v_div_scale_f32 v44, s[6:7], v38, v38, 2.0
	v_rcp_f32_e32 v46, v44
	v_div_scale_f32 v45, vcc, 2.0, v38, 2.0
	v_fma_f32 v34, -v44, v46, 1.0
	v_fmac_f32_e32 v46, v34, v46
	v_mul_f32_e32 v47, v45, v46
	v_fma_f32 v34, -v44, v47, v45
	v_fmac_f32_e32 v47, v34, v46
	v_fma_f32 v44, -v44, v47, v45
	v_div_fmas_f32 v44, v44, v46, v47
	v_div_fixup_f32 v38, v44, v38, 2.0
	v_div_scale_f32 v44, s[6:7], v39, v39, 2.0
	v_rcp_f32_e32 v46, v44
	v_div_scale_f32 v45, vcc, 2.0, v39, 2.0
	v_fma_f32 v35, -v44, v46, 1.0
	v_fmac_f32_e32 v46, v35, v46
	v_mul_f32_e32 v47, v45, v46
	v_fma_f32 v35, -v44, v47, v45
	v_fmac_f32_e32 v47, v35, v46
	v_fma_f32 v44, -v44, v47, v45
	v_div_fmas_f32 v44, v44, v46, v47
	v_div_fixup_f32 v39, v44, v39, 2.0
	v_sub_f32_e32 v36, 1.0, v36
	v_sub_f32_e32 v37, 1.0, v37
	v_sub_f32_e32 v38, 1.0, v38
	v_sub_f32_e32 v39, 1.0, v39
	v_add_f32_e32 v36, 1.0, v36
	v_add_f32_e32 v37, 1.0, v37
	v_add_f32_e32 v38, 1.0, v38
	v_add_f32_e32 v39, 1.0, v39
	v_mul_f32_e32 v40, 0.5, v40
	v_mul_f32_e32 v41, 0.5, v41
	v_mul_f32_e32 v42, 0.5, v42
	v_mul_f32_e32 v43, 0.5, v43
	v_mul_f32_e32 v36, v40, v36
	v_mul_f32_e32 v37, v41, v37
	v_mul_f32_e32 v38, v42, v38
	v_mul_f32_e32 v39, v43, v39
	v_mul_f32_e32 v24, v24, v36
	v_mul_f32_e32 v25, v25, v37
	v_mul_f32_e32 v26, v26, v38
	v_mul_f32_e32 v27, v27, v39
	v_cvt_pk_bf16_f32 v28, v24, v25
	v_cvt_pk_bf16_f32 v29, v26, v27
	global_store_dwordx2 v23, v[28:29], s[2:3]
	v_add_u32_e32 v23, 0x1000, v23
	s_waitcnt vmcnt(29)
; __device__ __forceinline__ unsigned pk2(float lo, float hi) { return f2bf(lo) | (f2bf(hi) << 16); }
; __device__ __forceinline__ float gelu_tanh_(float x) { const float u = 0.7978845608028654f * (x + 0.044715f * x * x * x); const float t = 1.f - 2.f / (1.f + __expf(2.f * u)); return 0.5f * x * (1.f + t); }
; __device__ __forceinline__ void phase_attn(const Args& a, const Ctx& c0, int l, bool last) {
;     ...
;         for (int r = 0; r < 32; ++r) {
;             const u32x4 wf = *(const u32x4*)(hf + (size_t)r * 4096), wb = *(const u32x4*)(hb + (size_t)r * 4096); const u32x2 gw2 = *(const u32x2*)(zg + (size_t)r * RW); const f32x4 gr = {bflo(gw2.x), bfhi(gw2.x), bflo(gw2.y), bfhi(gw2.y)};
;             const float h0 = fmaf(bflo(wf.z), cf.x, bflo(wf.x)) + fmaf(bflo(wb.z), cb.x, bflo(wb.x)), h1 = fmaf(bfhi(wf.z), cf.y, bfhi(wf.x)) + fmaf(bfhi(wb.z), cb.y, bfhi(wb.x));
;             const float h2 = fmaf(bflo(wf.w), cf.z, bflo(wf.y)) + fmaf(bflo(wb.w), cb.z, bflo(wb.y)), h3 = fmaf(bfhi(wf.w), cf.w, bfhi(wf.y)) + fmaf(bfhi(wb.w), cb.w, bfhi(wb.y));
;             u32x2 w; w.x = pk2(h0 * gelu_tanh_(gr.x), h1 * gelu_tanh_(gr.y)); w.y = pk2(h2 * gelu_tanh_(gr.z), h3 * gelu_tanh_(gr.w));
;             *(u32x2*)(yo + (size_t)r * DM) = w; }
	v_lshlrev_b32_e32 v24, 16, v96
	v_and_b32_e32 v25, 0xffff0000, v96
	v_lshlrev_b32_e32 v26, 16, v97
	v_and_b32_e32 v27, 0xffff0000, v97
	v_lshlrev_b32_e32 v28, 16, v98
	v_and_b32_e32 v29, 0xffff0000, v98
	v_lshlrev_b32_e32 v30, 16, v99
	v_and_b32_e32 v31, 0xffff0000, v99
	v_lshlrev_b32_e32 v32, 16, v100
	v_and_b32_e32 v33, 0xffff0000, v100
	v_lshlrev_b32_e32 v34, 16, v101
	v_and_b32_e32 v35, 0xffff0000, v101
	v_lshlrev_b32_e32 v36, 16, v102
	v_and_b32_e32 v37, 0xffff0000, v102
	v_lshlrev_b32_e32 v38, 16, v103
	v_and_b32_e32 v39, 0xffff0000, v103
	v_fma_f32 v24, v28, v2, v24
	v_fma_f32 v25, v29, v16, v25
	v_fma_f32 v26, v30, v3, v26
	v_fma_f32 v27, v31, v17, v27
	v_fma_f32 v32, v36, v6, v32
	v_fma_f32 v33, v37, v18, v33
	v_fma_f32 v34, v38, v7, v34
	v_fma_f32 v35, v39, v19, v35
	v_add_f32_e32 v24, v24, v32
	v_add_f32_e32 v25, v25, v33
	v_add_f32_e32 v26, v26, v34
	v_add_f32_e32 v27, v27, v35
	v_lshlrev_b32_e32 v40, 16, v104
	v_and_b32_e32 v41, 0xffff0000, v104
	v_lshlrev_b32_e32 v42, 16, v105
	v_and_b32_e32 v43, 0xffff0000, v105
	global_load_dwordx4 v[96:99], v20, s[2:3]
	global_load_dwordx4 v[100:103], v21, s[2:3]
	global_load_dwordx2 v[104:105], v22, s[2:3]
	v_add_u32_e32 v20, 0x1000, v20
	v_add_u32_e32 v21, 0x1000, v21
	v_add_u32_e32 v22, 0x800, v22
	v_mul_f32_e32 v32, 0x3d372713, v40
	v_mul_f32_e32 v33, 0x3d372713, v41
	v_mul_f32_e32 v34, 0x3d372713, v42
	v_mul_f32_e32 v35, 0x3d372713, v43
	v_mul_f32_e32 v32, v32, v40
	v_mul_f32_e32 v33, v33, v41
	v_mul_f32_e32 v34, v34, v42
	v_mul_f32_e32 v35, v35, v43
	v_mov_b32_e32 v36, v40
	v_mov_b32_e32 v37, v41
	v_mov_b32_e32 v38, v42
	v_mov_b32_e32 v39, v43
	v_fmac_f32_e32 v36, v32, v36
	v_fmac_f32_e32 v37, v33, v37
	v_fmac_f32_e32 v38, v34, v38
	v_fmac_f32_e32 v39, v35, v39
	v_mul_f32_e32 v36, 0x3f4c422a, v36
	v_mul_f32_e32 v37, 0x3f4c422a, v37
	v_mul_f32_e32 v38, 0x3f4c422a, v38
	v_mul_f32_e32 v39, 0x3f4c422a, v39
	v_add_f32_e32 v36, v36, v36
	v_add_f32_e32 v37, v37, v37
	v_add_f32_e32 v38, v38, v38
	v_add_f32_e32 v39, v39, v39
	v_mul_f32_e32 v36, 0x3fb8aa3b, v36
	v_mul_f32_e32 v37, 0x3fb8aa3b, v37
	v_mul_f32_e32 v38, 0x3fb8aa3b, v38
	v_mul_f32_e32 v39, 0x3fb8aa3b, v39
	v_exp_f32_e32 v36, v36
	v_exp_f32_e32 v37, v37
	v_exp_f32_e32 v38, v38
	v_exp_f32_e32 v39, v39
	v_add_f32_e32 v36, 1.0, v36
	v_add_f32_e32 v37, 1.0, v37
	v_add_f32_e32 v38, 1.0, v38
	v_add_f32_e32 v39, 1.0, v39
	v_div_scale_f32 v44, s[6:7], v36, v36, 2.0
	v_rcp_f32_e32 v46, v44
	v_div_scale_f32 v45, vcc, 2.0, v36, 2.0
	v_fma_f32 v32, -v44, v46, 1.0
	v_fmac_f32_e32 v46, v32, v46
	v_mul_f32_e32 v47, v45, v46
	v_fma_f32 v32, -v44, v47, v45
	v_fmac_f32_e32 v47, v32, v46
	v_fma_f32 v44, -v44, v47, v45
	v_div_fmas_f32 v44, v44, v46, v47
	v_div_fixup_f32 v36, v44, v36, 2.0
	v_div_scale_f32 v44, s[6:7], v37, v37, 2.0
	v_rcp_f32_e32 v46, v44
	v_div_scale_f32 v45, vcc, 2.0, v37, 2.0
	v_fma_f32 v33, -v44, v46, 1.0
	v_fmac_f32_e32 v46, v33, v46
	v_mul_f32_e32 v47, v45, v46
	v_fma_f32 v33, -v44, v47, v45
	v_fmac_f32_e32 v47, v33, v46
	v_fma_f32 v44, -v44, v47, v45
	v_div_fmas_f32 v44, v44, v46, v47
	v_div_fixup_f32 v37, v44, v37, 2.0
	v_div_scale_f32 v44, s[6:7], v38, v38, 2.0
	v_rcp_f32_e32 v46, v44
	v_div_scale_f32 v45, vcc, 2.0, v38, 2.0
	v_fma_f32 v34, -v44, v46, 1.0
	v_fmac_f32_e32 v46, v34, v46
	v_mul_f32_e32 v47, v45, v46
	v_fma_f32 v34, -v44, v47, v45
	v_fmac_f32_e32 v47, v34, v46
	v_fma_f32 v44, -v44, v47, v45
	v_div_fmas_f32 v44, v44, v46, v47
	v_div_fixup_f32 v38, v44, v38, 2.0
	v_div_scale_f32 v44, s[6:7], v39, v39, 2.0
	v_rcp_f32_e32 v46, v44
	v_div_scale_f32 v45, vcc, 2.0, v39, 2.0
	v_fma_f32 v35, -v44, v46, 1.0
	v_fmac_f32_e32 v46, v35, v46
	v_mul_f32_e32 v47, v45, v46
	v_fma_f32 v35, -v44, v47, v45
	v_fmac_f32_e32 v47, v35, v46
	v_fma_f32 v44, -v44, v47, v45
	v_div_fmas_f32 v44, v44, v46, v47
	v_div_fixup_f32 v39, v44, v39, 2.0
	v_sub_f32_e32 v36, 1.0, v36
	v_sub_f32_e32 v37, 1.0, v37
	v_sub_f32_e32 v38, 1.0, v38
	v_sub_f32_e32 v39, 1.0, v39
	v_add_f32_e32 v36, 1.0, v36
	v_add_f32_e32 v37, 1.0, v37
	v_add_f32_e32 v38, 1.0, v38
	v_add_f32_e32 v39, 1.0, v39
	v_mul_f32_e32 v40, 0.5, v40
	v_mul_f32_e32 v41, 0.5, v41
	v_mul_f32_e32 v42, 0.5, v42
	v_mul_f32_e32 v43, 0.5, v43
	v_mul_f32_e32 v36, v40, v36
	v_mul_f32_e32 v37, v41, v37
	v_mul_f32_e32 v38, v42, v38
	v_mul_f32_e32 v39, v43, v39
	v_mul_f32_e32 v24, v24, v36
	v_mul_f32_e32 v25, v25, v37
	v_mul_f32_e32 v26, v26, v38
	v_mul_f32_e32 v27, v27, v39
	v_cvt_pk_bf16_f32 v28, v24, v25
	v_cvt_pk_bf16_f32 v29, v26, v27
	global_store_dwordx2 v23, v[28:29], s[2:3]
	v_add_u32_e32 v23, 0x1000, v23
	s_waitcnt vmcnt(29)
; __device__ __forceinline__ unsigned pk2(float lo, float hi) { return f2bf(lo) | (f2bf(hi) << 16); }
; __device__ __forceinline__ float gelu_tanh_(float x) { const float u = 0.7978845608028654f * (x + 0.044715f * x * x * x); const float t = 1.f - 2.f / (1.f + __expf(2.f * u)); return 0.5f * x * (1.f + t); }
; __device__ __forceinline__ void phase_attn(const Args& a, const Ctx& c0, int l, bool last) {
;     ...
;         for (int r = 0; r < 32; ++r) {
;             const u32x4 wf = *(const u32x4*)(hf + (size_t)r * 4096), wb = *(const u32x4*)(hb + (size_t)r * 4096); const u32x2 gw2 = *(const u32x2*)(zg + (size_t)r * RW); const f32x4 gr = {bflo(gw2.x), bfhi(gw2.x), bflo(gw2.y), bfhi(gw2.y)};
;             const float h0 = fmaf(bflo(wf.z), cf.x, bflo(wf.x)) + fmaf(bflo(wb.z), cb.x, bflo(wb.x)), h1 = fmaf(bfhi(wf.z), cf.y, bfhi(wf.x)) + fmaf(bfhi(wb.z), cb.y, bfhi(wb.x));
;             const float h2 = fmaf(bflo(wf.w), cf.z, bflo(wf.y)) + fmaf(bflo(wb.w), cb.z, bflo(wb.y)), h3 = fmaf(bfhi(wf.w), cf.w, bfhi(wf.y)) + fmaf(bfhi(wb.w), cb.w, bfhi(wb.y));
;             u32x2 w; w.x = pk2(h0 * gelu_tanh_(gr.x), h1 * gelu_tanh_(gr.y)); w.y = pk2(h2 * gelu_tanh_(gr.z), h3 * gelu_tanh_(gr.w));
;             *(u32x2*)(yo + (size_t)r * DM) = w; }
	v_lshlrev_b32_e32 v24, 16, v108
	v_and_b32_e32 v25, 0xffff0000, v108
	v_lshlrev_b32_e32 v26, 16, v109
	v_and_b32_e32 v27, 0xffff0000, v109
	v_lshlrev_b32_e32 v28, 16, v110
	v_and_b32_e32 v29, 0xffff0000, v110
	v_lshlrev_b32_e32 v30, 16, v111
	v_and_b32_e32 v31, 0xffff0000, v111
	v_lshlrev_b32_e32 v32, 16, v112
	v_and_b32_e32 v33, 0xffff0000, v112
	v_lshlrev_b32_e32 v34, 16, v113
	v_and_b32_e32 v35, 0xffff0000, v113
	v_lshlrev_b32_e32 v36, 16, v114
	v_and_b32_e32 v37, 0xffff0000, v114
	v_lshlrev_b32_e32 v38, 16, v115
	v_and_b32_e32 v39, 0xffff0000, v115
	v_fma_f32 v24, v28, v2, v24
	v_fma_f32 v25, v29, v16, v25
	v_fma_f32 v26, v30, v3, v26
	v_fma_f32 v27, v31, v17, v27
	v_fma_f32 v32, v36, v6, v32
	v_fma_f32 v33, v37, v18, v33
	v_fma_f32 v34, v38, v7, v34
	v_fma_f32 v35, v39, v19, v35
	v_add_f32_e32 v24, v24, v32
	v_add_f32_e32 v25, v25, v33
	v_add_f32_e32 v26, v26, v34
	v_add_f32_e32 v27, v27, v35
	v_lshlrev_b32_e32 v40, 16, v116
	v_and_b32_e32 v41, 0xffff0000, v116
	v_lshlrev_b32_e32 v42, 16, v117
	v_and_b32_e32 v43, 0xffff0000, v117
	global_load_dwordx4 v[108:111], v20, s[2:3]
	global_load_dwordx4 v[112:115], v21, s[2:3]
	global_load_dwordx2 v[116:117], v22, s[2:3]
	v_add_u32_e32 v20, 0x1000, v20
	v_add_u32_e32 v21, 0x1000, v21
	v_add_u32_e32 v22, 0x800, v22
	v_mul_f32_e32 v32, 0x3d372713, v40
	v_mul_f32_e32 v33, 0x3d372713, v41
	v_mul_f32_e32 v34, 0x3d372713, v42
	v_mul_f32_e32 v35, 0x3d372713, v43
	v_mul_f32_e32 v32, v32, v40
	v_mul_f32_e32 v33, v33, v41
	v_mul_f32_e32 v34, v34, v42
	v_mul_f32_e32 v35, v35, v43
	v_mov_b32_e32 v36, v40
	v_mov_b32_e32 v37, v41
	v_mov_b32_e32 v38, v42
	v_mov_b32_e32 v39, v43
	v_fmac_f32_e32 v36, v32, v36
	v_fmac_f32_e32 v37, v33, v37
	v_fmac_f32_e32 v38, v34, v38
	v_fmac_f32_e32 v39, v35, v39
	v_mul_f32_e32 v36, 0x3f4c422a, v36
	v_mul_f32_e32 v37, 0x3f4c422a, v37
	v_mul_f32_e32 v38, 0x3f4c422a, v38
	v_mul_f32_e32 v39, 0x3f4c422a, v39
	v_add_f32_e32 v36, v36, v36
	v_add_f32_e32 v37, v37, v37
	v_add_f32_e32 v38, v38, v38
	v_add_f32_e32 v39, v39, v39
	v_mul_f32_e32 v36, 0x3fb8aa3b, v36
	v_mul_f32_e32 v37, 0x3fb8aa3b, v37
	v_mul_f32_e32 v38, 0x3fb8aa3b, v38
	v_mul_f32_e32 v39, 0x3fb8aa3b, v39
	v_exp_f32_e32 v36, v36
	v_exp_f32_e32 v37, v37
	v_exp_f32_e32 v38, v38
	v_exp_f32_e32 v39, v39
	v_add_f32_e32 v36, 1.0, v36
	v_add_f32_e32 v37, 1.0, v37
	v_add_f32_e32 v38, 1.0, v38
	v_add_f32_e32 v39, 1.0, v39
	v_div_scale_f32 v44, s[6:7], v36, v36, 2.0
	v_rcp_f32_e32 v46, v44
	v_div_scale_f32 v45, vcc, 2.0, v36, 2.0
	v_fma_f32 v32, -v44, v46, 1.0
	v_fmac_f32_e32 v46, v32, v46
	v_mul_f32_e32 v47, v45, v46
	v_fma_f32 v32, -v44, v47, v45
	v_fmac_f32_e32 v47, v32, v46
	v_fma_f32 v44, -v44, v47, v45
	v_div_fmas_f32 v44, v44, v46, v47
	v_div_fixup_f32 v36, v44, v36, 2.0
	v_div_scale_f32 v44, s[6:7], v37, v37, 2.0
	v_rcp_f32_e32 v46, v44
	v_div_scale_f32 v45, vcc, 2.0, v37, 2.0
	v_fma_f32 v33, -v44, v46, 1.0
	v_fmac_f32_e32 v46, v33, v46
	v_mul_f32_e32 v47, v45, v46
	v_fma_f32 v33, -v44, v47, v45
	v_fmac_f32_e32 v47, v33, v46
	v_fma_f32 v44, -v44, v47, v45
	v_div_fmas_f32 v44, v44, v46, v47
	v_div_fixup_f32 v37, v44, v37, 2.0
	v_div_scale_f32 v44, s[6:7], v38, v38, 2.0
	v_rcp_f32_e32 v46, v44
	v_div_scale_f32 v45, vcc, 2.0, v38, 2.0
	v_fma_f32 v34, -v44, v46, 1.0
	v_fmac_f32_e32 v46, v34, v46
	v_mul_f32_e32 v47, v45, v46
	v_fma_f32 v34, -v44, v47, v45
	v_fmac_f32_e32 v47, v34, v46
	v_fma_f32 v44, -v44, v47, v45
	v_div_fmas_f32 v44, v44, v46, v47
	v_div_fixup_f32 v38, v44, v38, 2.0
	v_div_scale_f32 v44, s[6:7], v39, v39, 2.0
	v_rcp_f32_e32 v46, v44
	v_div_scale_f32 v45, vcc, 2.0, v39, 2.0
	v_fma_f32 v35, -v44, v46, 1.0
	v_fmac_f32_e32 v46, v35, v46
	v_mul_f32_e32 v47, v45, v46
	v_fma_f32 v35, -v44, v47, v45
	v_fmac_f32_e32 v47, v35, v46
	v_fma_f32 v44, -v44, v47, v45
	v_div_fmas_f32 v44, v44, v46, v47
	v_div_fixup_f32 v39, v44, v39, 2.0
	v_sub_f32_e32 v36, 1.0, v36
	v_sub_f32_e32 v37, 1.0, v37
	v_sub_f32_e32 v38, 1.0, v38
	v_sub_f32_e32 v39, 1.0, v39
	v_add_f32_e32 v36, 1.0, v36
	v_add_f32_e32 v37, 1.0, v37
	v_add_f32_e32 v38, 1.0, v38
	v_add_f32_e32 v39, 1.0, v39
	v_mul_f32_e32 v40, 0.5, v40
	v_mul_f32_e32 v41, 0.5, v41
	v_mul_f32_e32 v42, 0.5, v42
	v_mul_f32_e32 v43, 0.5, v43
	v_mul_f32_e32 v36, v40, v36
	v_mul_f32_e32 v37, v41, v37
	v_mul_f32_e32 v38, v42, v38
	v_mul_f32_e32 v39, v43, v39
	v_mul_f32_e32 v24, v24, v36
	v_mul_f32_e32 v25, v25, v37
	v_mul_f32_e32 v26, v26, v38
	v_mul_f32_e32 v27, v27, v39
	v_cvt_pk_bf16_f32 v28, v24, v25
	v_cvt_pk_bf16_f32 v29, v26, v27
	global_store_dwordx2 v23, v[28:29], s[2:3]
	v_add_u32_e32 v23, 0x1000, v23
	s_waitcnt vmcnt(29)
; __device__ __forceinline__ unsigned pk2(float lo, float hi) { return f2bf(lo) | (f2bf(hi) << 16); }
; __device__ __forceinline__ float gelu_tanh_(float x) { const float u = 0.7978845608028654f * (x + 0.044715f * x * x * x); const float t = 1.f - 2.f / (1.f + __expf(2.f * u)); return 0.5f * x * (1.f + t); }
; __device__ __forceinline__ void phase_attn(const Args& a, const Ctx& c0, int l, bool last) {
;     ...
;         for (int r = 0; r < 32; ++r) {
;             const u32x4 wf = *(const u32x4*)(hf + (size_t)r * 4096), wb = *(const u32x4*)(hb + (size_t)r * 4096); const u32x2 gw2 = *(const u32x2*)(zg + (size_t)r * RW); const f32x4 gr = {bflo(gw2.x), bfhi(gw2.x), bflo(gw2.y), bfhi(gw2.y)};
;             const float h0 = fmaf(bflo(wf.z), cf.x, bflo(wf.x)) + fmaf(bflo(wb.z), cb.x, bflo(wb.x)), h1 = fmaf(bfhi(wf.z), cf.y, bfhi(wf.x)) + fmaf(bfhi(wb.z), cb.y, bfhi(wb.x));
;             const float h2 = fmaf(bflo(wf.w), cf.z, bflo(wf.y)) + fmaf(bflo(wb.w), cb.z, bflo(wb.y)), h3 = fmaf(bfhi(wf.w), cf.w, bfhi(wf.y)) + fmaf(bfhi(wb.w), cb.w, bfhi(wb.y));
;             u32x2 w; w.x = pk2(h0 * gelu_tanh_(gr.x), h1 * gelu_tanh_(gr.y)); w.y = pk2(h2 * gelu_tanh_(gr.z), h3 * gelu_tanh_(gr.w));
;             *(u32x2*)(yo + (size_t)r * DM) = w; }
	v_lshlrev_b32_e32 v24, 16, v120
	v_and_b32_e32 v25, 0xffff0000, v120
	v_lshlrev_b32_e32 v26, 16, v121
	v_and_b32_e32 v27, 0xffff0000, v121
	v_lshlrev_b32_e32 v28, 16, v122
	v_and_b32_e32 v29, 0xffff0000, v122
	v_lshlrev_b32_e32 v30, 16, v123
	v_and_b32_e32 v31, 0xffff0000, v123
	v_lshlrev_b32_e32 v32, 16, v124
	v_and_b32_e32 v33, 0xffff0000, v124
	v_lshlrev_b32_e32 v34, 16, v125
	v_and_b32_e32 v35, 0xffff0000, v125
	v_lshlrev_b32_e32 v36, 16, v126
	v_and_b32_e32 v37, 0xffff0000, v126
	v_lshlrev_b32_e32 v38, 16, v127
	v_and_b32_e32 v39, 0xffff0000, v127
	v_fma_f32 v24, v28, v2, v24
	v_fma_f32 v25, v29, v16, v25
	v_fma_f32 v26, v30, v3, v26
	v_fma_f32 v27, v31, v17, v27
	v_fma_f32 v32, v36, v6, v32
	v_fma_f32 v33, v37, v18, v33
	v_fma_f32 v34, v38, v7, v34
	v_fma_f32 v35, v39, v19, v35
	v_add_f32_e32 v24, v24, v32
	v_add_f32_e32 v25, v25, v33
	v_add_f32_e32 v26, v26, v34
	v_add_f32_e32 v27, v27, v35
	v_lshlrev_b32_e32 v40, 16, v128
	v_and_b32_e32 v41, 0xffff0000, v128
	v_lshlrev_b32_e32 v42, 16, v129
	v_and_b32_e32 v43, 0xffff0000, v129
	global_load_dwordx4 v[120:123], v20, s[2:3]
	global_load_dwordx4 v[124:127], v21, s[2:3]
	global_load_dwordx2 v[128:129], v22, s[2:3]
	v_add_u32_e32 v20, 0x1000, v20
	v_add_u32_e32 v21, 0x1000, v21
	v_add_u32_e32 v22, 0x800, v22
	v_mul_f32_e32 v32, 0x3d372713, v40
	v_mul_f32_e32 v33, 0x3d372713, v41
	v_mul_f32_e32 v34, 0x3d372713, v42
	v_mul_f32_e32 v35, 0x3d372713, v43
	v_mul_f32_e32 v32, v32, v40
	v_mul_f32_e32 v33, v33, v41
	v_mul_f32_e32 v34, v34, v42
	v_mul_f32_e32 v35, v35, v43
	v_mov_b32_e32 v36, v40
	v_mov_b32_e32 v37, v41
	v_mov_b32_e32 v38, v42
	v_mov_b32_e32 v39, v43
	v_fmac_f32_e32 v36, v32, v36
	v_fmac_f32_e32 v37, v33, v37
	v_fmac_f32_e32 v38, v34, v38
	v_fmac_f32_e32 v39, v35, v39
	v_mul_f32_e32 v36, 0x3f4c422a, v36
	v_mul_f32_e32 v37, 0x3f4c422a, v37
	v_mul_f32_e32 v38, 0x3f4c422a, v38
	v_mul_f32_e32 v39, 0x3f4c422a, v39
	v_add_f32_e32 v36, v36, v36
	v_add_f32_e32 v37, v37, v37
	v_add_f32_e32 v38, v38, v38
	v_add_f32_e32 v39, v39, v39
	v_mul_f32_e32 v36, 0x3fb8aa3b, v36
	v_mul_f32_e32 v37, 0x3fb8aa3b, v37
	v_mul_f32_e32 v38, 0x3fb8aa3b, v38
	v_mul_f32_e32 v39, 0x3fb8aa3b, v39
	v_exp_f32_e32 v36, v36
	v_exp_f32_e32 v37, v37
	v_exp_f32_e32 v38, v38
	v_exp_f32_e32 v39, v39
	v_add_f32_e32 v36, 1.0, v36
	v_add_f32_e32 v37, 1.0, v37
	v_add_f32_e32 v38, 1.0, v38
	v_add_f32_e32 v39, 1.0, v39
	v_div_scale_f32 v44, s[6:7], v36, v36, 2.0
	v_rcp_f32_e32 v46, v44
	v_div_scale_f32 v45, vcc, 2.0, v36, 2.0
	v_fma_f32 v32, -v44, v46, 1.0
	v_fmac_f32_e32 v46, v32, v46
	v_mul_f32_e32 v47, v45, v46
	v_fma_f32 v32, -v44, v47, v45
	v_fmac_f32_e32 v47, v32, v46
	v_fma_f32 v44, -v44, v47, v45
	v_div_fmas_f32 v44, v44, v46, v47
	v_div_fixup_f32 v36, v44, v36, 2.0
	v_div_scale_f32 v44, s[6:7], v37, v37, 2.0
	v_rcp_f32_e32 v46, v44
	v_div_scale_f32 v45, vcc, 2.0, v37, 2.0
	v_fma_f32 v33, -v44, v46, 1.0
	v_fmac_f32_e32 v46, v33, v46
	v_mul_f32_e32 v47, v45, v46
	v_fma_f32 v33, -v44, v47, v45
	v_fmac_f32_e32 v47, v33, v46
	v_fma_f32 v44, -v44, v47, v45
	v_div_fmas_f32 v44, v44, v46, v47
	v_div_fixup_f32 v37, v44, v37, 2.0
	v_div_scale_f32 v44, s[6:7], v38, v38, 2.0
	v_rcp_f32_e32 v46, v44
	v_div_scale_f32 v45, vcc, 2.0, v38, 2.0
	v_fma_f32 v34, -v44, v46, 1.0
	v_fmac_f32_e32 v46, v34, v46
	v_mul_f32_e32 v47, v45, v46
	v_fma_f32 v34, -v44, v47, v45
	v_fmac_f32_e32 v47, v34, v46
	v_fma_f32 v44, -v44, v47, v45
	v_div_fmas_f32 v44, v44, v46, v47
	v_div_fixup_f32 v38, v44, v38, 2.0
	v_div_scale_f32 v44, s[6:7], v39, v39, 2.0
	v_rcp_f32_e32 v46, v44
	v_div_scale_f32 v45, vcc, 2.0, v39, 2.0
	v_fma_f32 v35, -v44, v46, 1.0
	v_fmac_f32_e32 v46, v35, v46
	v_mul_f32_e32 v47, v45, v46
	v_fma_f32 v35, -v44, v47, v45
	v_fmac_f32_e32 v47, v35, v46
	v_fma_f32 v44, -v44, v47, v45
	v_div_fmas_f32 v44, v44, v46, v47
	v_div_fixup_f32 v39, v44, v39, 2.0
	v_sub_f32_e32 v36, 1.0, v36
	v_sub_f32_e32 v37, 1.0, v37
	v_sub_f32_e32 v38, 1.0, v38
	v_sub_f32_e32 v39, 1.0, v39
	v_add_f32_e32 v36, 1.0, v36
	v_add_f32_e32 v37, 1.0, v37
	v_add_f32_e32 v38, 1.0, v38
	v_add_f32_e32 v39, 1.0, v39
	v_mul_f32_e32 v40, 0.5, v40
	v_mul_f32_e32 v41, 0.5, v41
	v_mul_f32_e32 v42, 0.5, v42
	v_mul_f32_e32 v43, 0.5, v43
	v_mul_f32_e32 v36, v40, v36
	v_mul_f32_e32 v37, v41, v37
	v_mul_f32_e32 v38, v42, v38
	v_mul_f32_e32 v39, v43, v39
	v_mul_f32_e32 v24, v24, v36
	v_mul_f32_e32 v25, v25, v37
	v_mul_f32_e32 v26, v26, v38
	v_mul_f32_e32 v27, v27, v39
	v_cvt_pk_bf16_f32 v28, v24, v25
	v_cvt_pk_bf16_f32 v29, v26, v27
	global_store_dwordx2 v23, v[28:29], s[2:3]
	v_add_u32_e32 v23, 0x1000, v23
	s_waitcnt vmcnt(29)
; __device__ __forceinline__ unsigned pk2(float lo, float hi) { return f2bf(lo) | (f2bf(hi) << 16); }
; __device__ __forceinline__ float gelu_tanh_(float x) { const float u = 0.7978845608028654f * (x + 0.044715f * x * x * x); const float t = 1.f - 2.f / (1.f + __expf(2.f * u)); return 0.5f * x * (1.f + t); }
; __device__ __forceinline__ void phase_attn(const Args& a, const Ctx& c0, int l, bool last) {
;     ...
;         for (int r = 0; r < 32; ++r) {
;             const u32x4 wf = *(const u32x4*)(hf + (size_t)r * 4096), wb = *(const u32x4*)(hb + (size_t)r * 4096); const u32x2 gw2 = *(const u32x2*)(zg + (size_t)r * RW); const f32x4 gr = {bflo(gw2.x), bfhi(gw2.x), bflo(gw2.y), bfhi(gw2.y)};
;             const float h0 = fmaf(bflo(wf.z), cf.x, bflo(wf.x)) + fmaf(bflo(wb.z), cb.x, bflo(wb.x)), h1 = fmaf(bfhi(wf.z), cf.y, bfhi(wf.x)) + fmaf(bfhi(wb.z), cb.y, bfhi(wb.x));
;             const float h2 = fmaf(bflo(wf.w), cf.z, bflo(wf.y)) + fmaf(bflo(wb.w), cb.z, bflo(wb.y)), h3 = fmaf(bfhi(wf.w), cf.w, bfhi(wf.y)) + fmaf(bfhi(wb.w), cb.w, bfhi(wb.y));
;             u32x2 w; w.x = pk2(h0 * gelu_tanh_(gr.x), h1 * gelu_tanh_(gr.y)); w.y = pk2(h2 * gelu_tanh_(gr.z), h3 * gelu_tanh_(gr.w));
;             *(u32x2*)(yo + (size_t)r * DM) = w; }
	v_lshlrev_b32_e32 v24, 16, v132
	v_and_b32_e32 v25, 0xffff0000, v132
	v_lshlrev_b32_e32 v26, 16, v133
	v_and_b32_e32 v27, 0xffff0000, v133
	v_lshlrev_b32_e32 v28, 16, v134
	v_and_b32_e32 v29, 0xffff0000, v134
	v_lshlrev_b32_e32 v30, 16, v135
	v_and_b32_e32 v31, 0xffff0000, v135
	v_lshlrev_b32_e32 v32, 16, v136
	v_and_b32_e32 v33, 0xffff0000, v136
	v_lshlrev_b32_e32 v34, 16, v137
	v_and_b32_e32 v35, 0xffff0000, v137
	v_lshlrev_b32_e32 v36, 16, v138
	v_and_b32_e32 v37, 0xffff0000, v138
	v_lshlrev_b32_e32 v38, 16, v139
	v_and_b32_e32 v39, 0xffff0000, v139
	v_fma_f32 v24, v28, v2, v24
	v_fma_f32 v25, v29, v16, v25
	v_fma_f32 v26, v30, v3, v26
	v_fma_f32 v27, v31, v17, v27
	v_fma_f32 v32, v36, v6, v32
	v_fma_f32 v33, v37, v18, v33
	v_fma_f32 v34, v38, v7, v34
	v_fma_f32 v35, v39, v19, v35
	v_add_f32_e32 v24, v24, v32
	v_add_f32_e32 v25, v25, v33
	v_add_f32_e32 v26, v26, v34
	v_add_f32_e32 v27, v27, v35
	v_lshlrev_b32_e32 v40, 16, v140
	v_and_b32_e32 v41, 0xffff0000, v140
	v_lshlrev_b32_e32 v42, 16, v141
	v_and_b32_e32 v43, 0xffff0000, v141
	global_load_dwordx4 v[132:135], v20, s[2:3]
	global_load_dwordx4 v[136:139], v21, s[2:3]
	global_load_dwordx2 v[140:141], v22, s[2:3]
	v_add_u32_e32 v20, 0x1000, v20
	v_add_u32_e32 v21, 0x1000, v21
	v_add_u32_e32 v22, 0x800, v22
	v_mul_f32_e32 v32, 0x3d372713, v40
	v_mul_f32_e32 v33, 0x3d372713, v41
	v_mul_f32_e32 v34, 0x3d372713, v42
	v_mul_f32_e32 v35, 0x3d372713, v43
	v_mul_f32_e32 v32, v32, v40
	v_mul_f32_e32 v33, v33, v41
	v_mul_f32_e32 v34, v34, v42
	v_mul_f32_e32 v35, v35, v43
	v_mov_b32_e32 v36, v40
	v_mov_b32_e32 v37, v41
	v_mov_b32_e32 v38, v42
	v_mov_b32_e32 v39, v43
	v_fmac_f32_e32 v36, v32, v36
	v_fmac_f32_e32 v37, v33, v37
	v_fmac_f32_e32 v38, v34, v38
	v_fmac_f32_e32 v39, v35, v39
	v_mul_f32_e32 v36, 0x3f4c422a, v36
	v_mul_f32_e32 v37, 0x3f4c422a, v37
	v_mul_f32_e32 v38, 0x3f4c422a, v38
	v_mul_f32_e32 v39, 0x3f4c422a, v39
	v_add_f32_e32 v36, v36, v36
	v_add_f32_e32 v37, v37, v37
	v_add_f32_e32 v38, v38, v38
	v_add_f32_e32 v39, v39, v39
	v_mul_f32_e32 v36, 0x3fb8aa3b, v36
	v_mul_f32_e32 v37, 0x3fb8aa3b, v37
	v_mul_f32_e32 v38, 0x3fb8aa3b, v38
	v_mul_f32_e32 v39, 0x3fb8aa3b, v39
	v_exp_f32_e32 v36, v36
	v_exp_f32_e32 v37, v37
	v_exp_f32_e32 v38, v38
	v_exp_f32_e32 v39, v39
	v_add_f32_e32 v36, 1.0, v36
	v_add_f32_e32 v37, 1.0, v37
	v_add_f32_e32 v38, 1.0, v38
	v_add_f32_e32 v39, 1.0, v39
	v_div_scale_f32 v44, s[6:7], v36, v36, 2.0
	v_rcp_f32_e32 v46, v44
	v_div_scale_f32 v45, vcc, 2.0, v36, 2.0
	v_fma_f32 v32, -v44, v46, 1.0
	v_fmac_f32_e32 v46, v32, v46
	v_mul_f32_e32 v47, v45, v46
	v_fma_f32 v32, -v44, v47, v45
	v_fmac_f32_e32 v47, v32, v46
	v_fma_f32 v44, -v44, v47, v45
	v_div_fmas_f32 v44, v44, v46, v47
	v_div_fixup_f32 v36, v44, v36, 2.0
	v_div_scale_f32 v44, s[6:7], v37, v37, 2.0
	v_rcp_f32_e32 v46, v44
	v_div_scale_f32 v45, vcc, 2.0, v37, 2.0
	v_fma_f32 v33, -v44, v46, 1.0
	v_fmac_f32_e32 v46, v33, v46
	v_mul_f32_e32 v47, v45, v46
	v_fma_f32 v33, -v44, v47, v45
	v_fmac_f32_e32 v47, v33, v46
	v_fma_f32 v44, -v44, v47, v45
	v_div_fmas_f32 v44, v44, v46, v47
	v_div_fixup_f32 v37, v44, v37, 2.0
	v_div_scale_f32 v44, s[6:7], v38, v38, 2.0
	v_rcp_f32_e32 v46, v44
	v_div_scale_f32 v45, vcc, 2.0, v38, 2.0
	v_fma_f32 v34, -v44, v46, 1.0
	v_fmac_f32_e32 v46, v34, v46
	v_mul_f32_e32 v47, v45, v46
	v_fma_f32 v34, -v44, v47, v45
	v_fmac_f32_e32 v47, v34, v46
	v_fma_f32 v44, -v44, v47, v45
	v_div_fmas_f32 v44, v44, v46, v47
	v_div_fixup_f32 v38, v44, v38, 2.0
	v_div_scale_f32 v44, s[6:7], v39, v39, 2.0
	v_rcp_f32_e32 v46, v44
	v_div_scale_f32 v45, vcc, 2.0, v39, 2.0
	v_fma_f32 v35, -v44, v46, 1.0
	v_fmac_f32_e32 v46, v35, v46
	v_mul_f32_e32 v47, v45, v46
	v_fma_f32 v35, -v44, v47, v45
	v_fmac_f32_e32 v47, v35, v46
	v_fma_f32 v44, -v44, v47, v45
	v_div_fmas_f32 v44, v44, v46, v47
	v_div_fixup_f32 v39, v44, v39, 2.0
	v_sub_f32_e32 v36, 1.0, v36
	v_sub_f32_e32 v37, 1.0, v37
	v_sub_f32_e32 v38, 1.0, v38
	v_sub_f32_e32 v39, 1.0, v39
	v_add_f32_e32 v36, 1.0, v36
	v_add_f32_e32 v37, 1.0, v37
	v_add_f32_e32 v38, 1.0, v38
	v_add_f32_e32 v39, 1.0, v39
	v_mul_f32_e32 v40, 0.5, v40
	v_mul_f32_e32 v41, 0.5, v41
	v_mul_f32_e32 v42, 0.5, v42
	v_mul_f32_e32 v43, 0.5, v43
	v_mul_f32_e32 v36, v40, v36
	v_mul_f32_e32 v37, v41, v37
	v_mul_f32_e32 v38, v42, v38
	v_mul_f32_e32 v39, v43, v39
	v_mul_f32_e32 v24, v24, v36
	v_mul_f32_e32 v25, v25, v37
	v_mul_f32_e32 v26, v26, v38
	v_mul_f32_e32 v27, v27, v39
	v_cvt_pk_bf16_f32 v28, v24, v25
	v_cvt_pk_bf16_f32 v29, v26, v27
	global_store_dwordx2 v23, v[28:29], s[2:3]
	v_add_u32_e32 v23, 0x1000, v23
	s_waitcnt vmcnt(29)
; __device__ __forceinline__ unsigned pk2(float lo, float hi) { return f2bf(lo) | (f2bf(hi) << 16); }
; __device__ __forceinline__ float gelu_tanh_(float x) { const float u = 0.7978845608028654f * (x + 0.044715f * x * x * x); const float t = 1.f - 2.f / (1.f + __expf(2.f * u)); return 0.5f * x * (1.f + t); }
; __device__ __forceinline__ void phase_attn(const Args& a, const Ctx& c0, int l, bool last) {
;     ...
;         for (int r = 0; r < 32; ++r) {
;             const u32x4 wf = *(const u32x4*)(hf + (size_t)r * 4096), wb = *(const u32x4*)(hb + (size_t)r * 4096); const u32x2 gw2 = *(const u32x2*)(zg + (size_t)r * RW); const f32x4 gr = {bflo(gw2.x), bfhi(gw2.x), bflo(gw2.y), bfhi(gw2.y)};
;             const float h0 = fmaf(bflo(wf.z), cf.x, bflo(wf.x)) + fmaf(bflo(wb.z), cb.x, bflo(wb.x)), h1 = fmaf(bfhi(wf.z), cf.y, bfhi(wf.x)) + fmaf(bfhi(wb.z), cb.y, bfhi(wb.x));
;             const float h2 = fmaf(bflo(wf.w), cf.z, bflo(wf.y)) + fmaf(bflo(wb.w), cb.z, bflo(wb.y)), h3 = fmaf(bfhi(wf.w), cf.w, bfhi(wf.y)) + fmaf(bfhi(wb.w), cb.w, bfhi(wb.y));
;             u32x2 w; w.x = pk2(h0 * gelu_tanh_(gr.x), h1 * gelu_tanh_(gr.y)); w.y = pk2(h2 * gelu_tanh_(gr.z), h3 * gelu_tanh_(gr.w));
;             *(u32x2*)(yo + (size_t)r * DM) = w; }
	v_lshlrev_b32_e32 v24, 16, v48
	v_and_b32_e32 v25, 0xffff0000, v48
	v_lshlrev_b32_e32 v26, 16, v49
	v_and_b32_e32 v27, 0xffff0000, v49
	v_lshlrev_b32_e32 v28, 16, v50
	v_and_b32_e32 v29, 0xffff0000, v50
	v_lshlrev_b32_e32 v30, 16, v51
	v_and_b32_e32 v31, 0xffff0000, v51
	v_lshlrev_b32_e32 v32, 16, v52
	v_and_b32_e32 v33, 0xffff0000, v52
	v_lshlrev_b32_e32 v34, 16, v53
	v_and_b32_e32 v35, 0xffff0000, v53
	v_lshlrev_b32_e32 v36, 16, v54
	v_and_b32_e32 v37, 0xffff0000, v54
	v_lshlrev_b32_e32 v38, 16, v55
	v_and_b32_e32 v39, 0xffff0000, v55
	v_fma_f32 v24, v28, v2, v24
	v_fma_f32 v25, v29, v16, v25
	v_fma_f32 v26, v30, v3, v26
	v_fma_f32 v27, v31, v17, v27
	v_fma_f32 v32, v36, v6, v32
	v_fma_f32 v33, v37, v18, v33
	v_fma_f32 v34, v38, v7, v34
	v_fma_f32 v35, v39, v19, v35
	v_add_f32_e32 v24, v24, v32
	v_add_f32_e32 v25, v25, v33
	v_add_f32_e32 v26, v26, v34
	v_add_f32_e32 v27, v27, v35
	v_lshlrev_b32_e32 v40, 16, v56
	v_and_b32_e32 v41, 0xffff0000, v56
	v_lshlrev_b32_e32 v42, 16, v57
	v_and_b32_e32 v43, 0xffff0000, v57
	v_mul_f32_e32 v32, 0x3d372713, v40
	v_mul_f32_e32 v33, 0x3d372713, v41
	v_mul_f32_e32 v34, 0x3d372713, v42
	v_mul_f32_e32 v35, 0x3d372713, v43
	v_mul_f32_e32 v32, v32, v40
	v_mul_f32_e32 v33, v33, v41
	v_mul_f32_e32 v34, v34, v42
	v_mul_f32_e32 v35, v35, v43
	v_mov_b32_e32 v36, v40
	v_mov_b32_e32 v37, v41
	v_mov_b32_e32 v38, v42
	v_mov_b32_e32 v39, v43
	v_fmac_f32_e32 v36, v32, v36
	v_fmac_f32_e32 v37, v33, v37
	v_fmac_f32_e32 v38, v34, v38
	v_fmac_f32_e32 v39, v35, v39
	v_mul_f32_e32 v36, 0x3f4c422a, v36
	v_mul_f32_e32 v37, 0x3f4c422a, v37
	v_mul_f32_e32 v38, 0x3f4c422a, v38
	v_mul_f32_e32 v39, 0x3f4c422a, v39
	v_add_f32_e32 v36, v36, v36
	v_add_f32_e32 v37, v37, v37
	v_add_f32_e32 v38, v38, v38
	v_add_f32_e32 v39, v39, v39
	v_mul_f32_e32 v36, 0x3fb8aa3b, v36
	v_mul_f32_e32 v37, 0x3fb8aa3b, v37
	v_mul_f32_e32 v38, 0x3fb8aa3b, v38
	v_mul_f32_e32 v39, 0x3fb8aa3b, v39
	v_exp_f32_e32 v36, v36
	v_exp_f32_e32 v37, v37
	v_exp_f32_e32 v38, v38
	v_exp_f32_e32 v39, v39
	v_add_f32_e32 v36, 1.0, v36
	v_add_f32_e32 v37, 1.0, v37
	v_add_f32_e32 v38, 1.0, v38
	v_add_f32_e32 v39, 1.0, v39
	v_div_scale_f32 v44, s[6:7], v36, v36, 2.0
	v_rcp_f32_e32 v46, v44
	v_div_scale_f32 v45, vcc, 2.0, v36, 2.0
	v_fma_f32 v32, -v44, v46, 1.0
	v_fmac_f32_e32 v46, v32, v46
	v_mul_f32_e32 v47, v45, v46
	v_fma_f32 v32, -v44, v47, v45
	v_fmac_f32_e32 v47, v32, v46
	v_fma_f32 v44, -v44, v47, v45
	v_div_fmas_f32 v44, v44, v46, v47
	v_div_fixup_f32 v36, v44, v36, 2.0
	v_div_scale_f32 v44, s[6:7], v37, v37, 2.0
	v_rcp_f32_e32 v46, v44
	v_div_scale_f32 v45, vcc, 2.0, v37, 2.0
	v_fma_f32 v33, -v44, v46, 1.0
	v_fmac_f32_e32 v46, v33, v46
	v_mul_f32_e32 v47, v45, v46
	v_fma_f32 v33, -v44, v47, v45
	v_fmac_f32_e32 v47, v33, v46
	v_fma_f32 v44, -v44, v47, v45
	v_div_fmas_f32 v44, v44, v46, v47
	v_div_fixup_f32 v37, v44, v37, 2.0
	v_div_scale_f32 v44, s[6:7], v38, v38, 2.0
	v_rcp_f32_e32 v46, v44
	v_div_scale_f32 v45, vcc, 2.0, v38, 2.0
	v_fma_f32 v34, -v44, v46, 1.0
	v_fmac_f32_e32 v46, v34, v46
	v_mul_f32_e32 v47, v45, v46
	v_fma_f32 v34, -v44, v47, v45
	v_fmac_f32_e32 v47, v34, v46
	v_fma_f32 v44, -v44, v47, v45
	v_div_fmas_f32 v44, v44, v46, v47
	v_div_fixup_f32 v38, v44, v38, 2.0
	v_div_scale_f32 v44, s[6:7], v39, v39, 2.0
	v_rcp_f32_e32 v46, v44
	v_div_scale_f32 v45, vcc, 2.0, v39, 2.0
	v_fma_f32 v35, -v44, v46, 1.0
	v_fmac_f32_e32 v46, v35, v46
	v_mul_f32_e32 v47, v45, v46
	v_fma_f32 v35, -v44, v47, v45
	v_fmac_f32_e32 v47, v35, v46
	v_fma_f32 v44, -v44, v47, v45
	v_div_fmas_f32 v44, v44, v46, v47
	v_div_fixup_f32 v39, v44, v39, 2.0
	v_sub_f32_e32 v36, 1.0, v36
	v_sub_f32_e32 v37, 1.0, v37
	v_sub_f32_e32 v38, 1.0, v38
	v_sub_f32_e32 v39, 1.0, v39
	v_add_f32_e32 v36, 1.0, v36
	v_add_f32_e32 v37, 1.0, v37
	v_add_f32_e32 v38, 1.0, v38
	v_add_f32_e32 v39, 1.0, v39
	v_mul_f32_e32 v40, 0.5, v40
	v_mul_f32_e32 v41, 0.5, v41
	v_mul_f32_e32 v42, 0.5, v42
	v_mul_f32_e32 v43, 0.5, v43
	v_mul_f32_e32 v36, v40, v36
	v_mul_f32_e32 v37, v41, v37
	v_mul_f32_e32 v38, v42, v38
	v_mul_f32_e32 v39, v43, v39
	v_mul_f32_e32 v24, v24, v36
	v_mul_f32_e32 v25, v25, v37
	v_mul_f32_e32 v26, v26, v38
	v_mul_f32_e32 v27, v27, v39
	v_cvt_pk_bf16_f32 v28, v24, v25
	v_cvt_pk_bf16_f32 v29, v26, v27
	global_store_dwordx2 v23, v[28:29], s[2:3]
	v_add_u32_e32 v23, 0x1000, v23
	s_waitcnt vmcnt(26)
; __device__ __forceinline__ unsigned pk2(float lo, float hi) { return f2bf(lo) | (f2bf(hi) << 16); }
; __device__ __forceinline__ float gelu_tanh_(float x) { const float u = 0.7978845608028654f * (x + 0.044715f * x * x * x); const float t = 1.f - 2.f / (1.f + __expf(2.f * u)); return 0.5f * x * (1.f + t); }
; __device__ __forceinline__ void phase_attn(const Args& a, const Ctx& c0, int l, bool last) {
;     ...
;         for (int r = 0; r < 32; ++r) {
;             const u32x4 wf = *(const u32x4*)(hf + (size_t)r * 4096), wb = *(const u32x4*)(hb + (size_t)r * 4096); const u32x2 gw2 = *(const u32x2*)(zg + (size_t)r * RW); const f32x4 gr = {bflo(gw2.x), bfhi(gw2.x), bflo(gw2.y), bfhi(gw2.y)};
;             const float h0 = fmaf(bflo(wf.z), cf.x, bflo(wf.x)) + fmaf(bflo(wb.z), cb.x, bflo(wb.x)), h1 = fmaf(bfhi(wf.z), cf.y, bfhi(wf.x)) + fmaf(bfhi(wb.z), cb.y, bfhi(wb.x));
;             const float h2 = fmaf(bflo(wf.w), cf.z, bflo(wf.y)) + fmaf(bflo(wb.w), cb.z, bflo(wb.y)), h3 = fmaf(bfhi(wf.w), cf.w, bfhi(wf.y)) + fmaf(bfhi(wb.w), cb.w, bfhi(wb.y));
;             u32x2 w; w.x = pk2(h0 * gelu_tanh_(gr.x), h1 * gelu_tanh_(gr.y)); w.y = pk2(h2 * gelu_tanh_(gr.z), h3 * gelu_tanh_(gr.w));
;             *(u32x2*)(yo + (size_t)r * DM) = w; }
	v_lshlrev_b32_e32 v24, 16, v60
	v_and_b32_e32 v25, 0xffff0000, v60
	v_lshlrev_b32_e32 v26, 16, v61
	v_and_b32_e32 v27, 0xffff0000, v61
	v_lshlrev_b32_e32 v28, 16, v62
	v_and_b32_e32 v29, 0xffff0000, v62
	v_lshlrev_b32_e32 v30, 16, v63
	v_and_b32_e32 v31, 0xffff0000, v63
	v_lshlrev_b32_e32 v32, 16, v64
	v_and_b32_e32 v33, 0xffff0000, v64
	v_lshlrev_b32_e32 v34, 16, v65
	v_and_b32_e32 v35, 0xffff0000, v65
	v_lshlrev_b32_e32 v36, 16, v66
	v_and_b32_e32 v37, 0xffff0000, v66
	v_lshlrev_b32_e32 v38, 16, v67
	v_and_b32_e32 v39, 0xffff0000, v67
	v_fma_f32 v24, v28, v2, v24
	v_fma_f32 v25, v29, v16, v25
	v_fma_f32 v26, v30, v3, v26
	v_fma_f32 v27, v31, v17, v27
	v_fma_f32 v32, v36, v6, v32
	v_fma_f32 v33, v37, v18, v33
	v_fma_f32 v34, v38, v7, v34
	v_fma_f32 v35, v39, v19, v35
	v_add_f32_e32 v24, v24, v32
	v_add_f32_e32 v25, v25, v33
	v_add_f32_e32 v26, v26, v34
	v_add_f32_e32 v27, v27, v35
	v_lshlrev_b32_e32 v40, 16, v68
	v_and_b32_e32 v41, 0xffff0000, v68
	v_lshlrev_b32_e32 v42, 16, v69
	v_and_b32_e32 v43, 0xffff0000, v69
	v_mul_f32_e32 v32, 0x3d372713, v40
	v_mul_f32_e32 v33, 0x3d372713, v41
	v_mul_f32_e32 v34, 0x3d372713, v42
	v_mul_f32_e32 v35, 0x3d372713, v43
	v_mul_f32_e32 v32, v32, v40
	v_mul_f32_e32 v33, v33, v41
	v_mul_f32_e32 v34, v34, v42
	v_mul_f32_e32 v35, v35, v43
	v_mov_b32_e32 v36, v40
	v_mov_b32_e32 v37, v41
	v_mov_b32_e32 v38, v42
	v_mov_b32_e32 v39, v43
	v_fmac_f32_e32 v36, v32, v36
	v_fmac_f32_e32 v37, v33, v37
	v_fmac_f32_e32 v38, v34, v38
	v_fmac_f32_e32 v39, v35, v39
	v_mul_f32_e32 v36, 0x3f4c422a, v36
	v_mul_f32_e32 v37, 0x3f4c422a, v37
	v_mul_f32_e32 v38, 0x3f4c422a, v38
	v_mul_f32_e32 v39, 0x3f4c422a, v39
	v_add_f32_e32 v36, v36, v36
	v_add_f32_e32 v37, v37, v37
	v_add_f32_e32 v38, v38, v38
	v_add_f32_e32 v39, v39, v39
	v_mul_f32_e32 v36, 0x3fb8aa3b, v36
	v_mul_f32_e32 v37, 0x3fb8aa3b, v37
	v_mul_f32_e32 v38, 0x3fb8aa3b, v38
	v_mul_f32_e32 v39, 0x3fb8aa3b, v39
	v_exp_f32_e32 v36, v36
	v_exp_f32_e32 v37, v37
	v_exp_f32_e32 v38, v38
	v_exp_f32_e32 v39, v39
	v_add_f32_e32 v36, 1.0, v36
	v_add_f32_e32 v37, 1.0, v37
	v_add_f32_e32 v38, 1.0, v38
	v_add_f32_e32 v39, 1.0, v39
	v_div_scale_f32 v44, s[6:7], v36, v36, 2.0
	v_rcp_f32_e32 v46, v44
	v_div_scale_f32 v45, vcc, 2.0, v36, 2.0
	v_fma_f32 v32, -v44, v46, 1.0
	v_fmac_f32_e32 v46, v32, v46
	v_mul_f32_e32 v47, v45, v46
	v_fma_f32 v32, -v44, v47, v45
	v_fmac_f32_e32 v47, v32, v46
	v_fma_f32 v44, -v44, v47, v45
	v_div_fmas_f32 v44, v44, v46, v47
	v_div_fixup_f32 v36, v44, v36, 2.0
	v_div_scale_f32 v44, s[6:7], v37, v37, 2.0
	v_rcp_f32_e32 v46, v44
	v_div_scale_f32 v45, vcc, 2.0, v37, 2.0
	v_fma_f32 v33, -v44, v46, 1.0
	v_fmac_f32_e32 v46, v33, v46
	v_mul_f32_e32 v47, v45, v46
	v_fma_f32 v33, -v44, v47, v45
	v_fmac_f32_e32 v47, v33, v46
	v_fma_f32 v44, -v44, v47, v45
	v_div_fmas_f32 v44, v44, v46, v47
	v_div_fixup_f32 v37, v44, v37, 2.0
	v_div_scale_f32 v44, s[6:7], v38, v38, 2.0
	v_rcp_f32_e32 v46, v44
	v_div_scale_f32 v45, vcc, 2.0, v38, 2.0
	v_fma_f32 v34, -v44, v46, 1.0
	v_fmac_f32_e32 v46, v34, v46
	v_mul_f32_e32 v47, v45, v46
	v_fma_f32 v34, -v44, v47, v45
	v_fmac_f32_e32 v47, v34, v46
	v_fma_f32 v44, -v44, v47, v45
	v_div_fmas_f32 v44, v44, v46, v47
	v_div_fixup_f32 v38, v44, v38, 2.0
	v_div_scale_f32 v44, s[6:7], v39, v39, 2.0
	v_rcp_f32_e32 v46, v44
	v_div_scale_f32 v45, vcc, 2.0, v39, 2.0
	v_fma_f32 v35, -v44, v46, 1.0
	v_fmac_f32_e32 v46, v35, v46
	v_mul_f32_e32 v47, v45, v46
	v_fma_f32 v35, -v44, v47, v45
	v_fmac_f32_e32 v47, v35, v46
	v_fma_f32 v44, -v44, v47, v45
	v_div_fmas_f32 v44, v44, v46, v47
	v_div_fixup_f32 v39, v44, v39, 2.0
	v_sub_f32_e32 v36, 1.0, v36
	v_sub_f32_e32 v37, 1.0, v37
	v_sub_f32_e32 v38, 1.0, v38
	v_sub_f32_e32 v39, 1.0, v39
	v_add_f32_e32 v36, 1.0, v36
	v_add_f32_e32 v37, 1.0, v37
	v_add_f32_e32 v38, 1.0, v38
	v_add_f32_e32 v39, 1.0, v39
	v_mul_f32_e32 v40, 0.5, v40
	v_mul_f32_e32 v41, 0.5, v41
	v_mul_f32_e32 v42, 0.5, v42
	v_mul_f32_e32 v43, 0.5, v43
	v_mul_f32_e32 v36, v40, v36
	v_mul_f32_e32 v37, v41, v37
	v_mul_f32_e32 v38, v42, v38
	v_mul_f32_e32 v39, v43, v39
	v_mul_f32_e32 v24, v24, v36
	v_mul_f32_e32 v25, v25, v37
	v_mul_f32_e32 v26, v26, v38
	v_mul_f32_e32 v27, v27, v39
	v_cvt_pk_bf16_f32 v28, v24, v25
	v_cvt_pk_bf16_f32 v29, v26, v27
	global_store_dwordx2 v23, v[28:29], s[2:3]
	v_add_u32_e32 v23, 0x1000, v23
	s_waitcnt vmcnt(23)
; __device__ __forceinline__ unsigned pk2(float lo, float hi) { return f2bf(lo) | (f2bf(hi) << 16); }
; __device__ __forceinline__ float gelu_tanh_(float x) { const float u = 0.7978845608028654f * (x + 0.044715f * x * x * x); const float t = 1.f - 2.f / (1.f + __expf(2.f * u)); return 0.5f * x * (1.f + t); }
; __device__ __forceinline__ void phase_attn(const Args& a, const Ctx& c0, int l, bool last) {
;     ...
;         for (int r = 0; r < 32; ++r) {
;             const u32x4 wf = *(const u32x4*)(hf + (size_t)r * 4096), wb = *(const u32x4*)(hb + (size_t)r * 4096); const u32x2 gw2 = *(const u32x2*)(zg + (size_t)r * RW); const f32x4 gr = {bflo(gw2.x), bfhi(gw2.x), bflo(gw2.y), bfhi(gw2.y)};
;             const float h0 = fmaf(bflo(wf.z), cf.x, bflo(wf.x)) + fmaf(bflo(wb.z), cb.x, bflo(wb.x)), h1 = fmaf(bfhi(wf.z), cf.y, bfhi(wf.x)) + fmaf(bfhi(wb.z), cb.y, bfhi(wb.x));
;             const float h2 = fmaf(bflo(wf.w), cf.z, bflo(wf.y)) + fmaf(bflo(wb.w), cb.z, bflo(wb.y)), h3 = fmaf(bfhi(wf.w), cf.w, bfhi(wf.y)) + fmaf(bfhi(wb.w), cb.w, bfhi(wb.y));
;             u32x2 w; w.x = pk2(h0 * gelu_tanh_(gr.x), h1 * gelu_tanh_(gr.y)); w.y = pk2(h2 * gelu_tanh_(gr.z), h3 * gelu_tanh_(gr.w));
;             *(u32x2*)(yo + (size_t)r * DM) = w; }
	v_lshlrev_b32_e32 v24, 16, v72
	v_and_b32_e32 v25, 0xffff0000, v72
	v_lshlrev_b32_e32 v26, 16, v73
	v_and_b32_e32 v27, 0xffff0000, v73
	v_lshlrev_b32_e32 v28, 16, v74
	v_and_b32_e32 v29, 0xffff0000, v74
	v_lshlrev_b32_e32 v30, 16, v75
	v_and_b32_e32 v31, 0xffff0000, v75
	v_lshlrev_b32_e32 v32, 16, v76
	v_and_b32_e32 v33, 0xffff0000, v76
	v_lshlrev_b32_e32 v34, 16, v77
	v_and_b32_e32 v35, 0xffff0000, v77
	v_lshlrev_b32_e32 v36, 16, v78
	v_and_b32_e32 v37, 0xffff0000, v78
	v_lshlrev_b32_e32 v38, 16, v79
	v_and_b32_e32 v39, 0xffff0000, v79
	v_fma_f32 v24, v28, v2, v24
	v_fma_f32 v25, v29, v16, v25
	v_fma_f32 v26, v30, v3, v26
	v_fma_f32 v27, v31, v17, v27
	v_fma_f32 v32, v36, v6, v32
	v_fma_f32 v33, v37, v18, v33
	v_fma_f32 v34, v38, v7, v34
	v_fma_f32 v35, v39, v19, v35
	v_add_f32_e32 v24, v24, v32
	v_add_f32_e32 v25, v25, v33
	v_add_f32_e32 v26, v26, v34
	v_add_f32_e32 v27, v27, v35
	v_lshlrev_b32_e32 v40, 16, v80
	v_and_b32_e32 v41, 0xffff0000, v80
	v_lshlrev_b32_e32 v42, 16, v81
	v_and_b32_e32 v43, 0xffff0000, v81
	v_mul_f32_e32 v32, 0x3d372713, v40
	v_mul_f32_e32 v33, 0x3d372713, v41
	v_mul_f32_e32 v34, 0x3d372713, v42
	v_mul_f32_e32 v35, 0x3d372713, v43
	v_mul_f32_e32 v32, v32, v40
	v_mul_f32_e32 v33, v33, v41
	v_mul_f32_e32 v34, v34, v42
	v_mul_f32_e32 v35, v35, v43
	v_mov_b32_e32 v36, v40
	v_mov_b32_e32 v37, v41
	v_mov_b32_e32 v38, v42
	v_mov_b32_e32 v39, v43
	v_fmac_f32_e32 v36, v32, v36
	v_fmac_f32_e32 v37, v33, v37
	v_fmac_f32_e32 v38, v34, v38
	v_fmac_f32_e32 v39, v35, v39
	v_mul_f32_e32 v36, 0x3f4c422a, v36
	v_mul_f32_e32 v37, 0x3f4c422a, v37
	v_mul_f32_e32 v38, 0x3f4c422a, v38
	v_mul_f32_e32 v39, 0x3f4c422a, v39
	v_add_f32_e32 v36, v36, v36
	v_add_f32_e32 v37, v37, v37
	v_add_f32_e32 v38, v38, v38
	v_add_f32_e32 v39, v39, v39
	v_mul_f32_e32 v36, 0x3fb8aa3b, v36
	v_mul_f32_e32 v37, 0x3fb8aa3b, v37
	v_mul_f32_e32 v38, 0x3fb8aa3b, v38
	v_mul_f32_e32 v39, 0x3fb8aa3b, v39
	v_exp_f32_e32 v36, v36
	v_exp_f32_e32 v37, v37
	v_exp_f32_e32 v38, v38
	v_exp_f32_e32 v39, v39
	v_add_f32_e32 v36, 1.0, v36
	v_add_f32_e32 v37, 1.0, v37
	v_add_f32_e32 v38, 1.0, v38
	v_add_f32_e32 v39, 1.0, v39
	v_div_scale_f32 v44, s[6:7], v36, v36, 2.0
	v_rcp_f32_e32 v46, v44
	v_div_scale_f32 v45, vcc, 2.0, v36, 2.0
	v_fma_f32 v32, -v44, v46, 1.0
	v_fmac_f32_e32 v46, v32, v46
	v_mul_f32_e32 v47, v45, v46
	v_fma_f32 v32, -v44, v47, v45
	v_fmac_f32_e32 v47, v32, v46
	v_fma_f32 v44, -v44, v47, v45
	v_div_fmas_f32 v44, v44, v46, v47
	v_div_fixup_f32 v36, v44, v36, 2.0
	v_div_scale_f32 v44, s[6:7], v37, v37, 2.0
	v_rcp_f32_e32 v46, v44
	v_div_scale_f32 v45, vcc, 2.0, v37, 2.0
	v_fma_f32 v33, -v44, v46, 1.0
	v_fmac_f32_e32 v46, v33, v46
	v_mul_f32_e32 v47, v45, v46
	v_fma_f32 v33, -v44, v47, v45
	v_fmac_f32_e32 v47, v33, v46
	v_fma_f32 v44, -v44, v47, v45
	v_div_fmas_f32 v44, v44, v46, v47
	v_div_fixup_f32 v37, v44, v37, 2.0
	v_div_scale_f32 v44, s[6:7], v38, v38, 2.0
	v_rcp_f32_e32 v46, v44
	v_div_scale_f32 v45, vcc, 2.0, v38, 2.0
	v_fma_f32 v34, -v44, v46, 1.0
	v_fmac_f32_e32 v46, v34, v46
	v_mul_f32_e32 v47, v45, v46
	v_fma_f32 v34, -v44, v47, v45
	v_fmac_f32_e32 v47, v34, v46
	v_fma_f32 v44, -v44, v47, v45
	v_div_fmas_f32 v44, v44, v46, v47
	v_div_fixup_f32 v38, v44, v38, 2.0
	v_div_scale_f32 v44, s[6:7], v39, v39, 2.0
	v_rcp_f32_e32 v46, v44
	v_div_scale_f32 v45, vcc, 2.0, v39, 2.0
	v_fma_f32 v35, -v44, v46, 1.0
	v_fmac_f32_e32 v46, v35, v46
	v_mul_f32_e32 v47, v45, v46
	v_fma_f32 v35, -v44, v47, v45
	v_fmac_f32_e32 v47, v35, v46
	v_fma_f32 v44, -v44, v47, v45
	v_div_fmas_f32 v44, v44, v46, v47
	v_div_fixup_f32 v39, v44, v39, 2.0
	v_sub_f32_e32 v36, 1.0, v36
	v_sub_f32_e32 v37, 1.0, v37
	v_sub_f32_e32 v38, 1.0, v38
	v_sub_f32_e32 v39, 1.0, v39
	v_add_f32_e32 v36, 1.0, v36
	v_add_f32_e32 v37, 1.0, v37
	v_add_f32_e32 v38, 1.0, v38
	v_add_f32_e32 v39, 1.0, v39
	v_mul_f32_e32 v40, 0.5, v40
	v_mul_f32_e32 v41, 0.5, v41
	v_mul_f32_e32 v42, 0.5, v42
	v_mul_f32_e32 v43, 0.5, v43
	v_mul_f32_e32 v36, v40, v36
	v_mul_f32_e32 v37, v41, v37
	v_mul_f32_e32 v38, v42, v38
	v_mul_f32_e32 v39, v43, v39
	v_mul_f32_e32 v24, v24, v36
	v_mul_f32_e32 v25, v25, v37
	v_mul_f32_e32 v26, v26, v38
	v_mul_f32_e32 v27, v27, v39
	v_cvt_pk_bf16_f32 v28, v24, v25
	v_cvt_pk_bf16_f32 v29, v26, v27
	global_store_dwordx2 v23, v[28:29], s[2:3]
	v_add_u32_e32 v23, 0x1000, v23
	s_waitcnt vmcnt(20)
; __device__ __forceinline__ unsigned pk2(float lo, float hi) { return f2bf(lo) | (f2bf(hi) << 16); }
; __device__ __forceinline__ float gelu_tanh_(float x) { const float u = 0.7978845608028654f * (x + 0.044715f * x * x * x); const float t = 1.f - 2.f / (1.f + __expf(2.f * u)); return 0.5f * x * (1.f + t); }
; __device__ __forceinline__ void phase_attn(const Args& a, const Ctx& c0, int l, bool last) {
;     ...
;         for (int r = 0; r < 32; ++r) {
;             const u32x4 wf = *(const u32x4*)(hf + (size_t)r * 4096), wb = *(const u32x4*)(hb + (size_t)r * 4096); const u32x2 gw2 = *(const u32x2*)(zg + (size_t)r * RW); const f32x4 gr = {bflo(gw2.x), bfhi(gw2.x), bflo(gw2.y), bfhi(gw2.y)};
;             const float h0 = fmaf(bflo(wf.z), cf.x, bflo(wf.x)) + fmaf(bflo(wb.z), cb.x, bflo(wb.x)), h1 = fmaf(bfhi(wf.z), cf.y, bfhi(wf.x)) + fmaf(bfhi(wb.z), cb.y, bfhi(wb.x));
;             const float h2 = fmaf(bflo(wf.w), cf.z, bflo(wf.y)) + fmaf(bflo(wb.w), cb.z, bflo(wb.y)), h3 = fmaf(bfhi(wf.w), cf.w, bfhi(wf.y)) + fmaf(bfhi(wb.w), cb.w, bfhi(wb.y));
;             u32x2 w; w.x = pk2(h0 * gelu_tanh_(gr.x), h1 * gelu_tanh_(gr.y)); w.y = pk2(h2 * gelu_tanh_(gr.z), h3 * gelu_tanh_(gr.w));
;             *(u32x2*)(yo + (size_t)r * DM) = w; }
	v_lshlrev_b32_e32 v24, 16, v84
	v_and_b32_e32 v25, 0xffff0000, v84
	v_lshlrev_b32_e32 v26, 16, v85
	v_and_b32_e32 v27, 0xffff0000, v85
	v_lshlrev_b32_e32 v28, 16, v86
	v_and_b32_e32 v29, 0xffff0000, v86
	v_lshlrev_b32_e32 v30, 16, v87
	v_and_b32_e32 v31, 0xffff0000, v87
	v_lshlrev_b32_e32 v32, 16, v88
	v_and_b32_e32 v33, 0xffff0000, v88
	v_lshlrev_b32_e32 v34, 16, v89
	v_and_b32_e32 v35, 0xffff0000, v89
	v_lshlrev_b32_e32 v36, 16, v90
	v_and_b32_e32 v37, 0xffff0000, v90
	v_lshlrev_b32_e32 v38, 16, v91
	v_and_b32_e32 v39, 0xffff0000, v91
	v_fma_f32 v24, v28, v2, v24
	v_fma_f32 v25, v29, v16, v25
	v_fma_f32 v26, v30, v3, v26
	v_fma_f32 v27, v31, v17, v27
	v_fma_f32 v32, v36, v6, v32
	v_fma_f32 v33, v37, v18, v33
	v_fma_f32 v34, v38, v7, v34
	v_fma_f32 v35, v39, v19, v35
	v_add_f32_e32 v24, v24, v32
	v_add_f32_e32 v25, v25, v33
	v_add_f32_e32 v26, v26, v34
	v_add_f32_e32 v27, v27, v35
	v_lshlrev_b32_e32 v40, 16, v92
	v_and_b32_e32 v41, 0xffff0000, v92
	v_lshlrev_b32_e32 v42, 16, v93
	v_and_b32_e32 v43, 0xffff0000, v93
	v_mul_f32_e32 v32, 0x3d372713, v40
	v_mul_f32_e32 v33, 0x3d372713, v41
	v_mul_f32_e32 v34, 0x3d372713, v42
	v_mul_f32_e32 v35, 0x3d372713, v43
	v_mul_f32_e32 v32, v32, v40
	v_mul_f32_e32 v33, v33, v41
	v_mul_f32_e32 v34, v34, v42
	v_mul_f32_e32 v35, v35, v43
	v_mov_b32_e32 v36, v40
	v_mov_b32_e32 v37, v41
	v_mov_b32_e32 v38, v42
	v_mov_b32_e32 v39, v43
	v_fmac_f32_e32 v36, v32, v36
	v_fmac_f32_e32 v37, v33, v37
	v_fmac_f32_e32 v38, v34, v38
	v_fmac_f32_e32 v39, v35, v39
	v_mul_f32_e32 v36, 0x3f4c422a, v36
	v_mul_f32_e32 v37, 0x3f4c422a, v37
	v_mul_f32_e32 v38, 0x3f4c422a, v38
	v_mul_f32_e32 v39, 0x3f4c422a, v39
	v_add_f32_e32 v36, v36, v36
	v_add_f32_e32 v37, v37, v37
	v_add_f32_e32 v38, v38, v38
	v_add_f32_e32 v39, v39, v39
	v_mul_f32_e32 v36, 0x3fb8aa3b, v36
	v_mul_f32_e32 v37, 0x3fb8aa3b, v37
	v_mul_f32_e32 v38, 0x3fb8aa3b, v38
	v_mul_f32_e32 v39, 0x3fb8aa3b, v39
	v_exp_f32_e32 v36, v36
	v_exp_f32_e32 v37, v37
	v_exp_f32_e32 v38, v38
	v_exp_f32_e32 v39, v39
	v_add_f32_e32 v36, 1.0, v36
	v_add_f32_e32 v37, 1.0, v37
	v_add_f32_e32 v38, 1.0, v38
	v_add_f32_e32 v39, 1.0, v39
	v_div_scale_f32 v44, s[6:7], v36, v36, 2.0
	v_rcp_f32_e32 v46, v44
	v_div_scale_f32 v45, vcc, 2.0, v36, 2.0
	v_fma_f32 v32, -v44, v46, 1.0
	v_fmac_f32_e32 v46, v32, v46
	v_mul_f32_e32 v47, v45, v46
	v_fma_f32 v32, -v44, v47, v45
	v_fmac_f32_e32 v47, v32, v46
	v_fma_f32 v44, -v44, v47, v45
	v_div_fmas_f32 v44, v44, v46, v47
	v_div_fixup_f32 v36, v44, v36, 2.0
	v_div_scale_f32 v44, s[6:7], v37, v37, 2.0
	v_rcp_f32_e32 v46, v44
	v_div_scale_f32 v45, vcc, 2.0, v37, 2.0
	v_fma_f32 v33, -v44, v46, 1.0
	v_fmac_f32_e32 v46, v33, v46
	v_mul_f32_e32 v47, v45, v46
	v_fma_f32 v33, -v44, v47, v45
	v_fmac_f32_e32 v47, v33, v46
	v_fma_f32 v44, -v44, v47, v45
	v_div_fmas_f32 v44, v44, v46, v47
	v_div_fixup_f32 v37, v44, v37, 2.0
	v_div_scale_f32 v44, s[6:7], v38, v38, 2.0
	v_rcp_f32_e32 v46, v44
	v_div_scale_f32 v45, vcc, 2.0, v38, 2.0
	v_fma_f32 v34, -v44, v46, 1.0
	v_fmac_f32_e32 v46, v34, v46
	v_mul_f32_e32 v47, v45, v46
	v_fma_f32 v34, -v44, v47, v45
	v_fmac_f32_e32 v47, v34, v46
	v_fma_f32 v44, -v44, v47, v45
	v_div_fmas_f32 v44, v44, v46, v47
	v_div_fixup_f32 v38, v44, v38, 2.0
	v_div_scale_f32 v44, s[6:7], v39, v39, 2.0
	v_rcp_f32_e32 v46, v44
	v_div_scale_f32 v45, vcc, 2.0, v39, 2.0
	v_fma_f32 v35, -v44, v46, 1.0
	v_fmac_f32_e32 v46, v35, v46
	v_mul_f32_e32 v47, v45, v46
	v_fma_f32 v35, -v44, v47, v45
	v_fmac_f32_e32 v47, v35, v46
	v_fma_f32 v44, -v44, v47, v45
	v_div_fmas_f32 v44, v44, v46, v47
	v_div_fixup_f32 v39, v44, v39, 2.0
	v_sub_f32_e32 v36, 1.0, v36
	v_sub_f32_e32 v37, 1.0, v37
	v_sub_f32_e32 v38, 1.0, v38
	v_sub_f32_e32 v39, 1.0, v39
	v_add_f32_e32 v36, 1.0, v36
	v_add_f32_e32 v37, 1.0, v37
	v_add_f32_e32 v38, 1.0, v38
	v_add_f32_e32 v39, 1.0, v39
	v_mul_f32_e32 v40, 0.5, v40
	v_mul_f32_e32 v41, 0.5, v41
	v_mul_f32_e32 v42, 0.5, v42
	v_mul_f32_e32 v43, 0.5, v43
	v_mul_f32_e32 v36, v40, v36
	v_mul_f32_e32 v37, v41, v37
	v_mul_f32_e32 v38, v42, v38
	v_mul_f32_e32 v39, v43, v39
	v_mul_f32_e32 v24, v24, v36
	v_mul_f32_e32 v25, v25, v37
	v_mul_f32_e32 v26, v26, v38
	v_mul_f32_e32 v27, v27, v39
	v_cvt_pk_bf16_f32 v28, v24, v25
	v_cvt_pk_bf16_f32 v29, v26, v27
	global_store_dwordx2 v23, v[28:29], s[2:3]
	v_add_u32_e32 v23, 0x1000, v23
	s_waitcnt vmcnt(17)
; __device__ __forceinline__ unsigned pk2(float lo, float hi) { return f2bf(lo) | (f2bf(hi) << 16); }
; __device__ __forceinline__ float gelu_tanh_(float x) { const float u = 0.7978845608028654f * (x + 0.044715f * x * x * x); const float t = 1.f - 2.f / (1.f + __expf(2.f * u)); return 0.5f * x * (1.f + t); }
; __device__ __forceinline__ void phase_attn(const Args& a, const Ctx& c0, int l, bool last) {
;     ...
;         for (int r = 0; r < 32; ++r) {
;             const u32x4 wf = *(const u32x4*)(hf + (size_t)r * 4096), wb = *(const u32x4*)(hb + (size_t)r * 4096); const u32x2 gw2 = *(const u32x2*)(zg + (size_t)r * RW); const f32x4 gr = {bflo(gw2.x), bfhi(gw2.x), bflo(gw2.y), bfhi(gw2.y)};
;             const float h0 = fmaf(bflo(wf.z), cf.x, bflo(wf.x)) + fmaf(bflo(wb.z), cb.x, bflo(wb.x)), h1 = fmaf(bfhi(wf.z), cf.y, bfhi(wf.x)) + fmaf(bfhi(wb.z), cb.y, bfhi(wb.x));
;             const float h2 = fmaf(bflo(wf.w), cf.z, bflo(wf.y)) + fmaf(bflo(wb.w), cb.z, bflo(wb.y)), h3 = fmaf(bfhi(wf.w), cf.w, bfhi(wf.y)) + fmaf(bfhi(wb.w), cb.w, bfhi(wb.y));
;             u32x2 w; w.x = pk2(h0 * gelu_tanh_(gr.x), h1 * gelu_tanh_(gr.y)); w.y = pk2(h2 * gelu_tanh_(gr.z), h3 * gelu_tanh_(gr.w));
;             *(u32x2*)(yo + (size_t)r * DM) = w; }
	v_lshlrev_b32_e32 v24, 16, v96
	v_and_b32_e32 v25, 0xffff0000, v96
	v_lshlrev_b32_e32 v26, 16, v97
	v_and_b32_e32 v27, 0xffff0000, v97
	v_lshlrev_b32_e32 v28, 16, v98
	v_and_b32_e32 v29, 0xffff0000, v98
	v_lshlrev_b32_e32 v30, 16, v99
	v_and_b32_e32 v31, 0xffff0000, v99
	v_lshlrev_b32_e32 v32, 16, v100
	v_and_b32_e32 v33, 0xffff0000, v100
	v_lshlrev_b32_e32 v34, 16, v101
	v_and_b32_e32 v35, 0xffff0000, v101
	v_lshlrev_b32_e32 v36, 16, v102
	v_and_b32_e32 v37, 0xffff0000, v102
	v_lshlrev_b32_e32 v38, 16, v103
	v_and_b32_e32 v39, 0xffff0000, v103
	v_fma_f32 v24, v28, v2, v24
	v_fma_f32 v25, v29, v16, v25
	v_fma_f32 v26, v30, v3, v26
	v_fma_f32 v27, v31, v17, v27
	v_fma_f32 v32, v36, v6, v32
	v_fma_f32 v33, v37, v18, v33
	v_fma_f32 v34, v38, v7, v34
	v_fma_f32 v35, v39, v19, v35
	v_add_f32_e32 v24, v24, v32
	v_add_f32_e32 v25, v25, v33
	v_add_f32_e32 v26, v26, v34
	v_add_f32_e32 v27, v27, v35
	v_lshlrev_b32_e32 v40, 16, v104
	v_and_b32_e32 v41, 0xffff0000, v104
	v_lshlrev_b32_e32 v42, 16, v105
	v_and_b32_e32 v43, 0xffff0000, v105
	v_mul_f32_e32 v32, 0x3d372713, v40
	v_mul_f32_e32 v33, 0x3d372713, v41
	v_mul_f32_e32 v34, 0x3d372713, v42
	v_mul_f32_e32 v35, 0x3d372713, v43
	v_mul_f32_e32 v32, v32, v40
	v_mul_f32_e32 v33, v33, v41
	v_mul_f32_e32 v34, v34, v42
	v_mul_f32_e32 v35, v35, v43
	v_mov_b32_e32 v36, v40
	v_mov_b32_e32 v37, v41
	v_mov_b32_e32 v38, v42
	v_mov_b32_e32 v39, v43
	v_fmac_f32_e32 v36, v32, v36
	v_fmac_f32_e32 v37, v33, v37
	v_fmac_f32_e32 v38, v34, v38
	v_fmac_f32_e32 v39, v35, v39
	v_mul_f32_e32 v36, 0x3f4c422a, v36
	v_mul_f32_e32 v37, 0x3f4c422a, v37
	v_mul_f32_e32 v38, 0x3f4c422a, v38
	v_mul_f32_e32 v39, 0x3f4c422a, v39
	v_add_f32_e32 v36, v36, v36
	v_add_f32_e32 v37, v37, v37
	v_add_f32_e32 v38, v38, v38
	v_add_f32_e32 v39, v39, v39
	v_mul_f32_e32 v36, 0x3fb8aa3b, v36
	v_mul_f32_e32 v37, 0x3fb8aa3b, v37
	v_mul_f32_e32 v38, 0x3fb8aa3b, v38
	v_mul_f32_e32 v39, 0x3fb8aa3b, v39
	v_exp_f32_e32 v36, v36
	v_exp_f32_e32 v37, v37
	v_exp_f32_e32 v38, v38
	v_exp_f32_e32 v39, v39
	v_add_f32_e32 v36, 1.0, v36
	v_add_f32_e32 v37, 1.0, v37
	v_add_f32_e32 v38, 1.0, v38
	v_add_f32_e32 v39, 1.0, v39
	v_div_scale_f32 v44, s[6:7], v36, v36, 2.0
	v_rcp_f32_e32 v46, v44
	v_div_scale_f32 v45, vcc, 2.0, v36, 2.0
	v_fma_f32 v32, -v44, v46, 1.0
	v_fmac_f32_e32 v46, v32, v46
	v_mul_f32_e32 v47, v45, v46
	v_fma_f32 v32, -v44, v47, v45
	v_fmac_f32_e32 v47, v32, v46
	v_fma_f32 v44, -v44, v47, v45
	v_div_fmas_f32 v44, v44, v46, v47
	v_div_fixup_f32 v36, v44, v36, 2.0
	v_div_scale_f32 v44, s[6:7], v37, v37, 2.0
	v_rcp_f32_e32 v46, v44
	v_div_scale_f32 v45, vcc, 2.0, v37, 2.0
	v_fma_f32 v33, -v44, v46, 1.0
	v_fmac_f32_e32 v46, v33, v46
	v_mul_f32_e32 v47, v45, v46
	v_fma_f32 v33, -v44, v47, v45
	v_fmac_f32_e32 v47, v33, v46
	v_fma_f32 v44, -v44, v47, v45
	v_div_fmas_f32 v44, v44, v46, v47
	v_div_fixup_f32 v37, v44, v37, 2.0
	v_div_scale_f32 v44, s[6:7], v38, v38, 2.0
	v_rcp_f32_e32 v46, v44
	v_div_scale_f32 v45, vcc, 2.0, v38, 2.0
	v_fma_f32 v34, -v44, v46, 1.0
	v_fmac_f32_e32 v46, v34, v46
	v_mul_f32_e32 v47, v45, v46
	v_fma_f32 v34, -v44, v47, v45
	v_fmac_f32_e32 v47, v34, v46
	v_fma_f32 v44, -v44, v47, v45
	v_div_fmas_f32 v44, v44, v46, v47
	v_div_fixup_f32 v38, v44, v38, 2.0
	v_div_scale_f32 v44, s[6:7], v39, v39, 2.0
	v_rcp_f32_e32 v46, v44
	v_div_scale_f32 v45, vcc, 2.0, v39, 2.0
	v_fma_f32 v35, -v44, v46, 1.0
	v_fmac_f32_e32 v46, v35, v46
	v_mul_f32_e32 v47, v45, v46
	v_fma_f32 v35, -v44, v47, v45
	v_fmac_f32_e32 v47, v35, v46
	v_fma_f32 v44, -v44, v47, v45
	v_div_fmas_f32 v44, v44, v46, v47
	v_div_fixup_f32 v39, v44, v39, 2.0
	v_sub_f32_e32 v36, 1.0, v36
	v_sub_f32_e32 v37, 1.0, v37
	v_sub_f32_e32 v38, 1.0, v38
	v_sub_f32_e32 v39, 1.0, v39
	v_add_f32_e32 v36, 1.0, v36
	v_add_f32_e32 v37, 1.0, v37
	v_add_f32_e32 v38, 1.0, v38
	v_add_f32_e32 v39, 1.0, v39
	v_mul_f32_e32 v40, 0.5, v40
	v_mul_f32_e32 v41, 0.5, v41
	v_mul_f32_e32 v42, 0.5, v42
	v_mul_f32_e32 v43, 0.5, v43
	v_mul_f32_e32 v36, v40, v36
	v_mul_f32_e32 v37, v41, v37
	v_mul_f32_e32 v38, v42, v38
	v_mul_f32_e32 v39, v43, v39
	v_mul_f32_e32 v24, v24, v36
	v_mul_f32_e32 v25, v25, v37
	v_mul_f32_e32 v26, v26, v38
	v_mul_f32_e32 v27, v27, v39
	v_cvt_pk_bf16_f32 v28, v24, v25
	v_cvt_pk_bf16_f32 v29, v26, v27
	global_store_dwordx2 v23, v[28:29], s[2:3]
	v_add_u32_e32 v23, 0x1000, v23
	s_waitcnt vmcnt(14)
; __device__ __forceinline__ unsigned pk2(float lo, float hi) { return f2bf(lo) | (f2bf(hi) << 16); }
; __device__ __forceinline__ float gelu_tanh_(float x) { const float u = 0.7978845608028654f * (x + 0.044715f * x * x * x); const float t = 1.f - 2.f / (1.f + __expf(2.f * u)); return 0.5f * x * (1.f + t); }
; __device__ __forceinline__ void phase_attn(const Args& a, const Ctx& c0, int l, bool last) {
;     ...
;         for (int r = 0; r < 32; ++r) {
;             const u32x4 wf = *(const u32x4*)(hf + (size_t)r * 4096), wb = *(const u32x4*)(hb + (size_t)r * 4096); const u32x2 gw2 = *(const u32x2*)(zg + (size_t)r * RW); const f32x4 gr = {bflo(gw2.x), bfhi(gw2.x), bflo(gw2.y), bfhi(gw2.y)};
;             const float h0 = fmaf(bflo(wf.z), cf.x, bflo(wf.x)) + fmaf(bflo(wb.z), cb.x, bflo(wb.x)), h1 = fmaf(bfhi(wf.z), cf.y, bfhi(wf.x)) + fmaf(bfhi(wb.z), cb.y, bfhi(wb.x));
;             const float h2 = fmaf(bflo(wf.w), cf.z, bflo(wf.y)) + fmaf(bflo(wb.w), cb.z, bflo(wb.y)), h3 = fmaf(bfhi(wf.w), cf.w, bfhi(wf.y)) + fmaf(bfhi(wb.w), cb.w, bfhi(wb.y));
;             u32x2 w; w.x = pk2(h0 * gelu_tanh_(gr.x), h1 * gelu_tanh_(gr.y)); w.y = pk2(h2 * gelu_tanh_(gr.z), h3 * gelu_tanh_(gr.w));
;             *(u32x2*)(yo + (size_t)r * DM) = w; }
	v_lshlrev_b32_e32 v24, 16, v108
	v_and_b32_e32 v25, 0xffff0000, v108
	v_lshlrev_b32_e32 v26, 16, v109
	v_and_b32_e32 v27, 0xffff0000, v109
	v_lshlrev_b32_e32 v28, 16, v110
	v_and_b32_e32 v29, 0xffff0000, v110
	v_lshlrev_b32_e32 v30, 16, v111
	v_and_b32_e32 v31, 0xffff0000, v111
	v_lshlrev_b32_e32 v32, 16, v112
	v_and_b32_e32 v33, 0xffff0000, v112
	v_lshlrev_b32_e32 v34, 16, v113
	v_and_b32_e32 v35, 0xffff0000, v113
	v_lshlrev_b32_e32 v36, 16, v114
	v_and_b32_e32 v37, 0xffff0000, v114
	v_lshlrev_b32_e32 v38, 16, v115
	v_and_b32_e32 v39, 0xffff0000, v115
	v_fma_f32 v24, v28, v2, v24
	v_fma_f32 v25, v29, v16, v25
	v_fma_f32 v26, v30, v3, v26
	v_fma_f32 v27, v31, v17, v27
	v_fma_f32 v32, v36, v6, v32
	v_fma_f32 v33, v37, v18, v33
	v_fma_f32 v34, v38, v7, v34
	v_fma_f32 v35, v39, v19, v35
	v_add_f32_e32 v24, v24, v32
	v_add_f32_e32 v25, v25, v33
	v_add_f32_e32 v26, v26, v34
	v_add_f32_e32 v27, v27, v35
	v_lshlrev_b32_e32 v40, 16, v116
	v_and_b32_e32 v41, 0xffff0000, v116
	v_lshlrev_b32_e32 v42, 16, v117
	v_and_b32_e32 v43, 0xffff0000, v117
	v_mul_f32_e32 v32, 0x3d372713, v40
	v_mul_f32_e32 v33, 0x3d372713, v41
	v_mul_f32_e32 v34, 0x3d372713, v42
	v_mul_f32_e32 v35, 0x3d372713, v43
	v_mul_f32_e32 v32, v32, v40
	v_mul_f32_e32 v33, v33, v41
	v_mul_f32_e32 v34, v34, v42
	v_mul_f32_e32 v35, v35, v43
	v_mov_b32_e32 v36, v40
	v_mov_b32_e32 v37, v41
	v_mov_b32_e32 v38, v42
	v_mov_b32_e32 v39, v43
	v_fmac_f32_e32 v36, v32, v36
	v_fmac_f32_e32 v37, v33, v37
	v_fmac_f32_e32 v38, v34, v38
	v_fmac_f32_e32 v39, v35, v39
	v_mul_f32_e32 v36, 0x3f4c422a, v36
	v_mul_f32_e32 v37, 0x3f4c422a, v37
	v_mul_f32_e32 v38, 0x3f4c422a, v38
	v_mul_f32_e32 v39, 0x3f4c422a, v39
	v_add_f32_e32 v36, v36, v36
	v_add_f32_e32 v37, v37, v37
	v_add_f32_e32 v38, v38, v38
	v_add_f32_e32 v39, v39, v39
	v_mul_f32_e32 v36, 0x3fb8aa3b, v36
	v_mul_f32_e32 v37, 0x3fb8aa3b, v37
	v_mul_f32_e32 v38, 0x3fb8aa3b, v38
	v_mul_f32_e32 v39, 0x3fb8aa3b, v39
	v_exp_f32_e32 v36, v36
	v_exp_f32_e32 v37, v37
	v_exp_f32_e32 v38, v38
	v_exp_f32_e32 v39, v39
	v_add_f32_e32 v36, 1.0, v36
	v_add_f32_e32 v37, 1.0, v37
	v_add_f32_e32 v38, 1.0, v38
	v_add_f32_e32 v39, 1.0, v39
	v_div_scale_f32 v44, s[6:7], v36, v36, 2.0
	v_rcp_f32_e32 v46, v44
	v_div_scale_f32 v45, vcc, 2.0, v36, 2.0
	v_fma_f32 v32, -v44, v46, 1.0
	v_fmac_f32_e32 v46, v32, v46
	v_mul_f32_e32 v47, v45, v46
	v_fma_f32 v32, -v44, v47, v45
	v_fmac_f32_e32 v47, v32, v46
	v_fma_f32 v44, -v44, v47, v45
	v_div_fmas_f32 v44, v44, v46, v47
	v_div_fixup_f32 v36, v44, v36, 2.0
	v_div_scale_f32 v44, s[6:7], v37, v37, 2.0
	v_rcp_f32_e32 v46, v44
	v_div_scale_f32 v45, vcc, 2.0, v37, 2.0
	v_fma_f32 v33, -v44, v46, 1.0
	v_fmac_f32_e32 v46, v33, v46
	v_mul_f32_e32 v47, v45, v46
	v_fma_f32 v33, -v44, v47, v45
	v_fmac_f32_e32 v47, v33, v46
	v_fma_f32 v44, -v44, v47, v45
	v_div_fmas_f32 v44, v44, v46, v47
	v_div_fixup_f32 v37, v44, v37, 2.0
	v_div_scale_f32 v44, s[6:7], v38, v38, 2.0
	v_rcp_f32_e32 v46, v44
	v_div_scale_f32 v45, vcc, 2.0, v38, 2.0
	v_fma_f32 v34, -v44, v46, 1.0
	v_fmac_f32_e32 v46, v34, v46
	v_mul_f32_e32 v47, v45, v46
	v_fma_f32 v34, -v44, v47, v45
	v_fmac_f32_e32 v47, v34, v46
	v_fma_f32 v44, -v44, v47, v45
	v_div_fmas_f32 v44, v44, v46, v47
	v_div_fixup_f32 v38, v44, v38, 2.0
	v_div_scale_f32 v44, s[6:7], v39, v39, 2.0
	v_rcp_f32_e32 v46, v44
	v_div_scale_f32 v45, vcc, 2.0, v39, 2.0
	v_fma_f32 v35, -v44, v46, 1.0
	v_fmac_f32_e32 v46, v35, v46
	v_mul_f32_e32 v47, v45, v46
	v_fma_f32 v35, -v44, v47, v45
	v_fmac_f32_e32 v47, v35, v46
	v_fma_f32 v44, -v44, v47, v45
	v_div_fmas_f32 v44, v44, v46, v47
	v_div_fixup_f32 v39, v44, v39, 2.0
	v_sub_f32_e32 v36, 1.0, v36
	v_sub_f32_e32 v37, 1.0, v37
	v_sub_f32_e32 v38, 1.0, v38
	v_sub_f32_e32 v39, 1.0, v39
	v_add_f32_e32 v36, 1.0, v36
	v_add_f32_e32 v37, 1.0, v37
	v_add_f32_e32 v38, 1.0, v38
	v_add_f32_e32 v39, 1.0, v39
	v_mul_f32_e32 v40, 0.5, v40
	v_mul_f32_e32 v41, 0.5, v41
	v_mul_f32_e32 v42, 0.5, v42
	v_mul_f32_e32 v43, 0.5, v43
	v_mul_f32_e32 v36, v40, v36
	v_mul_f32_e32 v37, v41, v37
	v_mul_f32_e32 v38, v42, v38
	v_mul_f32_e32 v39, v43, v39
	v_mul_f32_e32 v24, v24, v36
	v_mul_f32_e32 v25, v25, v37
	v_mul_f32_e32 v26, v26, v38
	v_mul_f32_e32 v27, v27, v39
	v_cvt_pk_bf16_f32 v28, v24, v25
	v_cvt_pk_bf16_f32 v29, v26, v27
	global_store_dwordx2 v23, v[28:29], s[2:3]
	v_add_u32_e32 v23, 0x1000, v23
	s_waitcnt vmcnt(11)
; __device__ __forceinline__ unsigned pk2(float lo, float hi) { return f2bf(lo) | (f2bf(hi) << 16); }
; __device__ __forceinline__ float gelu_tanh_(float x) { const float u = 0.7978845608028654f * (x + 0.044715f * x * x * x); const float t = 1.f - 2.f / (1.f + __expf(2.f * u)); return 0.5f * x * (1.f + t); }
; __device__ __forceinline__ void phase_attn(const Args& a, const Ctx& c0, int l, bool last) {
;     ...
;         for (int r = 0; r < 32; ++r) {
;             const u32x4 wf = *(const u32x4*)(hf + (size_t)r * 4096), wb = *(const u32x4*)(hb + (size_t)r * 4096); const u32x2 gw2 = *(const u32x2*)(zg + (size_t)r * RW); const f32x4 gr = {bflo(gw2.x), bfhi(gw2.x), bflo(gw2.y), bfhi(gw2.y)};
;             const float h0 = fmaf(bflo(wf.z), cf.x, bflo(wf.x)) + fmaf(bflo(wb.z), cb.x, bflo(wb.x)), h1 = fmaf(bfhi(wf.z), cf.y, bfhi(wf.x)) + fmaf(bfhi(wb.z), cb.y, bfhi(wb.x));
;             const float h2 = fmaf(bflo(wf.w), cf.z, bflo(wf.y)) + fmaf(bflo(wb.w), cb.z, bflo(wb.y)), h3 = fmaf(bfhi(wf.w), cf.w, bfhi(wf.y)) + fmaf(bfhi(wb.w), cb.w, bfhi(wb.y));
;             u32x2 w; w.x = pk2(h0 * gelu_tanh_(gr.x), h1 * gelu_tanh_(gr.y)); w.y = pk2(h2 * gelu_tanh_(gr.z), h3 * gelu_tanh_(gr.w));
;             *(u32x2*)(yo + (size_t)r * DM) = w; }
	v_lshlrev_b32_e32 v24, 16, v120
	v_and_b32_e32 v25, 0xffff0000, v120
	v_lshlrev_b32_e32 v26, 16, v121
	v_and_b32_e32 v27, 0xffff0000, v121
	v_lshlrev_b32_e32 v28, 16, v122
	v_and_b32_e32 v29, 0xffff0000, v122
	v_lshlrev_b32_e32 v30, 16, v123
	v_and_b32_e32 v31, 0xffff0000, v123
	v_lshlrev_b32_e32 v32, 16, v124
	v_and_b32_e32 v33, 0xffff0000, v124
	v_lshlrev_b32_e32 v34, 16, v125
	v_and_b32_e32 v35, 0xffff0000, v125
	v_lshlrev_b32_e32 v36, 16, v126
	v_and_b32_e32 v37, 0xffff0000, v126
	v_lshlrev_b32_e32 v38, 16, v127
	v_and_b32_e32 v39, 0xffff0000, v127
	v_fma_f32 v24, v28, v2, v24
	v_fma_f32 v25, v29, v16, v25
	v_fma_f32 v26, v30, v3, v26
	v_fma_f32 v27, v31, v17, v27
	v_fma_f32 v32, v36, v6, v32
	v_fma_f32 v33, v37, v18, v33
	v_fma_f32 v34, v38, v7, v34
	v_fma_f32 v35, v39, v19, v35
	v_add_f32_e32 v24, v24, v32
	v_add_f32_e32 v25, v25, v33
	v_add_f32_e32 v26, v26, v34
	v_add_f32_e32 v27, v27, v35
	v_lshlrev_b32_e32 v40, 16, v128
	v_and_b32_e32 v41, 0xffff0000, v128
	v_lshlrev_b32_e32 v42, 16, v129
	v_and_b32_e32 v43, 0xffff0000, v129
	v_mul_f32_e32 v32, 0x3d372713, v40
	v_mul_f32_e32 v33, 0x3d372713, v41
	v_mul_f32_e32 v34, 0x3d372713, v42
	v_mul_f32_e32 v35, 0x3d372713, v43
	v_mul_f32_e32 v32, v32, v40
	v_mul_f32_e32 v33, v33, v41
	v_mul_f32_e32 v34, v34, v42
	v_mul_f32_e32 v35, v35, v43
	v_mov_b32_e32 v36, v40
	v_mov_b32_e32 v37, v41
	v_mov_b32_e32 v38, v42
	v_mov_b32_e32 v39, v43
	v_fmac_f32_e32 v36, v32, v36
	v_fmac_f32_e32 v37, v33, v37
	v_fmac_f32_e32 v38, v34, v38
	v_fmac_f32_e32 v39, v35, v39
	v_mul_f32_e32 v36, 0x3f4c422a, v36
	v_mul_f32_e32 v37, 0x3f4c422a, v37
	v_mul_f32_e32 v38, 0x3f4c422a, v38
	v_mul_f32_e32 v39, 0x3f4c422a, v39
	v_add_f32_e32 v36, v36, v36
	v_add_f32_e32 v37, v37, v37
	v_add_f32_e32 v38, v38, v38
	v_add_f32_e32 v39, v39, v39
	v_mul_f32_e32 v36, 0x3fb8aa3b, v36
	v_mul_f32_e32 v37, 0x3fb8aa3b, v37
	v_mul_f32_e32 v38, 0x3fb8aa3b, v38
	v_mul_f32_e32 v39, 0x3fb8aa3b, v39
	v_exp_f32_e32 v36, v36
	v_exp_f32_e32 v37, v37
	v_exp_f32_e32 v38, v38
	v_exp_f32_e32 v39, v39
	v_add_f32_e32 v36, 1.0, v36
	v_add_f32_e32 v37, 1.0, v37
	v_add_f32_e32 v38, 1.0, v38
	v_add_f32_e32 v39, 1.0, v39
	v_div_scale_f32 v44, s[6:7], v36, v36, 2.0
	v_rcp_f32_e32 v46, v44
	v_div_scale_f32 v45, vcc, 2.0, v36, 2.0
	v_fma_f32 v32, -v44, v46, 1.0
	v_fmac_f32_e32 v46, v32, v46
	v_mul_f32_e32 v47, v45, v46
	v_fma_f32 v32, -v44, v47, v45
	v_fmac_f32_e32 v47, v32, v46
	v_fma_f32 v44, -v44, v47, v45
	v_div_fmas_f32 v44, v44, v46, v47
	v_div_fixup_f32 v36, v44, v36, 2.0
	v_div_scale_f32 v44, s[6:7], v37, v37, 2.0
	v_rcp_f32_e32 v46, v44
	v_div_scale_f32 v45, vcc, 2.0, v37, 2.0
	v_fma_f32 v33, -v44, v46, 1.0
	v_fmac_f32_e32 v46, v33, v46
	v_mul_f32_e32 v47, v45, v46
	v_fma_f32 v33, -v44, v47, v45
	v_fmac_f32_e32 v47, v33, v46
	v_fma_f32 v44, -v44, v47, v45
	v_div_fmas_f32 v44, v44, v46, v47
	v_div_fixup_f32 v37, v44, v37, 2.0
	v_div_scale_f32 v44, s[6:7], v38, v38, 2.0
	v_rcp_f32_e32 v46, v44
	v_div_scale_f32 v45, vcc, 2.0, v38, 2.0
	v_fma_f32 v34, -v44, v46, 1.0
	v_fmac_f32_e32 v46, v34, v46
	v_mul_f32_e32 v47, v45, v46
	v_fma_f32 v34, -v44, v47, v45
	v_fmac_f32_e32 v47, v34, v46
	v_fma_f32 v44, -v44, v47, v45
	v_div_fmas_f32 v44, v44, v46, v47
	v_div_fixup_f32 v38, v44, v38, 2.0
	v_div_scale_f32 v44, s[6:7], v39, v39, 2.0
	v_rcp_f32_e32 v46, v44
	v_div_scale_f32 v45, vcc, 2.0, v39, 2.0
	v_fma_f32 v35, -v44, v46, 1.0
	v_fmac_f32_e32 v46, v35, v46
	v_mul_f32_e32 v47, v45, v46
	v_fma_f32 v35, -v44, v47, v45
	v_fmac_f32_e32 v47, v35, v46
	v_fma_f32 v44, -v44, v47, v45
	v_div_fmas_f32 v44, v44, v46, v47
	v_div_fixup_f32 v39, v44, v39, 2.0
	v_sub_f32_e32 v36, 1.0, v36
	v_sub_f32_e32 v37, 1.0, v37
	v_sub_f32_e32 v38, 1.0, v38
	v_sub_f32_e32 v39, 1.0, v39
	v_add_f32_e32 v36, 1.0, v36
	v_add_f32_e32 v37, 1.0, v37
	v_add_f32_e32 v38, 1.0, v38
	v_add_f32_e32 v39, 1.0, v39
	v_mul_f32_e32 v40, 0.5, v40
	v_mul_f32_e32 v41, 0.5, v41
	v_mul_f32_e32 v42, 0.5, v42
	v_mul_f32_e32 v43, 0.5, v43
	v_mul_f32_e32 v36, v40, v36
	v_mul_f32_e32 v37, v41, v37
	v_mul_f32_e32 v38, v42, v38
	v_mul_f32_e32 v39, v43, v39
	v_mul_f32_e32 v24, v24, v36
	v_mul_f32_e32 v25, v25, v37
	v_mul_f32_e32 v26, v26, v38
	v_mul_f32_e32 v27, v27, v39
	v_cvt_pk_bf16_f32 v28, v24, v25
	v_cvt_pk_bf16_f32 v29, v26, v27
	global_store_dwordx2 v23, v[28:29], s[2:3]
	v_add_u32_e32 v23, 0x1000, v23
	s_waitcnt vmcnt(8)
; __device__ __forceinline__ unsigned pk2(float lo, float hi) { return f2bf(lo) | (f2bf(hi) << 16); }
; __device__ __forceinline__ float gelu_tanh_(float x) { const float u = 0.7978845608028654f * (x + 0.044715f * x * x * x); const float t = 1.f - 2.f / (1.f + __expf(2.f * u)); return 0.5f * x * (1.f + t); }
; __device__ __forceinline__ void phase_attn(const Args& a, const Ctx& c0, int l, bool last) {
;     ...
;         for (int r = 0; r < 32; ++r) {
;             const u32x4 wf = *(const u32x4*)(hf + (size_t)r * 4096), wb = *(const u32x4*)(hb + (size_t)r * 4096); const u32x2 gw2 = *(const u32x2*)(zg + (size_t)r * RW); const f32x4 gr = {bflo(gw2.x), bfhi(gw2.x), bflo(gw2.y), bfhi(gw2.y)};
;             const float h0 = fmaf(bflo(wf.z), cf.x, bflo(wf.x)) + fmaf(bflo(wb.z), cb.x, bflo(wb.x)), h1 = fmaf(bfhi(wf.z), cf.y, bfhi(wf.x)) + fmaf(bfhi(wb.z), cb.y, bfhi(wb.x));
;             const float h2 = fmaf(bflo(wf.w), cf.z, bflo(wf.y)) + fmaf(bflo(wb.w), cb.z, bflo(wb.y)), h3 = fmaf(bfhi(wf.w), cf.w, bfhi(wf.y)) + fmaf(bfhi(wb.w), cb.w, bfhi(wb.y));
;             u32x2 w; w.x = pk2(h0 * gelu_tanh_(gr.x), h1 * gelu_tanh_(gr.y)); w.y = pk2(h2 * gelu_tanh_(gr.z), h3 * gelu_tanh_(gr.w));
;             *(u32x2*)(yo + (size_t)r * DM) = w; }
	v_lshlrev_b32_e32 v24, 16, v132
	v_and_b32_e32 v25, 0xffff0000, v132
	v_lshlrev_b32_e32 v26, 16, v133
	v_and_b32_e32 v27, 0xffff0000, v133
	v_lshlrev_b32_e32 v28, 16, v134
	v_and_b32_e32 v29, 0xffff0000, v134
	v_lshlrev_b32_e32 v30, 16, v135
	v_and_b32_e32 v31, 0xffff0000, v135
	v_lshlrev_b32_e32 v32, 16, v136
	v_and_b32_e32 v33, 0xffff0000, v136
	v_lshlrev_b32_e32 v34, 16, v137
	v_and_b32_e32 v35, 0xffff0000, v137
	v_lshlrev_b32_e32 v36, 16, v138
	v_and_b32_e32 v37, 0xffff0000, v138
	v_lshlrev_b32_e32 v38, 16, v139
	v_and_b32_e32 v39, 0xffff0000, v139
	v_fma_f32 v24, v28, v2, v24
	v_fma_f32 v25, v29, v16, v25
	v_fma_f32 v26, v30, v3, v26
	v_fma_f32 v27, v31, v17, v27
	v_fma_f32 v32, v36, v6, v32
	v_fma_f32 v33, v37, v18, v33
	v_fma_f32 v34, v38, v7, v34
	v_fma_f32 v35, v39, v19, v35
	v_add_f32_e32 v24, v24, v32
	v_add_f32_e32 v25, v25, v33
	v_add_f32_e32 v26, v26, v34
	v_add_f32_e32 v27, v27, v35
	v_lshlrev_b32_e32 v40, 16, v140
	v_and_b32_e32 v41, 0xffff0000, v140
	v_lshlrev_b32_e32 v42, 16, v141
	v_and_b32_e32 v43, 0xffff0000, v141
	v_mul_f32_e32 v32, 0x3d372713, v40
	v_mul_f32_e32 v33, 0x3d372713, v41
	v_mul_f32_e32 v34, 0x3d372713, v42
	v_mul_f32_e32 v35, 0x3d372713, v43
	v_mul_f32_e32 v32, v32, v40
	v_mul_f32_e32 v33, v33, v41
	v_mul_f32_e32 v34, v34, v42
	v_mul_f32_e32 v35, v35, v43
	v_mov_b32_e32 v36, v40
	v_mov_b32_e32 v37, v41
	v_mov_b32_e32 v38, v42
	v_mov_b32_e32 v39, v43
	v_fmac_f32_e32 v36, v32, v36
	v_fmac_f32_e32 v37, v33, v37
	v_fmac_f32_e32 v38, v34, v38
	v_fmac_f32_e32 v39, v35, v39
	v_mul_f32_e32 v36, 0x3f4c422a, v36
	v_mul_f32_e32 v37, 0x3f4c422a, v37
	v_mul_f32_e32 v38, 0x3f4c422a, v38
	v_mul_f32_e32 v39, 0x3f4c422a, v39
	v_add_f32_e32 v36, v36, v36
	v_add_f32_e32 v37, v37, v37
	v_add_f32_e32 v38, v38, v38
	v_add_f32_e32 v39, v39, v39
	v_mul_f32_e32 v36, 0x3fb8aa3b, v36
	v_mul_f32_e32 v37, 0x3fb8aa3b, v37
	v_mul_f32_e32 v38, 0x3fb8aa3b, v38
	v_mul_f32_e32 v39, 0x3fb8aa3b, v39
	v_exp_f32_e32 v36, v36
	v_exp_f32_e32 v37, v37
	v_exp_f32_e32 v38, v38
	v_exp_f32_e32 v39, v39
	v_add_f32_e32 v36, 1.0, v36
	v_add_f32_e32 v37, 1.0, v37
	v_add_f32_e32 v38, 1.0, v38
	v_add_f32_e32 v39, 1.0, v39
	v_div_scale_f32 v44, s[6:7], v36, v36, 2.0
	v_rcp_f32_e32 v46, v44
	v_div_scale_f32 v45, vcc, 2.0, v36, 2.0
	v_fma_f32 v32, -v44, v46, 1.0
	v_fmac_f32_e32 v46, v32, v46
	v_mul_f32_e32 v47, v45, v46
	v_fma_f32 v32, -v44, v47, v45
	v_fmac_f32_e32 v47, v32, v46
	v_fma_f32 v44, -v44, v47, v45
	v_div_fmas_f32 v44, v44, v46, v47
	v_div_fixup_f32 v36, v44, v36, 2.0
	v_div_scale_f32 v44, s[6:7], v37, v37, 2.0
	v_rcp_f32_e32 v46, v44
	v_div_scale_f32 v45, vcc, 2.0, v37, 2.0
	v_fma_f32 v33, -v44, v46, 1.0
	v_fmac_f32_e32 v46, v33, v46
	v_mul_f32_e32 v47, v45, v46
	v_fma_f32 v33, -v44, v47, v45
	v_fmac_f32_e32 v47, v33, v46
	v_fma_f32 v44, -v44, v47, v45
	v_div_fmas_f32 v44, v44, v46, v47
	v_div_fixup_f32 v37, v44, v37, 2.0
	v_div_scale_f32 v44, s[6:7], v38, v38, 2.0
	v_rcp_f32_e32 v46, v44
	v_div_scale_f32 v45, vcc, 2.0, v38, 2.0
	v_fma_f32 v34, -v44, v46, 1.0
	v_fmac_f32_e32 v46, v34, v46
	v_mul_f32_e32 v47, v45, v46
	v_fma_f32 v34, -v44, v47, v45
	v_fmac_f32_e32 v47, v34, v46
	v_fma_f32 v44, -v44, v47, v45
	v_div_fmas_f32 v44, v44, v46, v47
	v_div_fixup_f32 v38, v44, v38, 2.0
	v_div_scale_f32 v44, s[6:7], v39, v39, 2.0
	v_rcp_f32_e32 v46, v44
	v_div_scale_f32 v45, vcc, 2.0, v39, 2.0
	v_fma_f32 v35, -v44, v46, 1.0
	v_fmac_f32_e32 v46, v35, v46
	v_mul_f32_e32 v47, v45, v46
	v_fma_f32 v35, -v44, v47, v45
	v_fmac_f32_e32 v47, v35, v46
	v_fma_f32 v44, -v44, v47, v45
	v_div_fmas_f32 v44, v44, v46, v47
	v_div_fixup_f32 v39, v44, v39, 2.0
	v_sub_f32_e32 v36, 1.0, v36
	v_sub_f32_e32 v37, 1.0, v37
	v_sub_f32_e32 v38, 1.0, v38
	v_sub_f32_e32 v39, 1.0, v39
	v_add_f32_e32 v36, 1.0, v36
	v_add_f32_e32 v37, 1.0, v37
	v_add_f32_e32 v38, 1.0, v38
	v_add_f32_e32 v39, 1.0, v39
	v_mul_f32_e32 v40, 0.5, v40
	v_mul_f32_e32 v41, 0.5, v41
	v_mul_f32_e32 v42, 0.5, v42
	v_mul_f32_e32 v43, 0.5, v43
	v_mul_f32_e32 v36, v40, v36
	v_mul_f32_e32 v37, v41, v37
	v_mul_f32_e32 v38, v42, v38
	v_mul_f32_e32 v39, v43, v39
	v_mul_f32_e32 v24, v24, v36
	v_mul_f32_e32 v25, v25, v37
	v_mul_f32_e32 v26, v26, v38
	v_mul_f32_e32 v27, v27, v39
	v_cvt_pk_bf16_f32 v28, v24, v25
	v_cvt_pk_bf16_f32 v29, v26, v27
	global_store_dwordx2 v23, v[28:29], s[2:3]
	v_add_u32_e32 v23, 0x1000, v23
	s_branch .LBB0_1485
